# deeper epilogue operand prefetch in pool/merge/out/ple GEMM epilogues (4 row-groups ahead; pool: all up front), counted waits
# speedup vs baseline: 1.0382x; 1.0010x over previous
; template <class Epi, class Sched, bool GATHER, bool ALIGN_EPI = true, bool SP2 = true, bool REMAP64 = false>
; __device__ __forceinline__ void gemm_phase(LAS unsigned char* lds, const bf16* Ag, const bf16* Btg, const int K, const Sched& S, const Epi& E) {
;     ...
;             const bool hi = RP && (fr >= 8); const int rsh = hi ? -8 : 0, citx = hi ? cit + 32 : cit;
;             typename Epi::Pre pq[2];
;             { const int r0_ = wr * 64 + fr; pq[0] = E.pre(cur, (r0_ < cur.nrows ? r0_ : cur.nrows - 1) + rsh, citx); }
; #pragma unroll
;             for (int gq = 0; gq < 8; ++gq) { const int ai = gq >> 2, m = gq & 3, r = ai * HALF + wr * 64 + m * 16 + fr;
;                 if (gq + 1 < 8) { const int rn = ((gq + 1) >> 2) * HALF + wr * 64 + ((gq + 1) & 3) * 16 + fr; pq[(gq + 1) & 1] = E.pre(cur, (rn < cur.nrows ? rn : cur.nrows - 1) + rsh, citx); }
;                 __builtin_amdgcn_sched_barrier(0);
;                 if (r < cur.nrows) { float v0[8], v1[8];
; #pragma unroll
;                     for (int i = 0; i < 4; ++i) { v0[i] = acc[ai][0][m][0][i]; v0[4 + i] = acc[ai][0][m][1][i]; v1[i] = acc[ai][1][m][0][i]; v1[4 + i] = acc[ai][1][m][1][i]; }
;                     if constexpr (RP) {
; #pragma unroll
;                         for (int i = 0; i < 8; ++i) { const float snd = hi ? v0[i] : v1[i];
;                             const float rcv = __builtin_bit_cast(float, __builtin_amdgcn_update_dpp(0, __builtin_bit_cast(int, snd), 0x128, 0xf, 0xf, false));
;                             if (hi) v0[i] = rcv; else v1[i] = rcv; } }
;                     E.post(cur, r + rsh, citx, v0, v1, pq[gq & 1]); }
;                 __builtin_amdgcn_sched_barrier(0); }
;             }
;     __device__ __forceinline__ Pre pre(const Unit& u, int r, int cit) const { const size_t off = (size_t)(u.arow0 + r) * D + u.pn * 256 + cit; return Pre{__builtin_nontemporal_load((const v4u*)(gp + off)), __builtin_nontemporal_load((const v4u*)(gp + off + (size_t)8 * D))}; }
;     __device__ __forceinline__ void post(const Unit& u, int r, int cit, const float* v0, const float* v1, const Pre& p) const {
;         const size_t off = (size_t)(u.arow0 + r) * D + u.pn * 256 + cit; float g0[8], g1[8], a[8], b[8]; unpack8bf(p.g0, g0); unpack8bf(p.g1, g1);
; #pragma unroll
;         for (int i = 0; i < 8; ++i) { a[i] = g0[i] * v0[i]; b[i] = g1[i] * v1[i]; }
.LBB0_950:
	v_add_u32_e32 v130, s10, v176
	v_ashrrev_i32_e32 v131, 31, v130
	s_lshl_b32 s54, s52, 8
	s_ashr_i32 s55, s54, 31
	v_lshlrev_b64 v[130:131], 12, v[130:131]
	v_lshl_add_u64 v[130:131], s[48:49], 0, v[130:131]
	s_lshl_b64 s[54:55], s[54:55], 1
	v_lshl_add_u64 v[130:131], v[130:131], 0, s[54:55]
	v_lshl_add_u64 v[130:131], v[130:131], 0, v[154:155]
	v_add_co_u32_e32 v132, vcc, 0x8000, v130
	v_add_u32_e32 v188, s10, v175
	s_nop 0
	v_addc_co_u32_e32 v133, vcc, 0, v131, vcc
	global_load_dwordx4 v[142:145], v[130:131], off nt
	global_load_dwordx4 v[138:141], v[132:133], off nt
	v_add_u32_e32 v130, v188, v177
	v_ashrrev_i32_e32 v131, 31, v130
	v_lshl_add_u64 v[172:173], v[156:157], 0, s[54:55]
	v_lshlrev_b64 v[130:131], 12, v[130:131]
	v_lshl_add_u64 v[130:131], v[172:173], 0, v[130:131]
	v_add_co_u32_e32 v132, vcc, 0x8000, v130
	v_lshl_add_u64 v[168:169], v[158:159], 0, s[54:55]
	s_nop 0
	v_addc_co_u32_e32 v133, vcc, 0, v131, vcc
	global_load_dwordx4 v[134:137], v[130:131], off nt
	s_nop 0
	global_load_dwordx4 v[130:133], v[132:133], off nt
	v_add_u32_e32 v187, v188, v171
	s_nop 1
	v_add_u32_e32 v198, v188, v178
	v_ashrrev_i32_e32 v199, 31, v198
	v_lshlrev_b64 v[198:199], 12, v[198:199]
	v_lshl_add_u64 v[198:199], v[172:173], 0, v[198:199]
	v_add_co_u32_e32 v200, vcc, 0x8000, v198
	s_nop 1
	v_addc_co_u32_e32 v201, vcc, 0, v199, vcc
	global_load_dwordx4 v[202:205], v[198:199], off nt
	s_nop 0
	global_load_dwordx4 v[198:201], v[200:201], off nt
	s_nop 1
	v_add_u32_e32 v206, v188, v179
	v_ashrrev_i32_e32 v207, 31, v206
	v_lshlrev_b64 v[206:207], 12, v[206:207]
	v_lshl_add_u64 v[206:207], v[172:173], 0, v[206:207]
	v_add_co_u32_e32 v208, vcc, 0x8000, v206
	s_nop 1
	v_addc_co_u32_e32 v209, vcc, 0, v207, vcc
	global_load_dwordx4 v[210:213], v[206:207], off nt
	s_nop 0
	global_load_dwordx4 v[206:209], v[208:209], off nt
	s_nop 1
	v_add_u32_e32 v214, v188, v180
	v_ashrrev_i32_e32 v215, 31, v214
	v_lshlrev_b64 v[214:215], 12, v[214:215]
	v_lshl_add_u64 v[214:215], v[172:173], 0, v[214:215]
	v_add_co_u32_e32 v216, vcc, 0x8000, v214
	s_nop 1
	v_addc_co_u32_e32 v217, vcc, 0, v215, vcc
	global_load_dwordx4 v[218:221], v[214:215], off nt
	s_nop 0
	global_load_dwordx4 v[214:217], v[216:217], off nt
	s_nop 1
	v_add_u32_e32 v222, v188, v181
	v_ashrrev_i32_e32 v223, 31, v222
	v_lshlrev_b64 v[222:223], 12, v[222:223]
	v_lshl_add_u64 v[222:223], v[172:173], 0, v[222:223]
	v_add_co_u32_e32 v224, vcc, 0x8000, v222
	s_nop 1
	v_addc_co_u32_e32 v225, vcc, 0, v223, vcc
	global_load_dwordx4 v[226:229], v[222:223], off nt
	s_nop 0
	global_load_dwordx4 v[222:225], v[224:225], off nt
	s_nop 1
	v_add_u32_e32 v230, v188, v182
	v_ashrrev_i32_e32 v231, 31, v230
	v_lshlrev_b64 v[230:231], 12, v[230:231]
	v_lshl_add_u64 v[230:231], v[172:173], 0, v[230:231]
	v_add_co_u32_e32 v232, vcc, 0x8000, v230
	s_nop 1
	v_addc_co_u32_e32 v233, vcc, 0, v231, vcc
	global_load_dwordx4 v[234:237], v[230:231], off nt
	s_nop 0
	global_load_dwordx4 v[230:233], v[232:233], off nt
	s_nop 1
	v_add_u32_e32 v238, v188, v183
	v_ashrrev_i32_e32 v239, 31, v238
	v_lshlrev_b64 v[238:239], 12, v[238:239]
	v_lshl_add_u64 v[238:239], v[172:173], 0, v[238:239]
	v_add_co_u32_e32 v240, vcc, 0x8000, v238
	s_nop 1
	v_addc_co_u32_e32 v241, vcc, 0, v239, vcc
	global_load_dwordx4 v[242:245], v[238:239], off nt
	s_nop 0
	global_load_dwordx4 v[238:241], v[240:241], off nt
	s_and_b64 vcc, exec, s[16:17]
	s_cbranch_vccz .LBB0_952
	s_waitcnt vmcnt(14)
	v_cndmask_b32_e64 v189, v118, v126, s[6:7]
	v_mov_b32_e32 v190, v155
	s_nop 0
	v_lshlrev_b32_e32 v194, 16, v139
	v_and_b32_e32 v139, 0xffff0000, v139
	v_mov_b32_dpp v190, v189 row_ror:8 row_mask:0xf bank_mask:0xf
	v_cndmask_b32_e64 v189, v119, v127, s[6:7]
	v_cndmask_b32_e64 v126, v126, v190, s[6:7]
	v_cndmask_b32_e64 v118, v190, v118, s[6:7]
	v_mov_b32_e32 v190, v155
	v_lshlrev_b32_e32 v195, 16, v140
	v_and_b32_e32 v140, 0xffff0000, v140
	v_mov_b32_dpp v190, v189 row_ror:8 row_mask:0xf bank_mask:0xf
	v_cndmask_b32_e64 v189, v120, v128, s[6:7]
	v_cndmask_b32_e64 v127, v127, v190, s[6:7]
	v_cndmask_b32_e64 v119, v190, v119, s[6:7]
	v_mov_b32_e32 v190, v155
	v_lshlrev_b32_e32 v191, 16, v144
	v_and_b32_e32 v144, 0xffff0000, v144
	v_mov_b32_dpp v190, v189 row_ror:8 row_mask:0xf bank_mask:0xf
	v_cndmask_b32_e64 v189, v121, v129, s[6:7]
	v_cndmask_b32_e64 v128, v128, v190, s[6:7]
	v_cndmask_b32_e64 v120, v190, v120, s[6:7]
	v_mov_b32_e32 v190, v155
	v_lshlrev_b32_e32 v192, 16, v145
	v_and_b32_e32 v145, 0xffff0000, v145
	v_mov_b32_dpp v190, v189 row_ror:8 row_mask:0xf bank_mask:0xf
	v_cndmask_b32_e64 v189, v114, v122, s[6:7]
	v_cndmask_b32_e64 v129, v129, v190, s[6:7]
	v_cndmask_b32_e64 v121, v190, v121, s[6:7]
	v_mov_b32_e32 v190, v155
	v_mul_f32_e32 v121, v121, v139
	v_lshlrev_b32_e32 v193, 16, v138
	v_mov_b32_dpp v190, v189 row_ror:8 row_mask:0xf bank_mask:0xf
	v_cndmask_b32_e64 v189, v115, v123, s[6:7]
	v_cndmask_b32_e64 v122, v122, v190, s[6:7]
	v_cndmask_b32_e64 v114, v190, v114, s[6:7]
	v_mov_b32_e32 v190, v155
	v_mul_f32_e32 v139, v114, v195
	v_add_u32_e32 v114, s76, v187
	v_mov_b32_dpp v190, v189 row_ror:8 row_mask:0xf bank_mask:0xf
	v_cndmask_b32_e64 v189, v116, v124, s[6:7]
	v_cndmask_b32_e64 v123, v123, v190, s[6:7]
	v_cndmask_b32_e64 v115, v190, v115, s[6:7]
	v_mov_b32_e32 v190, v155
	v_mul_f32_e32 v140, v115, v140
	v_ashrrev_i32_e32 v115, 31, v114
	v_mov_b32_dpp v190, v189 row_ror:8 row_mask:0xf bank_mask:0xf
	v_cndmask_b32_e64 v189, v117, v125, s[6:7]
	v_cndmask_b32_e64 v124, v124, v190, s[6:7]
	v_cndmask_b32_e64 v116, v190, v116, s[6:7]
	v_mov_b32_e32 v190, v155
	v_and_b32_e32 v138, 0xffff0000, v138
	v_lshlrev_b32_e32 v196, 16, v141
	v_mov_b32_dpp v190, v189 row_ror:8 row_mask:0xf bank_mask:0xf
	v_cndmask_b32_e64 v125, v125, v190, s[6:7]
	v_cndmask_b32_e64 v117, v190, v117, s[6:7]
	v_lshlrev_b32_e32 v189, 16, v142
	v_and_b32_e32 v142, 0xffff0000, v142
	v_lshlrev_b32_e32 v190, 16, v143
	v_and_b32_e32 v143, 0xffff0000, v143
	v_and_b32_e32 v141, 0xffff0000, v141
	v_mul_f32_e32 v126, v126, v189
	v_mul_f32_e32 v127, v127, v142
	v_mul_f32_e32 v128, v128, v190
	v_mul_f32_e32 v129, v129, v143
	v_mul_f32_e32 v122, v122, v191
	v_mul_f32_e32 v123, v123, v144
	v_mul_f32_e32 v124, v124, v192
	v_mul_f32_e32 v125, v125, v145
	v_lshlrev_b64 v[114:115], 12, v[114:115]
	v_mul_f32_e32 v189, v118, v193
	v_mul_f32_e32 v138, v119, v138
	v_mul_f32_e32 v142, v116, v196
	v_mul_f32_e32 v141, v117, v141
	v_lshl_add_u64 v[118:119], v[168:169], 0, v[114:115]
	v_cvt_pk_bf16_f32 v114, v126, v127
	v_cvt_pk_bf16_f32 v115, v128, v129
	v_cvt_pk_bf16_f32 v116, v122, v123
	v_cvt_pk_bf16_f32 v117, v124, v125
	v_mul_f32_e32 v120, v120, v194
	global_store_dwordx4 v[118:119], v[114:117], off
	v_add_co_u32_e32 v118, vcc, 0x8000, v118
	s_nop 0
	v_cvt_pk_bf16_f32 v114, v189, v138
	v_cvt_pk_bf16_f32 v115, v120, v121
	v_cvt_pk_bf16_f32 v116, v139, v140
	v_cvt_pk_bf16_f32 v117, v142, v141
	v_addc_co_u32_e32 v119, vcc, 0, v119, vcc
	global_store_dwordx4 v[118:119], v[114:117], off
; template <class Epi, class Sched, bool GATHER, bool ALIGN_EPI = true, bool SP2 = true, bool REMAP64 = false>
; __device__ __forceinline__ void gemm_phase(LAS unsigned char* lds, const bf16* Ag, const bf16* Btg, const int K, const Sched& S, const Epi& E) {
;     ...
;             const bool hi = RP && (fr >= 8); const int rsh = hi ? -8 : 0, citx = hi ? cit + 32 : cit;
;             typename Epi::Pre pq[2];
;             { const int r0_ = wr * 64 + fr; pq[0] = E.pre(cur, (r0_ < cur.nrows ? r0_ : cur.nrows - 1) + rsh, citx); }
; #pragma unroll
;             for (int gq = 0; gq < 8; ++gq) { const int ai = gq >> 2, m = gq & 3, r = ai * HALF + wr * 64 + m * 16 + fr;
;                 if (gq + 1 < 8) { const int rn = ((gq + 1) >> 2) * HALF + wr * 64 + ((gq + 1) & 3) * 16 + fr; pq[(gq + 1) & 1] = E.pre(cur, (rn < cur.nrows ? rn : cur.nrows - 1) + rsh, citx); }
;                 __builtin_amdgcn_sched_barrier(0);
;                 if (r < cur.nrows) { float v0[8], v1[8];
; #pragma unroll
;                     for (int i = 0; i < 4; ++i) { v0[i] = acc[ai][0][m][0][i]; v0[4 + i] = acc[ai][0][m][1][i]; v1[i] = acc[ai][1][m][0][i]; v1[4 + i] = acc[ai][1][m][1][i]; }
;                     if constexpr (RP) {
; #pragma unroll
;                         for (int i = 0; i < 8; ++i) { const float snd = hi ? v0[i] : v1[i];
;                             const float rcv = __builtin_bit_cast(float, __builtin_amdgcn_update_dpp(0, __builtin_bit_cast(int, snd), 0x128, 0xf, 0xf, false));
;                             if (hi) v0[i] = rcv; else v1[i] = rcv; } }
;                     E.post(cur, r + rsh, citx, v0, v1, pq[gq & 1]); }
;                 __builtin_amdgcn_sched_barrier(0); }
;             }
;     __device__ __forceinline__ Pre pre(const Unit& u, int r, int cit) const { const size_t off = (size_t)(u.arow0 + r) * D + u.pn * 256 + cit; return Pre{__builtin_nontemporal_load((const v4u*)(gp + off)), __builtin_nontemporal_load((const v4u*)(gp + off + (size_t)8 * D))}; }
;     __device__ __forceinline__ void post(const Unit& u, int r, int cit, const float* v0, const float* v1, const Pre& p) const {
;         const size_t off = (size_t)(u.arow0 + r) * D + u.pn * 256 + cit; float g0[8], g1[8], a[8], b[8]; unpack8bf(p.g0, g0); unpack8bf(p.g1, g1);
; #pragma unroll
;         for (int i = 0; i < 8; ++i) { a[i] = g0[i] * v0[i]; b[i] = g1[i] * v1[i]; }
.LBB0_952:
	v_cndmask_b32_e64 v122, 0, 1, s[16:17]
	v_cmp_ne_u32_e64 s[10:11], 1, v122
	s_andn2_b64 vcc, exec, s[16:17]
	s_cbranch_vccnz .LBB0_954
	s_waitcnt vmcnt(14)
	v_cndmask_b32_e64 v122, v102, v110, s[6:7]
	v_mov_b32_e32 v123, v155
	s_nop 0
	v_lshlrev_b32_e32 v124, 16, v135
	v_lshlrev_b32_e32 v126, 16, v136
	v_mov_b32_dpp v123, v122 row_ror:8 row_mask:0xf bank_mask:0xf
	v_cndmask_b32_e64 v122, v103, v111, s[6:7]
	v_cndmask_b32_e64 v110, v110, v123, s[6:7]
	v_cndmask_b32_e64 v102, v123, v102, s[6:7]
	v_mov_b32_e32 v123, v155
	v_and_b32_e32 v127, 0xffff0000, v136
	v_lshlrev_b32_e32 v136, 16, v132
	v_mov_b32_dpp v123, v122 row_ror:8 row_mask:0xf bank_mask:0xf
	v_cndmask_b32_e64 v122, v104, v112, s[6:7]
	v_cndmask_b32_e64 v111, v111, v123, s[6:7]
	v_cndmask_b32_e64 v103, v123, v103, s[6:7]
	v_mov_b32_e32 v123, v155
	v_and_b32_e32 v125, 0xffff0000, v135
	v_and_b32_e32 v132, 0xffff0000, v132
	v_mov_b32_dpp v123, v122 row_ror:8 row_mask:0xf bank_mask:0xf
	v_cndmask_b32_e64 v122, v105, v113, s[6:7]
	v_cndmask_b32_e64 v112, v112, v123, s[6:7]
	v_cndmask_b32_e64 v104, v123, v104, s[6:7]
	v_mov_b32_e32 v123, v155
	v_mul_f32_e32 v112, v112, v124
	v_lshlrev_b32_e32 v128, 16, v137
	v_mov_b32_dpp v123, v122 row_ror:8 row_mask:0xf bank_mask:0xf
	v_cndmask_b32_e64 v122, v98, v106, s[6:7]
	v_cndmask_b32_e64 v113, v113, v123, s[6:7]
	v_cndmask_b32_e64 v105, v123, v105, s[6:7]
	v_mov_b32_e32 v123, v155
	v_and_b32_e32 v129, 0xffff0000, v137
	v_mul_f32_e32 v113, v113, v125
	v_mov_b32_dpp v123, v122 row_ror:8 row_mask:0xf bank_mask:0xf
	v_cndmask_b32_e64 v122, v99, v107, s[6:7]
	v_cndmask_b32_e64 v106, v106, v123, s[6:7]
	v_cndmask_b32_e64 v98, v123, v98, s[6:7]
	v_mov_b32_e32 v123, v155
	v_mul_f32_e32 v124, v98, v136
	v_add_u32_e32 v98, s80, v187
	v_mov_b32_dpp v123, v122 row_ror:8 row_mask:0xf bank_mask:0xf
	v_cndmask_b32_e64 v122, v100, v108, s[6:7]
	v_cndmask_b32_e64 v107, v107, v123, s[6:7]
	v_cndmask_b32_e64 v99, v123, v99, s[6:7]
	v_mov_b32_e32 v123, v155
	v_mul_f32_e32 v125, v99, v132
	v_ashrrev_i32_e32 v99, 31, v98
	v_mov_b32_dpp v123, v122 row_ror:8 row_mask:0xf bank_mask:0xf
	v_cndmask_b32_e64 v122, v101, v109, s[6:7]
	v_cndmask_b32_e64 v108, v108, v123, s[6:7]
	v_cndmask_b32_e64 v100, v123, v100, s[6:7]
	v_mov_b32_e32 v123, v155
	v_lshlrev_b32_e32 v137, 16, v133
	v_and_b32_e32 v133, 0xffff0000, v133
	v_mov_b32_dpp v123, v122 row_ror:8 row_mask:0xf bank_mask:0xf
	v_cndmask_b32_e64 v109, v109, v123, s[6:7]
	v_cndmask_b32_e64 v101, v123, v101, s[6:7]
	v_lshlrev_b32_e32 v122, 16, v134
	v_and_b32_e32 v123, 0xffff0000, v134
	v_lshlrev_b32_e32 v134, 16, v130
	v_and_b32_e32 v130, 0xffff0000, v130
	v_mul_f32_e32 v110, v110, v122
	v_mul_f32_e32 v111, v111, v123
	v_mul_f32_e32 v106, v106, v126
	v_mul_f32_e32 v107, v107, v127
	v_mul_f32_e32 v108, v108, v128
	v_mul_f32_e32 v109, v109, v129
	v_lshlrev_b64 v[98:99], 12, v[98:99]
	v_lshlrev_b32_e32 v135, 16, v131
	v_and_b32_e32 v131, 0xffff0000, v131
	v_mul_f32_e32 v122, v102, v134
	v_mul_f32_e32 v123, v103, v130
	v_mul_f32_e32 v126, v100, v137
	v_mul_f32_e32 v127, v101, v133
	v_lshl_add_u64 v[102:103], v[168:169], 0, v[98:99]
	v_cvt_pk_bf16_f32 v98, v110, v111
	v_cvt_pk_bf16_f32 v99, v112, v113
	v_cvt_pk_bf16_f32 v100, v106, v107
	v_cvt_pk_bf16_f32 v101, v108, v109
	v_mul_f32_e32 v104, v104, v135
	v_mul_f32_e32 v105, v105, v131
	global_store_dwordx4 v[102:103], v[98:101], off
	v_add_co_u32_e32 v102, vcc, 0x8000, v102
	s_nop 0
	v_cvt_pk_bf16_f32 v98, v122, v123
	v_cvt_pk_bf16_f32 v99, v104, v105
	v_cvt_pk_bf16_f32 v100, v124, v125
	v_cvt_pk_bf16_f32 v101, v126, v127
	v_addc_co_u32_e32 v103, vcc, 0, v103, vcc
	global_store_dwordx4 v[102:103], v[98:101], off
.LBB0_954:
	s_and_b64 vcc, exec, s[10:11]
	s_cbranch_vccnz .LBB0_956
	s_waitcnt vmcnt(14)
	v_cndmask_b32_e64 v106, v86, v94, s[6:7]
	v_mov_b32_e32 v107, v155
	s_nop 0
	v_lshlrev_b32_e32 v108, 16, v203
	v_lshlrev_b32_e32 v110, 16, v204
	v_mov_b32_dpp v107, v106 row_ror:8 row_mask:0xf bank_mask:0xf
	v_cndmask_b32_e64 v106, v87, v95, s[6:7]
	v_cndmask_b32_e64 v94, v94, v107, s[6:7]
	v_cndmask_b32_e64 v86, v107, v86, s[6:7]
	v_mov_b32_e32 v107, v155
	v_and_b32_e32 v111, 0xffff0000, v204
	v_lshlrev_b32_e32 v204, 16, v200
	v_mov_b32_dpp v107, v106 row_ror:8 row_mask:0xf bank_mask:0xf
	v_cndmask_b32_e64 v106, v88, v96, s[6:7]
	v_cndmask_b32_e64 v95, v95, v107, s[6:7]
	v_cndmask_b32_e64 v87, v107, v87, s[6:7]
	v_mov_b32_e32 v107, v155
	v_and_b32_e32 v109, 0xffff0000, v203
	v_and_b32_e32 v200, 0xffff0000, v200
	v_mov_b32_dpp v107, v106 row_ror:8 row_mask:0xf bank_mask:0xf
	v_cndmask_b32_e64 v106, v89, v97, s[6:7]
	v_cndmask_b32_e64 v96, v96, v107, s[6:7]
	v_cndmask_b32_e64 v88, v107, v88, s[6:7]
	v_mov_b32_e32 v107, v155
	v_mul_f32_e32 v96, v96, v108
	v_lshlrev_b32_e32 v112, 16, v205
	v_mov_b32_dpp v107, v106 row_ror:8 row_mask:0xf bank_mask:0xf
	v_cndmask_b32_e64 v106, v82, v90, s[6:7]
	v_cndmask_b32_e64 v97, v97, v107, s[6:7]
	v_cndmask_b32_e64 v89, v107, v89, s[6:7]
	v_mov_b32_e32 v107, v155
	v_and_b32_e32 v113, 0xffff0000, v205
	v_mul_f32_e32 v97, v97, v109
	v_mov_b32_dpp v107, v106 row_ror:8 row_mask:0xf bank_mask:0xf
	v_cndmask_b32_e64 v106, v83, v91, s[6:7]
	v_cndmask_b32_e64 v90, v90, v107, s[6:7]
	v_cndmask_b32_e64 v82, v107, v82, s[6:7]
	v_mov_b32_e32 v107, v155
	v_mul_f32_e32 v108, v82, v204
	v_add_u32_e32 v82, s81, v187
	v_mov_b32_dpp v107, v106 row_ror:8 row_mask:0xf bank_mask:0xf
	v_cndmask_b32_e64 v106, v84, v92, s[6:7]
	v_cndmask_b32_e64 v91, v91, v107, s[6:7]
	v_cndmask_b32_e64 v83, v107, v83, s[6:7]
	v_mov_b32_e32 v107, v155
	v_mul_f32_e32 v109, v83, v200
	v_ashrrev_i32_e32 v83, 31, v82
	v_mov_b32_dpp v107, v106 row_ror:8 row_mask:0xf bank_mask:0xf
; template <class Epi, class Sched, bool GATHER, bool ALIGN_EPI = true, bool SP2 = true, bool REMAP64 = false>
; __device__ __forceinline__ void gemm_phase(LAS unsigned char* lds, const bf16* Ag, const bf16* Btg, const int K, const Sched& S, const Epi& E) {
;     ...
;             const bool hi = RP && (fr >= 8); const int rsh = hi ? -8 : 0, citx = hi ? cit + 32 : cit;
;             typename Epi::Pre pq[2];
;             { const int r0_ = wr * 64 + fr; pq[0] = E.pre(cur, (r0_ < cur.nrows ? r0_ : cur.nrows - 1) + rsh, citx); }
; #pragma unroll
;             for (int gq = 0; gq < 8; ++gq) { const int ai = gq >> 2, m = gq & 3, r = ai * HALF + wr * 64 + m * 16 + fr;
;                 if (gq + 1 < 8) { const int rn = ((gq + 1) >> 2) * HALF + wr * 64 + ((gq + 1) & 3) * 16 + fr; pq[(gq + 1) & 1] = E.pre(cur, (rn < cur.nrows ? rn : cur.nrows - 1) + rsh, citx); }
;                 __builtin_amdgcn_sched_barrier(0);
;                 if (r < cur.nrows) { float v0[8], v1[8];
; #pragma unroll
;                     for (int i = 0; i < 4; ++i) { v0[i] = acc[ai][0][m][0][i]; v0[4 + i] = acc[ai][0][m][1][i]; v1[i] = acc[ai][1][m][0][i]; v1[4 + i] = acc[ai][1][m][1][i]; }
;                     if constexpr (RP) {
; #pragma unroll
;                         for (int i = 0; i < 8; ++i) { const float snd = hi ? v0[i] : v1[i];
;                             const float rcv = __builtin_bit_cast(float, __builtin_amdgcn_update_dpp(0, __builtin_bit_cast(int, snd), 0x128, 0xf, 0xf, false));
;                             if (hi) v0[i] = rcv; else v1[i] = rcv; } }
;                     E.post(cur, r + rsh, citx, v0, v1, pq[gq & 1]); }
;                 __builtin_amdgcn_sched_barrier(0); }
;             }
;     __device__ __forceinline__ Pre pre(const Unit& u, int r, int cit) const { const size_t off = (size_t)(u.arow0 + r) * D + u.pn * 256 + cit; return Pre{__builtin_nontemporal_load((const v4u*)(gp + off)), __builtin_nontemporal_load((const v4u*)(gp + off + (size_t)8 * D))}; }
;     __device__ __forceinline__ void post(const Unit& u, int r, int cit, const float* v0, const float* v1, const Pre& p) const {
;         const size_t off = (size_t)(u.arow0 + r) * D + u.pn * 256 + cit; float g0[8], g1[8], a[8], b[8]; unpack8bf(p.g0, g0); unpack8bf(p.g1, g1);
; #pragma unroll
;         for (int i = 0; i < 8; ++i) { a[i] = g0[i] * v0[i]; b[i] = g1[i] * v1[i]; }
	v_cndmask_b32_e64 v106, v85, v93, s[6:7]
	v_cndmask_b32_e64 v92, v92, v107, s[6:7]
	v_cndmask_b32_e64 v84, v107, v84, s[6:7]
	v_mov_b32_e32 v107, v155
	v_lshlrev_b32_e32 v205, 16, v201
	v_and_b32_e32 v201, 0xffff0000, v201
	v_mov_b32_dpp v107, v106 row_ror:8 row_mask:0xf bank_mask:0xf
	v_cndmask_b32_e64 v93, v93, v107, s[6:7]
	v_cndmask_b32_e64 v85, v107, v85, s[6:7]
	v_lshlrev_b32_e32 v106, 16, v202
	v_and_b32_e32 v107, 0xffff0000, v202
	v_lshlrev_b32_e32 v202, 16, v198
	v_and_b32_e32 v198, 0xffff0000, v198
	v_mul_f32_e32 v94, v94, v106
	v_mul_f32_e32 v95, v95, v107
	v_mul_f32_e32 v90, v90, v110
	v_mul_f32_e32 v91, v91, v111
	v_mul_f32_e32 v92, v92, v112
	v_mul_f32_e32 v93, v93, v113
	v_lshlrev_b64 v[82:83], 12, v[82:83]
	v_lshlrev_b32_e32 v203, 16, v199
	v_and_b32_e32 v199, 0xffff0000, v199
	v_mul_f32_e32 v106, v86, v202
	v_mul_f32_e32 v107, v87, v198
	v_mul_f32_e32 v110, v84, v205
	v_mul_f32_e32 v111, v85, v201
	v_lshl_add_u64 v[86:87], v[168:169], 0, v[82:83]
	v_cvt_pk_bf16_f32 v82, v94, v95
	v_cvt_pk_bf16_f32 v83, v96, v97
	v_cvt_pk_bf16_f32 v84, v90, v91
	v_cvt_pk_bf16_f32 v85, v92, v93
	v_mul_f32_e32 v88, v88, v203
	v_mul_f32_e32 v89, v89, v199
	global_store_dwordx4 v[86:87], v[82:85], off
	v_add_co_u32_e32 v86, vcc, 0x8000, v86
	s_nop 0
	v_cvt_pk_bf16_f32 v82, v106, v107
	v_cvt_pk_bf16_f32 v83, v88, v89
	v_cvt_pk_bf16_f32 v84, v108, v109
	v_cvt_pk_bf16_f32 v85, v110, v111
	v_addc_co_u32_e32 v87, vcc, 0, v87, vcc
	global_store_dwordx4 v[86:87], v[82:85], off
.LBB0_956:
	s_and_b64 vcc, exec, s[10:11]
	s_cbranch_vccnz .LBB0_958
	s_waitcnt vmcnt(14)
	v_cndmask_b32_e64 v90, v70, v78, s[6:7]
	v_mov_b32_e32 v91, v155
	s_nop 0
	v_lshlrev_b32_e32 v92, 16, v211
	v_lshlrev_b32_e32 v94, 16, v212
	v_mov_b32_dpp v91, v90 row_ror:8 row_mask:0xf bank_mask:0xf
	v_cndmask_b32_e64 v90, v71, v79, s[6:7]
	v_cndmask_b32_e64 v78, v78, v91, s[6:7]
	v_cndmask_b32_e64 v70, v91, v70, s[6:7]
	v_mov_b32_e32 v91, v155
	v_and_b32_e32 v95, 0xffff0000, v212
	v_lshlrev_b32_e32 v212, 16, v208
	v_mov_b32_dpp v91, v90 row_ror:8 row_mask:0xf bank_mask:0xf
	v_cndmask_b32_e64 v90, v72, v80, s[6:7]
	v_cndmask_b32_e64 v79, v79, v91, s[6:7]
	v_cndmask_b32_e64 v71, v91, v71, s[6:7]
	v_mov_b32_e32 v91, v155
	v_and_b32_e32 v93, 0xffff0000, v211
	v_and_b32_e32 v208, 0xffff0000, v208
	v_mov_b32_dpp v91, v90 row_ror:8 row_mask:0xf bank_mask:0xf
	v_cndmask_b32_e64 v90, v73, v81, s[6:7]
	v_cndmask_b32_e64 v80, v80, v91, s[6:7]
	v_cndmask_b32_e64 v72, v91, v72, s[6:7]
	v_mov_b32_e32 v91, v155
	v_mul_f32_e32 v80, v80, v92
	v_lshlrev_b32_e32 v96, 16, v213
	v_mov_b32_dpp v91, v90 row_ror:8 row_mask:0xf bank_mask:0xf
	v_cndmask_b32_e64 v90, v66, v74, s[6:7]
	v_cndmask_b32_e64 v81, v81, v91, s[6:7]
	v_cndmask_b32_e64 v73, v91, v73, s[6:7]
	v_mov_b32_e32 v91, v155
	v_and_b32_e32 v97, 0xffff0000, v213
	v_mul_f32_e32 v81, v81, v93
	v_mov_b32_dpp v91, v90 row_ror:8 row_mask:0xf bank_mask:0xf
	v_cndmask_b32_e64 v90, v67, v75, s[6:7]
	v_cndmask_b32_e64 v74, v74, v91, s[6:7]
	v_cndmask_b32_e64 v66, v91, v66, s[6:7]
	v_mov_b32_e32 v91, v155
	v_mul_f32_e32 v92, v66, v212
	v_add_u32_e32 v66, s83, v187
	v_mov_b32_dpp v91, v90 row_ror:8 row_mask:0xf bank_mask:0xf
	v_cndmask_b32_e64 v90, v68, v76, s[6:7]
	v_cndmask_b32_e64 v75, v75, v91, s[6:7]
	v_cndmask_b32_e64 v67, v91, v67, s[6:7]
	v_mov_b32_e32 v91, v155
	v_mul_f32_e32 v93, v67, v208
	v_ashrrev_i32_e32 v67, 31, v66
	v_mov_b32_dpp v91, v90 row_ror:8 row_mask:0xf bank_mask:0xf
	v_cndmask_b32_e64 v90, v69, v77, s[6:7]
	v_cndmask_b32_e64 v76, v76, v91, s[6:7]
	v_cndmask_b32_e64 v68, v91, v68, s[6:7]
	v_mov_b32_e32 v91, v155
	v_lshlrev_b32_e32 v213, 16, v209
	v_and_b32_e32 v209, 0xffff0000, v209
	v_mov_b32_dpp v91, v90 row_ror:8 row_mask:0xf bank_mask:0xf
	v_cndmask_b32_e64 v77, v77, v91, s[6:7]
	v_cndmask_b32_e64 v69, v91, v69, s[6:7]
	v_lshlrev_b32_e32 v90, 16, v210
	v_and_b32_e32 v91, 0xffff0000, v210
	v_lshlrev_b32_e32 v210, 16, v206
	v_and_b32_e32 v206, 0xffff0000, v206
	v_mul_f32_e32 v78, v78, v90
	v_mul_f32_e32 v79, v79, v91
	v_mul_f32_e32 v74, v74, v94
	v_mul_f32_e32 v75, v75, v95
	v_mul_f32_e32 v76, v76, v96
	v_mul_f32_e32 v77, v77, v97
	v_lshlrev_b64 v[66:67], 12, v[66:67]
	v_lshlrev_b32_e32 v211, 16, v207
	v_and_b32_e32 v207, 0xffff0000, v207
	v_mul_f32_e32 v90, v70, v210
	v_mul_f32_e32 v91, v71, v206
	v_mul_f32_e32 v94, v68, v213
	v_mul_f32_e32 v95, v69, v209
	v_lshl_add_u64 v[70:71], v[168:169], 0, v[66:67]
	v_cvt_pk_bf16_f32 v66, v78, v79
	v_cvt_pk_bf16_f32 v67, v80, v81
	v_cvt_pk_bf16_f32 v68, v74, v75
	v_cvt_pk_bf16_f32 v69, v76, v77
	v_mul_f32_e32 v72, v72, v211
	v_mul_f32_e32 v73, v73, v207
	global_store_dwordx4 v[70:71], v[66:69], off
	v_add_co_u32_e32 v70, vcc, 0x8000, v70
	s_nop 0
	v_cvt_pk_bf16_f32 v66, v90, v91
	v_cvt_pk_bf16_f32 v67, v72, v73
	v_cvt_pk_bf16_f32 v68, v92, v93
	v_cvt_pk_bf16_f32 v69, v94, v95
	v_addc_co_u32_e32 v71, vcc, 0, v71, vcc
	global_store_dwordx4 v[70:71], v[66:69], off
; template <class Epi, class Sched, bool GATHER, bool ALIGN_EPI = true, bool SP2 = true, bool REMAP64 = false>
; __device__ __forceinline__ void gemm_phase(LAS unsigned char* lds, const bf16* Ag, const bf16* Btg, const int K, const Sched& S, const Epi& E) {
;     ...
;             const bool hi = RP && (fr >= 8); const int rsh = hi ? -8 : 0, citx = hi ? cit + 32 : cit;
;             typename Epi::Pre pq[2];
;             { const int r0_ = wr * 64 + fr; pq[0] = E.pre(cur, (r0_ < cur.nrows ? r0_ : cur.nrows - 1) + rsh, citx); }
; #pragma unroll
;             for (int gq = 0; gq < 8; ++gq) { const int ai = gq >> 2, m = gq & 3, r = ai * HALF + wr * 64 + m * 16 + fr;
;                 if (gq + 1 < 8) { const int rn = ((gq + 1) >> 2) * HALF + wr * 64 + ((gq + 1) & 3) * 16 + fr; pq[(gq + 1) & 1] = E.pre(cur, (rn < cur.nrows ? rn : cur.nrows - 1) + rsh, citx); }
;                 __builtin_amdgcn_sched_barrier(0);
;                 if (r < cur.nrows) { float v0[8], v1[8];
; #pragma unroll
;                     for (int i = 0; i < 4; ++i) { v0[i] = acc[ai][0][m][0][i]; v0[4 + i] = acc[ai][0][m][1][i]; v1[i] = acc[ai][1][m][0][i]; v1[4 + i] = acc[ai][1][m][1][i]; }
;                     if constexpr (RP) {
; #pragma unroll
;                         for (int i = 0; i < 8; ++i) { const float snd = hi ? v0[i] : v1[i];
;                             const float rcv = __builtin_bit_cast(float, __builtin_amdgcn_update_dpp(0, __builtin_bit_cast(int, snd), 0x128, 0xf, 0xf, false));
;                             if (hi) v0[i] = rcv; else v1[i] = rcv; } }
;                     E.post(cur, r + rsh, citx, v0, v1, pq[gq & 1]); }
;                 __builtin_amdgcn_sched_barrier(0); }
;             }
;     __device__ __forceinline__ Pre pre(const Unit& u, int r, int cit) const { const size_t off = (size_t)(u.arow0 + r) * D + u.pn * 256 + cit; return Pre{__builtin_nontemporal_load((const v4u*)(gp + off)), __builtin_nontemporal_load((const v4u*)(gp + off + (size_t)8 * D))}; }
;     __device__ __forceinline__ void post(const Unit& u, int r, int cit, const float* v0, const float* v1, const Pre& p) const {
;         const size_t off = (size_t)(u.arow0 + r) * D + u.pn * 256 + cit; float g0[8], g1[8], a[8], b[8]; unpack8bf(p.g0, g0); unpack8bf(p.g1, g1);
; #pragma unroll
;         for (int i = 0; i < 8; ++i) { a[i] = g0[i] * v0[i]; b[i] = g1[i] * v1[i]; }
.LBB0_958:
	v_cndmask_b32_e64 v74, 0, 1, s[18:19]
	v_cmp_ne_u32_e64 s[10:11], 1, v74
	s_andn2_b64 vcc, exec, s[18:19]
	s_cbranch_vccnz .LBB0_960
	s_waitcnt vmcnt(14)
	v_cndmask_b32_e64 v74, v54, v62, s[6:7]
	v_mov_b32_e32 v75, v155
	s_nop 0
	v_lshlrev_b32_e32 v76, 16, v219
	v_lshlrev_b32_e32 v78, 16, v220
	v_mov_b32_dpp v75, v74 row_ror:8 row_mask:0xf bank_mask:0xf
	v_cndmask_b32_e64 v74, v55, v63, s[6:7]
	v_cndmask_b32_e64 v62, v62, v75, s[6:7]
	v_cndmask_b32_e64 v54, v75, v54, s[6:7]
	v_mov_b32_e32 v75, v155
	v_and_b32_e32 v79, 0xffff0000, v220
	v_lshlrev_b32_e32 v220, 16, v216
	v_mov_b32_dpp v75, v74 row_ror:8 row_mask:0xf bank_mask:0xf
	v_cndmask_b32_e64 v74, v56, v64, s[6:7]
	v_cndmask_b32_e64 v63, v63, v75, s[6:7]
	v_cndmask_b32_e64 v55, v75, v55, s[6:7]
	v_mov_b32_e32 v75, v155
	v_and_b32_e32 v77, 0xffff0000, v219
	v_and_b32_e32 v216, 0xffff0000, v216
	v_mov_b32_dpp v75, v74 row_ror:8 row_mask:0xf bank_mask:0xf
	v_cndmask_b32_e64 v74, v57, v65, s[6:7]
	v_cndmask_b32_e64 v64, v64, v75, s[6:7]
	v_cndmask_b32_e64 v56, v75, v56, s[6:7]
	v_mov_b32_e32 v75, v155
	v_mul_f32_e32 v64, v64, v76
	v_lshlrev_b32_e32 v80, 16, v221
	v_mov_b32_dpp v75, v74 row_ror:8 row_mask:0xf bank_mask:0xf
	v_cndmask_b32_e64 v74, v50, v58, s[6:7]
	v_cndmask_b32_e64 v65, v65, v75, s[6:7]
	v_cndmask_b32_e64 v57, v75, v57, s[6:7]
	v_mov_b32_e32 v75, v155
	v_and_b32_e32 v81, 0xffff0000, v221
	v_mul_f32_e32 v65, v65, v77
	v_mov_b32_dpp v75, v74 row_ror:8 row_mask:0xf bank_mask:0xf
	v_cndmask_b32_e64 v74, v51, v59, s[6:7]
	v_cndmask_b32_e64 v58, v58, v75, s[6:7]
	v_cndmask_b32_e64 v50, v75, v50, s[6:7]
	v_mov_b32_e32 v75, v155
	v_mul_f32_e32 v76, v50, v220
	v_add_u32_e32 v50, s82, v187
	v_mov_b32_dpp v75, v74 row_ror:8 row_mask:0xf bank_mask:0xf
	v_cndmask_b32_e64 v74, v52, v60, s[6:7]
	v_cndmask_b32_e64 v59, v59, v75, s[6:7]
	v_cndmask_b32_e64 v51, v75, v51, s[6:7]
	v_mov_b32_e32 v75, v155
	v_mul_f32_e32 v77, v51, v216
	v_ashrrev_i32_e32 v51, 31, v50
	v_mov_b32_dpp v75, v74 row_ror:8 row_mask:0xf bank_mask:0xf
	v_cndmask_b32_e64 v74, v53, v61, s[6:7]
	v_cndmask_b32_e64 v60, v60, v75, s[6:7]
	v_cndmask_b32_e64 v52, v75, v52, s[6:7]
	v_mov_b32_e32 v75, v155
	v_lshlrev_b32_e32 v221, 16, v217
	v_and_b32_e32 v217, 0xffff0000, v217
	v_mov_b32_dpp v75, v74 row_ror:8 row_mask:0xf bank_mask:0xf
	v_cndmask_b32_e64 v61, v61, v75, s[6:7]
	v_cndmask_b32_e64 v53, v75, v53, s[6:7]
	v_lshlrev_b32_e32 v74, 16, v218
	v_and_b32_e32 v75, 0xffff0000, v218
	v_lshlrev_b32_e32 v218, 16, v214
	v_and_b32_e32 v214, 0xffff0000, v214
	v_mul_f32_e32 v62, v62, v74
	v_mul_f32_e32 v63, v63, v75
	v_mul_f32_e32 v58, v58, v78
	v_mul_f32_e32 v59, v59, v79
	v_mul_f32_e32 v60, v60, v80
	v_mul_f32_e32 v61, v61, v81
	v_lshlrev_b64 v[50:51], 12, v[50:51]
	v_lshlrev_b32_e32 v219, 16, v215
	v_and_b32_e32 v215, 0xffff0000, v215
	v_mul_f32_e32 v74, v54, v218
	v_mul_f32_e32 v75, v55, v214
	v_mul_f32_e32 v78, v52, v221
	v_mul_f32_e32 v79, v53, v217
	v_lshl_add_u64 v[54:55], v[168:169], 0, v[50:51]
	v_cvt_pk_bf16_f32 v50, v62, v63
	v_cvt_pk_bf16_f32 v51, v64, v65
	v_cvt_pk_bf16_f32 v52, v58, v59
	v_cvt_pk_bf16_f32 v53, v60, v61
	v_mul_f32_e32 v56, v56, v219
	v_mul_f32_e32 v57, v57, v215
	global_store_dwordx4 v[54:55], v[50:53], off
	v_add_co_u32_e32 v54, vcc, 0x8000, v54
	s_nop 0
	v_cvt_pk_bf16_f32 v50, v74, v75
	v_cvt_pk_bf16_f32 v51, v56, v57
	v_cvt_pk_bf16_f32 v52, v76, v77
	v_cvt_pk_bf16_f32 v53, v78, v79
	v_addc_co_u32_e32 v55, vcc, 0, v55, vcc
	global_store_dwordx4 v[54:55], v[50:53], off
.LBB0_960:
	s_and_b64 vcc, exec, s[10:11]
	s_cbranch_vccnz .LBB0_962
	s_waitcnt vmcnt(14)
	v_cndmask_b32_e64 v58, v38, v46, s[6:7]
	v_mov_b32_e32 v59, v155
	s_nop 0
	v_lshlrev_b32_e32 v60, 16, v227
	v_lshlrev_b32_e32 v62, 16, v228
	v_mov_b32_dpp v59, v58 row_ror:8 row_mask:0xf bank_mask:0xf
	v_cndmask_b32_e64 v58, v39, v47, s[6:7]
	v_cndmask_b32_e64 v46, v46, v59, s[6:7]
	v_cndmask_b32_e64 v38, v59, v38, s[6:7]
	v_mov_b32_e32 v59, v155
	v_and_b32_e32 v63, 0xffff0000, v228
	v_lshlrev_b32_e32 v228, 16, v224
	v_mov_b32_dpp v59, v58 row_ror:8 row_mask:0xf bank_mask:0xf
	v_cndmask_b32_e64 v58, v40, v48, s[6:7]
	v_cndmask_b32_e64 v47, v47, v59, s[6:7]
	v_cndmask_b32_e64 v39, v59, v39, s[6:7]
	v_mov_b32_e32 v59, v155
	v_and_b32_e32 v61, 0xffff0000, v227
	v_and_b32_e32 v224, 0xffff0000, v224
	v_mov_b32_dpp v59, v58 row_ror:8 row_mask:0xf bank_mask:0xf
	v_cndmask_b32_e64 v58, v41, v49, s[6:7]
	v_cndmask_b32_e64 v48, v48, v59, s[6:7]
	v_cndmask_b32_e64 v40, v59, v40, s[6:7]
	v_mov_b32_e32 v59, v155
	v_mul_f32_e32 v48, v48, v60
	v_lshlrev_b32_e32 v64, 16, v229
	v_mov_b32_dpp v59, v58 row_ror:8 row_mask:0xf bank_mask:0xf
	v_cndmask_b32_e64 v58, v34, v42, s[6:7]
	v_cndmask_b32_e64 v49, v49, v59, s[6:7]
	v_cndmask_b32_e64 v41, v59, v41, s[6:7]
	v_mov_b32_e32 v59, v155
	v_and_b32_e32 v65, 0xffff0000, v229
	v_mul_f32_e32 v49, v49, v61
	v_mov_b32_dpp v59, v58 row_ror:8 row_mask:0xf bank_mask:0xf
	v_cndmask_b32_e64 v58, v35, v43, s[6:7]
	v_cndmask_b32_e64 v42, v42, v59, s[6:7]
	v_cndmask_b32_e64 v34, v59, v34, s[6:7]
	v_mov_b32_e32 v59, v155
	v_mul_f32_e32 v60, v34, v228
	v_add_u32_e32 v34, s84, v187
	v_mov_b32_dpp v59, v58 row_ror:8 row_mask:0xf bank_mask:0xf
	v_cndmask_b32_e64 v58, v36, v44, s[6:7]
	v_cndmask_b32_e64 v43, v43, v59, s[6:7]
	v_cndmask_b32_e64 v35, v59, v35, s[6:7]
	v_mov_b32_e32 v59, v155
	v_mul_f32_e32 v61, v35, v224
	v_ashrrev_i32_e32 v35, 31, v34
	v_mov_b32_dpp v59, v58 row_ror:8 row_mask:0xf bank_mask:0xf
	v_cndmask_b32_e64 v58, v37, v45, s[6:7]
	v_cndmask_b32_e64 v44, v44, v59, s[6:7]
	v_cndmask_b32_e64 v36, v59, v36, s[6:7]
	v_mov_b32_e32 v59, v155
	v_lshlrev_b32_e32 v229, 16, v225
	v_and_b32_e32 v225, 0xffff0000, v225
	v_mov_b32_dpp v59, v58 row_ror:8 row_mask:0xf bank_mask:0xf
	v_cndmask_b32_e64 v45, v45, v59, s[6:7]
	v_cndmask_b32_e64 v37, v59, v37, s[6:7]
	v_lshlrev_b32_e32 v58, 16, v226
	v_and_b32_e32 v59, 0xffff0000, v226
	v_lshlrev_b32_e32 v226, 16, v222
	v_and_b32_e32 v222, 0xffff0000, v222
	v_mul_f32_e32 v46, v46, v58
	v_mul_f32_e32 v47, v47, v59
	v_mul_f32_e32 v42, v42, v62
	v_mul_f32_e32 v43, v43, v63
	v_mul_f32_e32 v44, v44, v64
	v_mul_f32_e32 v45, v45, v65
	v_lshlrev_b64 v[34:35], 12, v[34:35]
	v_lshlrev_b32_e32 v227, 16, v223
	v_and_b32_e32 v223, 0xffff0000, v223
	v_mul_f32_e32 v58, v38, v226
	v_mul_f32_e32 v59, v39, v222
	v_mul_f32_e32 v62, v36, v229
	v_mul_f32_e32 v63, v37, v225
	v_lshl_add_u64 v[38:39], v[168:169], 0, v[34:35]
	v_cvt_pk_bf16_f32 v34, v46, v47
	v_cvt_pk_bf16_f32 v35, v48, v49
	v_cvt_pk_bf16_f32 v36, v42, v43
	v_cvt_pk_bf16_f32 v37, v44, v45
	v_mul_f32_e32 v40, v40, v227
	v_mul_f32_e32 v41, v41, v223
	global_store_dwordx4 v[38:39], v[34:37], off
	v_add_co_u32_e32 v38, vcc, 0x8000, v38
	s_nop 0
	v_cvt_pk_bf16_f32 v34, v58, v59
	v_cvt_pk_bf16_f32 v35, v40, v41
	v_cvt_pk_bf16_f32 v36, v60, v61
	v_cvt_pk_bf16_f32 v37, v62, v63
	v_addc_co_u32_e32 v39, vcc, 0, v39, vcc
	global_store_dwordx4 v[38:39], v[34:37], off
; template <class Epi, class Sched, bool GATHER, bool ALIGN_EPI = true, bool SP2 = true, bool REMAP64 = false>
; __device__ __forceinline__ void gemm_phase(LAS unsigned char* lds, const bf16* Ag, const bf16* Btg, const int K, const Sched& S, const Epi& E) {
;     ...
;             const bool hi = RP && (fr >= 8); const int rsh = hi ? -8 : 0, citx = hi ? cit + 32 : cit;
;             typename Epi::Pre pq[2];
;             { const int r0_ = wr * 64 + fr; pq[0] = E.pre(cur, (r0_ < cur.nrows ? r0_ : cur.nrows - 1) + rsh, citx); }
; #pragma unroll
;             for (int gq = 0; gq < 8; ++gq) { const int ai = gq >> 2, m = gq & 3, r = ai * HALF + wr * 64 + m * 16 + fr;
;                 if (gq + 1 < 8) { const int rn = ((gq + 1) >> 2) * HALF + wr * 64 + ((gq + 1) & 3) * 16 + fr; pq[(gq + 1) & 1] = E.pre(cur, (rn < cur.nrows ? rn : cur.nrows - 1) + rsh, citx); }
;                 __builtin_amdgcn_sched_barrier(0);
;                 if (r < cur.nrows) { float v0[8], v1[8];
; #pragma unroll
;                     for (int i = 0; i < 4; ++i) { v0[i] = acc[ai][0][m][0][i]; v0[4 + i] = acc[ai][0][m][1][i]; v1[i] = acc[ai][1][m][0][i]; v1[4 + i] = acc[ai][1][m][1][i]; }
;                     if constexpr (RP) {
; #pragma unroll
;                         for (int i = 0; i < 8; ++i) { const float snd = hi ? v0[i] : v1[i];
;                             const float rcv = __builtin_bit_cast(float, __builtin_amdgcn_update_dpp(0, __builtin_bit_cast(int, snd), 0x128, 0xf, 0xf, false));
;                             if (hi) v0[i] = rcv; else v1[i] = rcv; } }
;                     E.post(cur, r + rsh, citx, v0, v1, pq[gq & 1]); }
;                 __builtin_amdgcn_sched_barrier(0); }
;             }
;     __device__ __forceinline__ Pre pre(const Unit& u, int r, int cit) const { const size_t off = (size_t)(u.arow0 + r) * D + u.pn * 256 + cit; return Pre{__builtin_nontemporal_load((const v4u*)(gp + off)), __builtin_nontemporal_load((const v4u*)(gp + off + (size_t)8 * D))}; }
;     __device__ __forceinline__ void post(const Unit& u, int r, int cit, const float* v0, const float* v1, const Pre& p) const {
;         const size_t off = (size_t)(u.arow0 + r) * D + u.pn * 256 + cit; float g0[8], g1[8], a[8], b[8]; unpack8bf(p.g0, g0); unpack8bf(p.g1, g1);
; #pragma unroll
;         for (int i = 0; i < 8; ++i) { a[i] = g0[i] * v0[i]; b[i] = g1[i] * v1[i]; }
.LBB0_962:
	s_and_b64 vcc, exec, s[10:11]
	s_cbranch_vccnz .LBB0_964
	s_waitcnt vmcnt(14)
	v_cndmask_b32_e64 v42, v22, v30, s[6:7]
	v_mov_b32_e32 v43, v155
	s_nop 0
	v_lshlrev_b32_e32 v44, 16, v235
	v_lshlrev_b32_e32 v46, 16, v236
	v_mov_b32_dpp v43, v42 row_ror:8 row_mask:0xf bank_mask:0xf
	v_cndmask_b32_e64 v42, v23, v31, s[6:7]
	v_cndmask_b32_e64 v30, v30, v43, s[6:7]
	v_cndmask_b32_e64 v22, v43, v22, s[6:7]
	v_mov_b32_e32 v43, v155
	v_and_b32_e32 v47, 0xffff0000, v236
	v_lshlrev_b32_e32 v236, 16, v232
	v_mov_b32_dpp v43, v42 row_ror:8 row_mask:0xf bank_mask:0xf
	v_cndmask_b32_e64 v42, v24, v32, s[6:7]
	v_cndmask_b32_e64 v31, v31, v43, s[6:7]
	v_cndmask_b32_e64 v23, v43, v23, s[6:7]
	v_mov_b32_e32 v43, v155
	v_and_b32_e32 v45, 0xffff0000, v235
	v_and_b32_e32 v232, 0xffff0000, v232
	v_mov_b32_dpp v43, v42 row_ror:8 row_mask:0xf bank_mask:0xf
	v_cndmask_b32_e64 v42, v25, v33, s[6:7]
	v_cndmask_b32_e64 v32, v32, v43, s[6:7]
	v_cndmask_b32_e64 v24, v43, v24, s[6:7]
	v_mov_b32_e32 v43, v155
	v_mul_f32_e32 v32, v32, v44
	v_lshlrev_b32_e32 v48, 16, v237
	v_mov_b32_dpp v43, v42 row_ror:8 row_mask:0xf bank_mask:0xf
	v_cndmask_b32_e64 v42, v18, v26, s[6:7]
	v_cndmask_b32_e64 v33, v33, v43, s[6:7]
	v_cndmask_b32_e64 v25, v43, v25, s[6:7]
	v_mov_b32_e32 v43, v155
	v_and_b32_e32 v49, 0xffff0000, v237
	v_mul_f32_e32 v33, v33, v45
	v_mov_b32_dpp v43, v42 row_ror:8 row_mask:0xf bank_mask:0xf
	v_cndmask_b32_e64 v42, v19, v27, s[6:7]
	v_cndmask_b32_e64 v26, v26, v43, s[6:7]
	v_cndmask_b32_e64 v18, v43, v18, s[6:7]
	v_mov_b32_e32 v43, v155
	v_mul_f32_e32 v44, v18, v236
	v_add_u32_e32 v18, s85, v187
	v_mov_b32_dpp v43, v42 row_ror:8 row_mask:0xf bank_mask:0xf
	v_cndmask_b32_e64 v42, v20, v28, s[6:7]
	v_cndmask_b32_e64 v27, v27, v43, s[6:7]
	v_cndmask_b32_e64 v19, v43, v19, s[6:7]
	v_mov_b32_e32 v43, v155
	v_mul_f32_e32 v45, v19, v232
	v_ashrrev_i32_e32 v19, 31, v18
	v_mov_b32_dpp v43, v42 row_ror:8 row_mask:0xf bank_mask:0xf
	v_cndmask_b32_e64 v42, v21, v29, s[6:7]
	v_cndmask_b32_e64 v28, v28, v43, s[6:7]
	v_cndmask_b32_e64 v20, v43, v20, s[6:7]
	v_mov_b32_e32 v43, v155
	v_lshlrev_b32_e32 v237, 16, v233
	v_and_b32_e32 v233, 0xffff0000, v233
	v_mov_b32_dpp v43, v42 row_ror:8 row_mask:0xf bank_mask:0xf
	v_cndmask_b32_e64 v29, v29, v43, s[6:7]
	v_cndmask_b32_e64 v21, v43, v21, s[6:7]
	v_lshlrev_b32_e32 v42, 16, v234
	v_and_b32_e32 v43, 0xffff0000, v234
	v_lshlrev_b32_e32 v234, 16, v230
	v_and_b32_e32 v230, 0xffff0000, v230
	v_mul_f32_e32 v30, v30, v42
	v_mul_f32_e32 v31, v31, v43
	v_mul_f32_e32 v26, v26, v46
	v_mul_f32_e32 v27, v27, v47
	v_mul_f32_e32 v28, v28, v48
	v_mul_f32_e32 v29, v29, v49
	v_lshlrev_b64 v[18:19], 12, v[18:19]
	v_lshlrev_b32_e32 v235, 16, v231
	v_and_b32_e32 v231, 0xffff0000, v231
	v_mul_f32_e32 v42, v22, v234
	v_mul_f32_e32 v43, v23, v230
	v_mul_f32_e32 v46, v20, v237
	v_mul_f32_e32 v47, v21, v233
	v_lshl_add_u64 v[22:23], v[168:169], 0, v[18:19]
	v_cvt_pk_bf16_f32 v18, v30, v31
	v_cvt_pk_bf16_f32 v19, v32, v33
	v_cvt_pk_bf16_f32 v20, v26, v27
	v_cvt_pk_bf16_f32 v21, v28, v29
	v_mul_f32_e32 v24, v24, v235
	v_mul_f32_e32 v25, v25, v231
	global_store_dwordx4 v[22:23], v[18:21], off
	v_add_co_u32_e32 v22, vcc, 0x8000, v22
	s_nop 0
	v_cvt_pk_bf16_f32 v18, v42, v43
	v_cvt_pk_bf16_f32 v19, v24, v25
	v_cvt_pk_bf16_f32 v20, v44, v45
	v_cvt_pk_bf16_f32 v21, v46, v47
	v_addc_co_u32_e32 v23, vcc, 0, v23, vcc
	global_store_dwordx4 v[22:23], v[18:21], off
.LBB0_964:
	s_and_b64 vcc, exec, s[10:11]
	s_cbranch_vccnz .LBB0_966
	s_waitcnt vmcnt(14)
	v_cndmask_b32_e64 v18, v6, v14, s[6:7]
	v_mov_b32_e32 v19, v155
	s_nop 0
	v_lshlrev_b32_e32 v20, 16, v243
	v_lshlrev_b32_e32 v30, 16, v240
	v_mov_b32_dpp v19, v18 row_ror:8 row_mask:0xf bank_mask:0xf
	v_cndmask_b32_e64 v18, v7, v15, s[6:7]
	v_cndmask_b32_e64 v14, v14, v19, s[6:7]
	v_cndmask_b32_e64 v6, v19, v6, s[6:7]
	v_mov_b32_e32 v19, v155
	v_and_b32_e32 v21, 0xffff0000, v243
	v_and_b32_e32 v31, 0xffff0000, v240
	v_mov_b32_dpp v19, v18 row_ror:8 row_mask:0xf bank_mask:0xf
	v_cndmask_b32_e64 v18, v8, v16, s[6:7]
	v_cndmask_b32_e64 v15, v15, v19, s[6:7]
	v_cndmask_b32_e64 v7, v19, v7, s[6:7]
	v_mov_b32_e32 v19, v155
	v_lshlrev_b32_e32 v22, 16, v244
	v_and_b32_e32 v23, 0xffff0000, v244
	v_mov_b32_dpp v19, v18 row_ror:8 row_mask:0xf bank_mask:0xf
	v_cndmask_b32_e64 v18, v9, v17, s[6:7]
	v_cndmask_b32_e64 v16, v16, v19, s[6:7]
	v_cndmask_b32_e64 v8, v19, v8, s[6:7]
	v_mov_b32_e32 v19, v155
	v_mul_f32_e32 v16, v16, v20
	v_lshlrev_b32_e32 v24, 16, v245
	v_mov_b32_dpp v19, v18 row_ror:8 row_mask:0xf bank_mask:0xf
	v_cndmask_b32_e64 v18, v2, v10, s[6:7]
	v_cndmask_b32_e64 v17, v17, v19, s[6:7]
	v_cndmask_b32_e64 v9, v19, v9, s[6:7]
	v_mov_b32_e32 v19, v155
	v_and_b32_e32 v25, 0xffff0000, v245
	v_mul_f32_e32 v17, v17, v21
	v_mov_b32_dpp v19, v18 row_ror:8 row_mask:0xf bank_mask:0xf
	v_cndmask_b32_e64 v18, v3, v11, s[6:7]
	v_cndmask_b32_e64 v10, v10, v19, s[6:7]
	v_cndmask_b32_e64 v2, v19, v2, s[6:7]
	v_mov_b32_e32 v19, v155
	v_mul_f32_e32 v20, v2, v30
	v_add_u32_e32 v2, s86, v187
	v_mov_b32_dpp v19, v18 row_ror:8 row_mask:0xf bank_mask:0xf
	v_cndmask_b32_e64 v18, v4, v12, s[6:7]
	v_cndmask_b32_e64 v11, v11, v19, s[6:7]
	v_cndmask_b32_e64 v3, v19, v3, s[6:7]
	v_mov_b32_e32 v19, v155
	v_mul_f32_e32 v21, v3, v31
	v_ashrrev_i32_e32 v3, 31, v2
	v_mov_b32_dpp v19, v18 row_ror:8 row_mask:0xf bank_mask:0xf
	v_cndmask_b32_e64 v18, v5, v13, s[6:7]
	v_cndmask_b32_e64 v12, v12, v19, s[6:7]
	v_cndmask_b32_e64 v4, v19, v4, s[6:7]
	v_mov_b32_e32 v19, v155
	v_lshlrev_b32_e32 v26, 16, v238
	v_and_b32_e32 v27, 0xffff0000, v238
	v_mov_b32_dpp v19, v18 row_ror:8 row_mask:0xf bank_mask:0xf
	v_cndmask_b32_e64 v13, v13, v19, s[6:7]
	v_cndmask_b32_e64 v5, v19, v5, s[6:7]
	v_lshlrev_b32_e32 v18, 16, v242
	v_and_b32_e32 v19, 0xffff0000, v242
	v_lshlrev_b32_e32 v32, 16, v241
	v_and_b32_e32 v33, 0xffff0000, v241
	v_mul_f32_e32 v14, v14, v18
	v_mul_f32_e32 v15, v15, v19
	v_mul_f32_e32 v10, v10, v22
	v_mul_f32_e32 v11, v11, v23
	v_mul_f32_e32 v12, v12, v24
	v_mul_f32_e32 v13, v13, v25
	v_lshlrev_b64 v[2:3], 12, v[2:3]
	v_lshlrev_b32_e32 v28, 16, v239
	v_and_b32_e32 v29, 0xffff0000, v239
	v_mul_f32_e32 v18, v6, v26
	v_mul_f32_e32 v19, v7, v27
	v_mul_f32_e32 v22, v4, v32
	v_mul_f32_e32 v23, v5, v33
	v_lshl_add_u64 v[6:7], v[168:169], 0, v[2:3]
	v_cvt_pk_bf16_f32 v2, v14, v15
	v_cvt_pk_bf16_f32 v3, v16, v17
	v_cvt_pk_bf16_f32 v4, v10, v11
	v_cvt_pk_bf16_f32 v5, v12, v13
	v_mul_f32_e32 v8, v8, v28
	v_mul_f32_e32 v9, v9, v29
	global_store_dwordx4 v[6:7], v[2:5], off
	v_add_co_u32_e32 v6, vcc, 0x8000, v6
	s_nop 0
	v_cvt_pk_bf16_f32 v2, v18, v19
	v_cvt_pk_bf16_f32 v3, v8, v9
	v_cvt_pk_bf16_f32 v4, v20, v21
	v_cvt_pk_bf16_f32 v5, v22, v23
	v_addc_co_u32_e32 v7, vcc, 0, v7, vcc
	global_store_dwordx4 v[6:7], v[2:5], off

; template <class Epi, class Sched, bool GATHER, bool ALIGN_EPI = true, bool SP2 = true, bool REMAP64 = false>
; __device__ __forceinline__ void gemm_phase(LAS unsigned char* lds, const bf16* Ag, const bf16* Btg, const int K, const Sched& S, const Epi& E) {
;     ...
;             constexpr bool RP = REMAP64 && Epi::ROWPAIR;
;             const bool hi = RP && (fr >= 8); const int rsh = hi ? -8 : 0, citx = hi ? cit + 32 : cit;
;             typename Epi::Pre pq[2];
;             { const int r0_ = wr * 64 + fr; pq[0] = E.pre(cur, (r0_ < cur.nrows ? r0_ : cur.nrows - 1) + rsh, citx); }
; #pragma unroll
;             for (int gq = 0; gq < 8; ++gq) { const int ai = gq >> 2, m = gq & 3, r = ai * HALF + wr * 64 + m * 16 + fr;
;                 if (gq + 1 < 8) { const int rn = ((gq + 1) >> 2) * HALF + wr * 64 + ((gq + 1) & 3) * 16 + fr; pq[(gq + 1) & 1] = E.pre(cur, (rn < cur.nrows ? rn : cur.nrows - 1) + rsh, citx); }
;                 __builtin_amdgcn_sched_barrier(0);
;                 if (r < cur.nrows) { float v0[8], v1[8];
; #pragma unroll
;                     for (int i = 0; i < 4; ++i) { v0[i] = acc[ai][0][m][0][i]; v0[4 + i] = acc[ai][0][m][1][i]; v1[i] = acc[ai][1][m][0][i]; v1[4 + i] = acc[ai][1][m][1][i]; }
;                     if constexpr (RP) {
; #pragma unroll
;                         for (int i = 0; i < 8; ++i) { const float snd = hi ? v0[i] : v1[i];
;                             const float rcv = __builtin_bit_cast(float, __builtin_amdgcn_update_dpp(0, __builtin_bit_cast(int, snd), 0x128, 0xf, 0xf, false));
;                             if (hi) v0[i] = rcv; else v1[i] = rcv; } }
;                     E.post(cur, r + rsh, citx, v0, v1, pq[gq & 1]); }
;                 __builtin_amdgcn_sched_barrier(0); }
;     __device__ __forceinline__ Pre pre(const Unit& u, int r, int cit) const { const size_t off = (size_t)(u.arow0 + r) * D + u.pn * 256 + cit; return Pre{__builtin_nontemporal_load((const v4u*)(gd + off)), __builtin_nontemporal_load((const v4u*)(gd + off + (size_t)8 * D)), __builtin_nontemporal_load ...
;     __device__ __forceinline__ void post(const Unit& u, int r, int cit, const float* v0, const float* v1, const Pre& p) const {
;         const size_t off = (size_t)(u.arow0 + r) * D + u.pn * 256 + cit; float g0[8], g1[8], m0[8], m1[8]; unpack8bf(p.g0, g0); unpack8bf(p.g1, g1); unpack8bf(p.m0, m0); unpack8bf(p.m1, m1);
; #pragma unroll
.LBB0_1152:
	v_add_u32_e32 v130, s8, v185
	v_ashrrev_i32_e32 v131, 31, v130
	s_lshl_b32 s42, s40, 8
	v_lshlrev_b64 v[130:131], 11, v[130:131]
	s_ashr_i32 s43, s42, 31
	v_lshl_add_u64 v[130:131], v[130:131], 0, s[42:43]
	v_or_b32_e32 v130, v130, v172
	v_lshlrev_b64 v[130:131], 1, v[130:131]
	v_lshl_add_u64 v[132:133], s[50:51], 0, v[130:131]
	v_add_co_u32_e32 v134, vcc, s63, v132
	v_lshl_add_u64 v[130:131], s[20:21], 0, v[130:131]
	s_nop 0
	v_addc_co_u32_e32 v135, vcc, 0, v133, vcc
	global_load_dwordx4 v[158:161], v[132:133], off nt
	global_load_dwordx4 v[154:157], v[134:135], off nt
	v_add_co_u32_e32 v132, vcc, s63, v130
	v_add_u32_e32 v197, s8, v184
	s_nop 0
	v_addc_co_u32_e32 v133, vcc, 0, v131, vcc
	global_load_dwordx4 v[150:153], v[130:131], off nt
	global_load_dwordx4 v[146:149], v[132:133], off nt
	v_add_u32_e32 v130, v197, v186
	v_ashrrev_i32_e32 v131, 31, v130
	v_mov_b32_e32 v183, s43
	v_or_b32_e32 v182, s42, v172
	v_lshlrev_b64 v[130:131], 11, v[130:131]
	v_lshl_add_u64 v[130:131], v[130:131], 0, v[182:183]
	v_lshlrev_b64 v[130:131], 1, v[130:131]
	v_lshl_add_u64 v[132:133], s[50:51], 0, v[130:131]
	v_add_co_u32_e32 v134, vcc, 0x8000, v132
	v_lshl_add_u64 v[130:131], s[20:21], 0, v[130:131]
	s_nop 0
	v_addc_co_u32_e32 v135, vcc, 0, v133, vcc
	global_load_dwordx4 v[142:145], v[132:133], off nt
	global_load_dwordx4 v[138:141], v[134:135], off nt
	v_add_co_u32_e32 v132, vcc, 0x8000, v130
	v_add_u32_e32 v196, v197, v171
	s_nop 0
	v_addc_co_u32_e32 v133, vcc, 0, v131, vcc
	global_load_dwordx4 v[134:137], v[130:131], off nt
	s_nop 0
	global_load_dwordx4 v[130:133], v[132:133], off nt
	s_nop 1
	v_add_u32_e32 v214, v197, v187
	v_ashrrev_i32_e32 v215, 31, v214
	v_lshlrev_b64 v[214:215], 11, v[214:215]
	v_lshl_add_u64 v[214:215], v[214:215], 0, v[182:183]
	v_lshlrev_b64 v[214:215], 1, v[214:215]
	v_lshl_add_u64 v[216:217], s[50:51], 0, v[214:215]
	v_add_co_u32_e32 v218, vcc, 0x8000, v216
	v_lshl_add_u64 v[214:215], s[20:21], 0, v[214:215]
	s_nop 0
	v_addc_co_u32_e32 v219, vcc, 0, v217, vcc
	global_load_dwordx4 v[226:229], v[216:217], off nt
	global_load_dwordx4 v[222:225], v[218:219], off nt
	v_add_co_u32_e32 v216, vcc, 0x8000, v214
	s_nop 1
	v_addc_co_u32_e32 v217, vcc, 0, v215, vcc
	global_load_dwordx4 v[218:221], v[214:215], off nt
	s_nop 0
	global_load_dwordx4 v[214:217], v[216:217], off nt
	s_nop 1
	v_add_u32_e32 v230, v197, v188
	v_ashrrev_i32_e32 v231, 31, v230
	v_lshlrev_b64 v[230:231], 11, v[230:231]
	v_lshl_add_u64 v[230:231], v[230:231], 0, v[182:183]
	v_lshlrev_b64 v[230:231], 1, v[230:231]
	v_lshl_add_u64 v[232:233], s[50:51], 0, v[230:231]
	v_add_co_u32_e32 v234, vcc, 0x8000, v232
	v_lshl_add_u64 v[230:231], s[20:21], 0, v[230:231]
	s_nop 0
	v_addc_co_u32_e32 v235, vcc, 0, v233, vcc
	global_load_dwordx4 v[242:245], v[232:233], off nt
	global_load_dwordx4 v[238:241], v[234:235], off nt
	v_add_co_u32_e32 v232, vcc, 0x8000, v230
	s_nop 1
	v_addc_co_u32_e32 v233, vcc, 0, v231, vcc
	global_load_dwordx4 v[234:237], v[230:231], off nt
	s_nop 0
	global_load_dwordx4 v[230:233], v[232:233], off nt
	s_and_b64 vcc, exec, s[16:17]
	s_cbranch_vccz .LBB0_1154
	s_waitcnt vmcnt(12)
	v_cndmask_b32_e64 v198, v118, v126, s[0:1]
	v_mov_b32_e32 v199, 0
	s_nop 0
	v_lshlrev_b32_e32 v204, 16, v156
	v_lshlrev_b32_e32 v212, 16, v148
	v_mov_b32_dpp v199, v198 row_ror:8 row_mask:0xf bank_mask:0xf
	v_cndmask_b32_e64 v198, v119, v127, s[0:1]
	v_cndmask_b32_e64 v126, v126, v199, s[0:1]
	v_cndmask_b32_e64 v118, v199, v118, s[0:1]
	v_mov_b32_e32 v199, 0
	v_and_b32_e32 v156, 0xffff0000, v156
	v_and_b32_e32 v148, 0xffff0000, v148
	v_mov_b32_dpp v199, v198 row_ror:8 row_mask:0xf bank_mask:0xf
	v_cndmask_b32_e64 v198, v120, v128, s[0:1]
	v_cndmask_b32_e64 v127, v127, v199, s[0:1]
	v_cndmask_b32_e64 v119, v199, v119, s[0:1]
	v_mov_b32_e32 v199, 0
	v_lshlrev_b32_e32 v200, 16, v160
	v_and_b32_e32 v160, 0xffff0000, v160
	v_mov_b32_dpp v199, v198 row_ror:8 row_mask:0xf bank_mask:0xf
	v_cndmask_b32_e64 v198, v121, v129, s[0:1]
	v_cndmask_b32_e64 v128, v128, v199, s[0:1]
	v_cndmask_b32_e64 v120, v199, v120, s[0:1]
	v_mov_b32_e32 v199, 0
	v_lshlrev_b32_e32 v201, 16, v161
	v_and_b32_e32 v161, 0xffff0000, v161
	v_mov_b32_dpp v199, v198 row_ror:8 row_mask:0xf bank_mask:0xf
	v_cndmask_b32_e64 v198, v114, v122, s[0:1]
	v_cndmask_b32_e64 v129, v129, v199, s[0:1]
	v_cndmask_b32_e64 v121, v199, v121, s[0:1]
	v_mov_b32_e32 v199, 0
	v_lshlrev_b32_e32 v206, 16, v150
	v_and_b32_e32 v150, 0xffff0000, v150
	v_mov_b32_dpp v199, v198 row_ror:8 row_mask:0xf bank_mask:0xf
	v_cndmask_b32_e64 v198, v115, v123, s[0:1]
	v_cndmask_b32_e64 v122, v122, v199, s[0:1]
	v_cndmask_b32_e64 v114, v199, v114, s[0:1]
	v_mov_b32_e32 v199, 0
	v_fmac_f32_e32 v212, v114, v204
	v_add_u32_e32 v114, s60, v196
	v_mov_b32_dpp v199, v198 row_ror:8 row_mask:0xf bank_mask:0xf
	v_cndmask_b32_e64 v198, v116, v124, s[0:1]
	v_cndmask_b32_e64 v123, v123, v199, s[0:1]
	v_cndmask_b32_e64 v115, v199, v115, s[0:1]
	v_mov_b32_e32 v199, 0
	v_fmac_f32_e32 v148, v115, v156
	v_ashrrev_i32_e32 v115, 31, v114
	v_mov_b32_dpp v199, v198 row_ror:8 row_mask:0xf bank_mask:0xf
	v_cndmask_b32_e64 v198, v117, v125, s[0:1]
	v_cndmask_b32_e64 v124, v124, v199, s[0:1]
	v_cndmask_b32_e64 v116, v199, v116, s[0:1]
	v_mov_b32_e32 v199, 0
	v_lshlrev_b32_e32 v207, 16, v151
	v_and_b32_e32 v151, 0xffff0000, v151
	v_mov_b32_dpp v199, v198 row_ror:8 row_mask:0xf bank_mask:0xf
	v_cndmask_b32_e64 v125, v125, v199, s[0:1]
	v_cndmask_b32_e64 v117, v199, v117, s[0:1]
	v_lshlrev_b32_e32 v198, 16, v158
	v_and_b32_e32 v158, 0xffff0000, v158
	v_lshlrev_b32_e32 v199, 16, v159
	v_and_b32_e32 v159, 0xffff0000, v159
	v_lshlrev_b32_e32 v208, 16, v152
; template <class Epi, class Sched, bool GATHER, bool ALIGN_EPI = true, bool SP2 = true, bool REMAP64 = false>
; __device__ __forceinline__ void gemm_phase(LAS unsigned char* lds, const bf16* Ag, const bf16* Btg, const int K, const Sched& S, const Epi& E) {
;     ...
;             constexpr bool RP = REMAP64 && Epi::ROWPAIR;
;             const bool hi = RP && (fr >= 8); const int rsh = hi ? -8 : 0, citx = hi ? cit + 32 : cit;
;             typename Epi::Pre pq[2];
;             { const int r0_ = wr * 64 + fr; pq[0] = E.pre(cur, (r0_ < cur.nrows ? r0_ : cur.nrows - 1) + rsh, citx); }
; #pragma unroll
;             for (int gq = 0; gq < 8; ++gq) { const int ai = gq >> 2, m = gq & 3, r = ai * HALF + wr * 64 + m * 16 + fr;
;                 if (gq + 1 < 8) { const int rn = ((gq + 1) >> 2) * HALF + wr * 64 + ((gq + 1) & 3) * 16 + fr; pq[(gq + 1) & 1] = E.pre(cur, (rn < cur.nrows ? rn : cur.nrows - 1) + rsh, citx); }
;                 __builtin_amdgcn_sched_barrier(0);
;                 if (r < cur.nrows) { float v0[8], v1[8];
; #pragma unroll
;                     for (int i = 0; i < 4; ++i) { v0[i] = acc[ai][0][m][0][i]; v0[4 + i] = acc[ai][0][m][1][i]; v1[i] = acc[ai][1][m][0][i]; v1[4 + i] = acc[ai][1][m][1][i]; }
;                     if constexpr (RP) {
; #pragma unroll
;                         for (int i = 0; i < 8; ++i) { const float snd = hi ? v0[i] : v1[i];
;                             const float rcv = __builtin_bit_cast(float, __builtin_amdgcn_update_dpp(0, __builtin_bit_cast(int, snd), 0x128, 0xf, 0xf, false));
;                             if (hi) v0[i] = rcv; else v1[i] = rcv; } }
;                     E.post(cur, r + rsh, citx, v0, v1, pq[gq & 1]); }
;                 __builtin_amdgcn_sched_barrier(0); }
;     __device__ __forceinline__ Pre pre(const Unit& u, int r, int cit) const { const size_t off = (size_t)(u.arow0 + r) * D + u.pn * 256 + cit; return Pre{__builtin_nontemporal_load((const v4u*)(gd + off)), __builtin_nontemporal_load((const v4u*)(gd + off + (size_t)8 * D)), __builtin_nontemporal_load ...
;     __device__ __forceinline__ void post(const Unit& u, int r, int cit, const float* v0, const float* v1, const Pre& p) const {
;         const size_t off = (size_t)(u.arow0 + r) * D + u.pn * 256 + cit; float g0[8], g1[8], m0[8], m1[8]; unpack8bf(p.g0, g0); unpack8bf(p.g1, g1); unpack8bf(p.m0, m0); unpack8bf(p.m1, m1);
; #pragma unroll
	v_and_b32_e32 v152, 0xffff0000, v152
	v_lshlrev_b32_e32 v209, 16, v153
	v_and_b32_e32 v153, 0xffff0000, v153
	v_lshlrev_b64 v[114:115], 12, v[114:115]
	v_lshlrev_b32_e32 v202, 16, v154
	v_and_b32_e32 v154, 0xffff0000, v154
	v_lshlrev_b32_e32 v205, 16, v157
	v_and_b32_e32 v157, 0xffff0000, v157
	v_lshlrev_b32_e32 v210, 16, v146
	v_and_b32_e32 v146, 0xffff0000, v146
	v_lshlrev_b32_e32 v213, 16, v149
	v_and_b32_e32 v149, 0xffff0000, v149
	v_fmac_f32_e32 v206, v126, v198
	v_fmac_f32_e32 v150, v127, v158
	v_fmac_f32_e32 v207, v128, v199
	v_fmac_f32_e32 v151, v129, v159
	v_fmac_f32_e32 v208, v122, v200
	v_fmac_f32_e32 v152, v123, v160
	v_fmac_f32_e32 v209, v124, v201
	v_fmac_f32_e32 v153, v125, v161
	v_lshl_add_u64 v[114:115], s[36:37], 0, v[114:115]
	v_lshlrev_b32_e32 v203, 16, v155
	v_and_b32_e32 v155, 0xffff0000, v155
	v_lshlrev_b32_e32 v211, 16, v147
	v_and_b32_e32 v147, 0xffff0000, v147
	v_fmac_f32_e32 v210, v118, v202
	v_fmac_f32_e32 v146, v119, v154
	v_fmac_f32_e32 v213, v116, v205
	v_fmac_f32_e32 v149, v117, v157
	v_lshl_add_u64 v[118:119], v[182:183], 1, v[114:115]
	v_cvt_pk_bf16_f32 v114, v206, v150
	v_cvt_pk_bf16_f32 v115, v207, v151
	v_cvt_pk_bf16_f32 v116, v208, v152
	v_cvt_pk_bf16_f32 v117, v209, v153
	v_fmac_f32_e32 v211, v120, v203
	v_fmac_f32_e32 v147, v121, v155
	global_store_dwordx4 v[118:119], v[114:117], off
	v_add_co_u32_e32 v118, vcc, 0x8000, v118
	s_nop 0
	v_cvt_pk_bf16_f32 v114, v210, v146
	v_cvt_pk_bf16_f32 v115, v211, v147
	v_cvt_pk_bf16_f32 v116, v212, v148
	v_cvt_pk_bf16_f32 v117, v213, v149
	v_addc_co_u32_e32 v119, vcc, 0, v119, vcc
	global_store_dwordx4 v[118:119], v[114:117], off
.LBB0_1154:
	s_nop 1
	v_add_u32_e32 v114, v197, v189
	v_ashrrev_i32_e32 v115, 31, v114
	v_lshlrev_b64 v[114:115], 11, v[114:115]
	v_lshl_add_u64 v[114:115], v[114:115], 0, v[182:183]
	v_lshlrev_b64 v[114:115], 1, v[114:115]
	v_lshl_add_u64 v[116:117], s[50:51], 0, v[114:115]
	v_add_co_u32_e32 v118, vcc, 0x8000, v116
	v_lshl_add_u64 v[114:115], s[20:21], 0, v[114:115]
	s_nop 0
	v_addc_co_u32_e32 v119, vcc, 0, v117, vcc
	global_load_dwordx4 v[126:129], v[116:117], off nt
	global_load_dwordx4 v[122:125], v[118:119], off nt
	v_add_co_u32_e32 v116, vcc, 0x8000, v114
	s_nop 1
	v_addc_co_u32_e32 v117, vcc, 0, v115, vcc
	global_load_dwordx4 v[118:121], v[114:115], off nt
	s_nop 0
	global_load_dwordx4 v[114:117], v[116:117], off nt
	s_nop 0
	v_cndmask_b32_e64 v146, 0, 1, s[16:17]
	v_cmp_ne_u32_e64 s[8:9], 1, v146
	s_andn2_b64 vcc, exec, s[16:17]
	s_cbranch_vccnz .LBB0_1156
	s_waitcnt vmcnt(14)
	v_cndmask_b32_e64 v146, v102, v110, s[0:1]
	v_mov_b32_e32 v147, 0
	v_lshlrev_b32_e32 v152, 16, v140
	v_lshlrev_b32_e32 v160, 16, v132
	v_mov_b32_dpp v147, v146 row_ror:8 row_mask:0xf bank_mask:0xf
	v_cndmask_b32_e64 v146, v103, v111, s[0:1]
	v_cndmask_b32_e64 v110, v110, v147, s[0:1]
	v_cndmask_b32_e64 v102, v147, v102, s[0:1]
	v_mov_b32_e32 v147, 0
	v_and_b32_e32 v140, 0xffff0000, v140
	v_and_b32_e32 v132, 0xffff0000, v132
	v_mov_b32_dpp v147, v146 row_ror:8 row_mask:0xf bank_mask:0xf
	v_cndmask_b32_e64 v146, v104, v112, s[0:1]
	v_cndmask_b32_e64 v111, v111, v147, s[0:1]
	v_cndmask_b32_e64 v103, v147, v103, s[0:1]
	v_mov_b32_e32 v147, 0
	v_lshlrev_b32_e32 v148, 16, v144
	v_and_b32_e32 v144, 0xffff0000, v144
	v_mov_b32_dpp v147, v146 row_ror:8 row_mask:0xf bank_mask:0xf
	v_cndmask_b32_e64 v146, v105, v113, s[0:1]
	v_cndmask_b32_e64 v112, v112, v147, s[0:1]
	v_cndmask_b32_e64 v104, v147, v104, s[0:1]
	v_mov_b32_e32 v147, 0
	v_lshlrev_b32_e32 v149, 16, v145
	v_and_b32_e32 v145, 0xffff0000, v145
	v_mov_b32_dpp v147, v146 row_ror:8 row_mask:0xf bank_mask:0xf
	v_cndmask_b32_e64 v146, v98, v106, s[0:1]
	v_cndmask_b32_e64 v113, v113, v147, s[0:1]
	v_cndmask_b32_e64 v105, v147, v105, s[0:1]
	v_mov_b32_e32 v147, 0
	v_lshlrev_b32_e32 v154, 16, v134
	v_and_b32_e32 v134, 0xffff0000, v134
	v_mov_b32_dpp v147, v146 row_ror:8 row_mask:0xf bank_mask:0xf
	v_cndmask_b32_e64 v146, v99, v107, s[0:1]
	v_cndmask_b32_e64 v106, v106, v147, s[0:1]
	v_cndmask_b32_e64 v98, v147, v98, s[0:1]
	v_mov_b32_e32 v147, 0
	v_fmac_f32_e32 v160, v98, v152
	v_add_u32_e32 v98, s64, v196
	v_mov_b32_dpp v147, v146 row_ror:8 row_mask:0xf bank_mask:0xf
	v_cndmask_b32_e64 v146, v100, v108, s[0:1]
	v_cndmask_b32_e64 v107, v107, v147, s[0:1]
	v_cndmask_b32_e64 v99, v147, v99, s[0:1]
	v_mov_b32_e32 v147, 0
	v_fmac_f32_e32 v132, v99, v140
	v_ashrrev_i32_e32 v99, 31, v98
	v_mov_b32_dpp v147, v146 row_ror:8 row_mask:0xf bank_mask:0xf
	v_cndmask_b32_e64 v146, v101, v109, s[0:1]
	v_cndmask_b32_e64 v108, v108, v147, s[0:1]
	v_cndmask_b32_e64 v100, v147, v100, s[0:1]
	v_mov_b32_e32 v147, 0
	v_lshlrev_b32_e32 v155, 16, v135
	v_and_b32_e32 v135, 0xffff0000, v135
	v_mov_b32_dpp v147, v146 row_ror:8 row_mask:0xf bank_mask:0xf
	v_cndmask_b32_e64 v109, v109, v147, s[0:1]
	v_cndmask_b32_e64 v101, v147, v101, s[0:1]
	v_lshlrev_b32_e32 v146, 16, v142
	v_and_b32_e32 v142, 0xffff0000, v142
	v_lshlrev_b32_e32 v147, 16, v143
	v_and_b32_e32 v143, 0xffff0000, v143
	v_lshlrev_b32_e32 v156, 16, v136
	v_and_b32_e32 v136, 0xffff0000, v136
	v_lshlrev_b32_e32 v157, 16, v137
	v_and_b32_e32 v137, 0xffff0000, v137
	v_lshlrev_b64 v[98:99], 12, v[98:99]
	v_lshlrev_b32_e32 v150, 16, v138
	v_and_b32_e32 v138, 0xffff0000, v138
	v_lshlrev_b32_e32 v153, 16, v141
	v_and_b32_e32 v141, 0xffff0000, v141
	v_lshlrev_b32_e32 v158, 16, v130
	v_and_b32_e32 v130, 0xffff0000, v130
	v_lshlrev_b32_e32 v161, 16, v133
	v_and_b32_e32 v133, 0xffff0000, v133
	v_fmac_f32_e32 v154, v110, v146
	v_fmac_f32_e32 v134, v111, v142
	v_fmac_f32_e32 v155, v112, v147
	v_fmac_f32_e32 v135, v113, v143
	v_fmac_f32_e32 v156, v106, v148
	v_fmac_f32_e32 v136, v107, v144
	v_fmac_f32_e32 v157, v108, v149
	v_fmac_f32_e32 v137, v109, v145
	v_lshl_add_u64 v[98:99], s[36:37], 0, v[98:99]
	v_lshlrev_b32_e32 v151, 16, v139
	v_and_b32_e32 v139, 0xffff0000, v139
	v_lshlrev_b32_e32 v159, 16, v131
	v_and_b32_e32 v131, 0xffff0000, v131
	v_fmac_f32_e32 v158, v102, v150
	v_fmac_f32_e32 v130, v103, v138
	v_fmac_f32_e32 v161, v100, v153
	v_fmac_f32_e32 v133, v101, v141
	v_lshl_add_u64 v[102:103], v[182:183], 1, v[98:99]
	v_cvt_pk_bf16_f32 v98, v154, v134
	v_cvt_pk_bf16_f32 v99, v155, v135
	v_cvt_pk_bf16_f32 v100, v156, v136
	v_cvt_pk_bf16_f32 v101, v157, v137
	v_fmac_f32_e32 v159, v104, v151
	v_fmac_f32_e32 v131, v105, v139
	global_store_dwordx4 v[102:103], v[98:101], off
	v_add_co_u32_e32 v102, vcc, 0x8000, v102
	s_nop 0
	v_cvt_pk_bf16_f32 v98, v158, v130
	v_cvt_pk_bf16_f32 v99, v159, v131
	v_cvt_pk_bf16_f32 v100, v160, v132
	v_cvt_pk_bf16_f32 v101, v161, v133
	v_addc_co_u32_e32 v103, vcc, 0, v103, vcc
	global_store_dwordx4 v[102:103], v[98:101], off
; template <class Epi, class Sched, bool GATHER, bool ALIGN_EPI = true, bool SP2 = true, bool REMAP64 = false>
; __device__ __forceinline__ void gemm_phase(LAS unsigned char* lds, const bf16* Ag, const bf16* Btg, const int K, const Sched& S, const Epi& E) {
;     ...
;             constexpr bool RP = REMAP64 && Epi::ROWPAIR;
;             const bool hi = RP && (fr >= 8); const int rsh = hi ? -8 : 0, citx = hi ? cit + 32 : cit;
;             typename Epi::Pre pq[2];
;             { const int r0_ = wr * 64 + fr; pq[0] = E.pre(cur, (r0_ < cur.nrows ? r0_ : cur.nrows - 1) + rsh, citx); }
; #pragma unroll
;             for (int gq = 0; gq < 8; ++gq) { const int ai = gq >> 2, m = gq & 3, r = ai * HALF + wr * 64 + m * 16 + fr;
;                 if (gq + 1 < 8) { const int rn = ((gq + 1) >> 2) * HALF + wr * 64 + ((gq + 1) & 3) * 16 + fr; pq[(gq + 1) & 1] = E.pre(cur, (rn < cur.nrows ? rn : cur.nrows - 1) + rsh, citx); }
;                 __builtin_amdgcn_sched_barrier(0);
;                 if (r < cur.nrows) { float v0[8], v1[8];
; #pragma unroll
;                     for (int i = 0; i < 4; ++i) { v0[i] = acc[ai][0][m][0][i]; v0[4 + i] = acc[ai][0][m][1][i]; v1[i] = acc[ai][1][m][0][i]; v1[4 + i] = acc[ai][1][m][1][i]; }
;                     if constexpr (RP) {
; #pragma unroll
;                         for (int i = 0; i < 8; ++i) { const float snd = hi ? v0[i] : v1[i];
;                             const float rcv = __builtin_bit_cast(float, __builtin_amdgcn_update_dpp(0, __builtin_bit_cast(int, snd), 0x128, 0xf, 0xf, false));
;                             if (hi) v0[i] = rcv; else v1[i] = rcv; } }
;                     E.post(cur, r + rsh, citx, v0, v1, pq[gq & 1]); }
;                 __builtin_amdgcn_sched_barrier(0); }
;     __device__ __forceinline__ Pre pre(const Unit& u, int r, int cit) const { const size_t off = (size_t)(u.arow0 + r) * D + u.pn * 256 + cit; return Pre{__builtin_nontemporal_load((const v4u*)(gd + off)), __builtin_nontemporal_load((const v4u*)(gd + off + (size_t)8 * D)), __builtin_nontemporal_load ...
;     __device__ __forceinline__ void post(const Unit& u, int r, int cit, const float* v0, const float* v1, const Pre& p) const {
;         const size_t off = (size_t)(u.arow0 + r) * D + u.pn * 256 + cit; float g0[8], g1[8], m0[8], m1[8]; unpack8bf(p.g0, g0); unpack8bf(p.g1, g1); unpack8bf(p.m0, m0); unpack8bf(p.m1, m1);
; #pragma unroll
.LBB0_1156:
	s_nop 1
	v_add_u32_e32 v98, v197, v190
	v_ashrrev_i32_e32 v99, 31, v98
	v_lshlrev_b64 v[98:99], 11, v[98:99]
	v_lshl_add_u64 v[98:99], v[98:99], 0, v[182:183]
	v_lshlrev_b64 v[98:99], 1, v[98:99]
	v_lshl_add_u64 v[100:101], s[50:51], 0, v[98:99]
	v_add_co_u32_e32 v102, vcc, 0x8000, v100
	v_lshl_add_u64 v[98:99], s[20:21], 0, v[98:99]
	s_nop 0
	v_addc_co_u32_e32 v103, vcc, 0, v101, vcc
	global_load_dwordx4 v[110:113], v[100:101], off nt
	global_load_dwordx4 v[106:109], v[102:103], off nt
	v_add_co_u32_e32 v100, vcc, 0x8000, v98
	s_nop 1
	v_addc_co_u32_e32 v101, vcc, 0, v99, vcc
	global_load_dwordx4 v[102:105], v[98:99], off nt
	s_nop 0
	global_load_dwordx4 v[98:101], v[100:101], off nt
	s_and_b64 vcc, exec, s[8:9]
	s_cbranch_vccnz .LBB0_1158
	s_waitcnt vmcnt(16)
	v_cndmask_b32_e64 v130, v86, v94, s[0:1]
	v_mov_b32_e32 v131, 0
	v_lshlrev_b32_e32 v136, 16, v224
	v_lshlrev_b32_e32 v144, 16, v216
	v_mov_b32_dpp v131, v130 row_ror:8 row_mask:0xf bank_mask:0xf
	v_cndmask_b32_e64 v130, v87, v95, s[0:1]
	v_cndmask_b32_e64 v94, v94, v131, s[0:1]
	v_cndmask_b32_e64 v86, v131, v86, s[0:1]
	v_mov_b32_e32 v131, 0
	v_and_b32_e32 v224, 0xffff0000, v224
	v_and_b32_e32 v216, 0xffff0000, v216
	v_mov_b32_dpp v131, v130 row_ror:8 row_mask:0xf bank_mask:0xf
	v_cndmask_b32_e64 v130, v88, v96, s[0:1]
	v_cndmask_b32_e64 v95, v95, v131, s[0:1]
	v_cndmask_b32_e64 v87, v131, v87, s[0:1]
	v_mov_b32_e32 v131, 0
	v_lshlrev_b32_e32 v132, 16, v228
	v_and_b32_e32 v228, 0xffff0000, v228
	v_mov_b32_dpp v131, v130 row_ror:8 row_mask:0xf bank_mask:0xf
	v_cndmask_b32_e64 v130, v89, v97, s[0:1]
	v_cndmask_b32_e64 v96, v96, v131, s[0:1]
	v_cndmask_b32_e64 v88, v131, v88, s[0:1]
	v_mov_b32_e32 v131, 0
	v_lshlrev_b32_e32 v133, 16, v229
	v_and_b32_e32 v229, 0xffff0000, v229
	v_mov_b32_dpp v131, v130 row_ror:8 row_mask:0xf bank_mask:0xf
	v_cndmask_b32_e64 v130, v82, v90, s[0:1]
	v_cndmask_b32_e64 v97, v97, v131, s[0:1]
	v_cndmask_b32_e64 v89, v131, v89, s[0:1]
	v_mov_b32_e32 v131, 0
	v_lshlrev_b32_e32 v138, 16, v218
	v_and_b32_e32 v218, 0xffff0000, v218
	v_mov_b32_dpp v131, v130 row_ror:8 row_mask:0xf bank_mask:0xf
	v_cndmask_b32_e64 v130, v83, v91, s[0:1]
	v_cndmask_b32_e64 v90, v90, v131, s[0:1]
	v_cndmask_b32_e64 v82, v131, v82, s[0:1]
	v_mov_b32_e32 v131, 0
	v_fmac_f32_e32 v144, v82, v136
	v_add_u32_e32 v82, s65, v196
	v_mov_b32_dpp v131, v130 row_ror:8 row_mask:0xf bank_mask:0xf
	v_cndmask_b32_e64 v130, v84, v92, s[0:1]
	v_cndmask_b32_e64 v91, v91, v131, s[0:1]
	v_cndmask_b32_e64 v83, v131, v83, s[0:1]
	v_mov_b32_e32 v131, 0
	v_fmac_f32_e32 v216, v83, v224
	v_ashrrev_i32_e32 v83, 31, v82
	v_mov_b32_dpp v131, v130 row_ror:8 row_mask:0xf bank_mask:0xf
	v_cndmask_b32_e64 v130, v85, v93, s[0:1]
	v_cndmask_b32_e64 v92, v92, v131, s[0:1]
	v_cndmask_b32_e64 v84, v131, v84, s[0:1]
	v_mov_b32_e32 v131, 0
	v_lshlrev_b32_e32 v139, 16, v219
	v_and_b32_e32 v219, 0xffff0000, v219
	v_mov_b32_dpp v131, v130 row_ror:8 row_mask:0xf bank_mask:0xf
	v_cndmask_b32_e64 v93, v93, v131, s[0:1]
	v_cndmask_b32_e64 v85, v131, v85, s[0:1]
	v_lshlrev_b32_e32 v130, 16, v226
	v_and_b32_e32 v226, 0xffff0000, v226
	v_lshlrev_b32_e32 v131, 16, v227
	v_and_b32_e32 v227, 0xffff0000, v227
	v_lshlrev_b32_e32 v140, 16, v220
	v_and_b32_e32 v220, 0xffff0000, v220
	v_lshlrev_b32_e32 v141, 16, v221
	v_and_b32_e32 v221, 0xffff0000, v221
	v_lshlrev_b64 v[82:83], 12, v[82:83]
	v_lshlrev_b32_e32 v134, 16, v222
	v_and_b32_e32 v222, 0xffff0000, v222
	v_lshlrev_b32_e32 v137, 16, v225
	v_and_b32_e32 v225, 0xffff0000, v225
	v_lshlrev_b32_e32 v142, 16, v214
	v_and_b32_e32 v214, 0xffff0000, v214
	v_lshlrev_b32_e32 v145, 16, v217
	v_and_b32_e32 v217, 0xffff0000, v217
	v_fmac_f32_e32 v138, v94, v130
	v_fmac_f32_e32 v218, v95, v226
	v_fmac_f32_e32 v139, v96, v131
	v_fmac_f32_e32 v219, v97, v227
	v_fmac_f32_e32 v140, v90, v132
	v_fmac_f32_e32 v220, v91, v228
	v_fmac_f32_e32 v141, v92, v133
	v_fmac_f32_e32 v221, v93, v229
	v_lshl_add_u64 v[82:83], s[36:37], 0, v[82:83]
	v_lshlrev_b32_e32 v135, 16, v223
	v_and_b32_e32 v223, 0xffff0000, v223
	v_lshlrev_b32_e32 v143, 16, v215
	v_and_b32_e32 v215, 0xffff0000, v215
	v_fmac_f32_e32 v142, v86, v134
	v_fmac_f32_e32 v214, v87, v222
	v_fmac_f32_e32 v145, v84, v137
	v_fmac_f32_e32 v217, v85, v225
	v_lshl_add_u64 v[86:87], v[182:183], 1, v[82:83]
	v_cvt_pk_bf16_f32 v82, v138, v218
	v_cvt_pk_bf16_f32 v83, v139, v219
	v_cvt_pk_bf16_f32 v84, v140, v220
	v_cvt_pk_bf16_f32 v85, v141, v221
	v_fmac_f32_e32 v143, v88, v135
	v_fmac_f32_e32 v215, v89, v223
	global_store_dwordx4 v[86:87], v[82:85], off
	v_add_co_u32_e32 v86, vcc, 0x8000, v86
	s_nop 0
	v_cvt_pk_bf16_f32 v82, v142, v214
	v_cvt_pk_bf16_f32 v83, v143, v215
	v_cvt_pk_bf16_f32 v84, v144, v216
	v_cvt_pk_bf16_f32 v85, v145, v217
	v_addc_co_u32_e32 v87, vcc, 0, v87, vcc
	global_store_dwordx4 v[86:87], v[82:85], off
; template <class Epi, class Sched, bool GATHER, bool ALIGN_EPI = true, bool SP2 = true, bool REMAP64 = false>
; __device__ __forceinline__ void gemm_phase(LAS unsigned char* lds, const bf16* Ag, const bf16* Btg, const int K, const Sched& S, const Epi& E) {
;     ...
;             constexpr bool RP = REMAP64 && Epi::ROWPAIR;
;             const bool hi = RP && (fr >= 8); const int rsh = hi ? -8 : 0, citx = hi ? cit + 32 : cit;
;             typename Epi::Pre pq[2];
;             { const int r0_ = wr * 64 + fr; pq[0] = E.pre(cur, (r0_ < cur.nrows ? r0_ : cur.nrows - 1) + rsh, citx); }
; #pragma unroll
;             for (int gq = 0; gq < 8; ++gq) { const int ai = gq >> 2, m = gq & 3, r = ai * HALF + wr * 64 + m * 16 + fr;
;                 if (gq + 1 < 8) { const int rn = ((gq + 1) >> 2) * HALF + wr * 64 + ((gq + 1) & 3) * 16 + fr; pq[(gq + 1) & 1] = E.pre(cur, (rn < cur.nrows ? rn : cur.nrows - 1) + rsh, citx); }
;                 __builtin_amdgcn_sched_barrier(0);
;                 if (r < cur.nrows) { float v0[8], v1[8];
; #pragma unroll
;                     for (int i = 0; i < 4; ++i) { v0[i] = acc[ai][0][m][0][i]; v0[4 + i] = acc[ai][0][m][1][i]; v1[i] = acc[ai][1][m][0][i]; v1[4 + i] = acc[ai][1][m][1][i]; }
;                     if constexpr (RP) {
; #pragma unroll
;                         for (int i = 0; i < 8; ++i) { const float snd = hi ? v0[i] : v1[i];
;                             const float rcv = __builtin_bit_cast(float, __builtin_amdgcn_update_dpp(0, __builtin_bit_cast(int, snd), 0x128, 0xf, 0xf, false));
;                             if (hi) v0[i] = rcv; else v1[i] = rcv; } }
;                     E.post(cur, r + rsh, citx, v0, v1, pq[gq & 1]); }
;                 __builtin_amdgcn_sched_barrier(0); }
;     __device__ __forceinline__ Pre pre(const Unit& u, int r, int cit) const { const size_t off = (size_t)(u.arow0 + r) * D + u.pn * 256 + cit; return Pre{__builtin_nontemporal_load((const v4u*)(gd + off)), __builtin_nontemporal_load((const v4u*)(gd + off + (size_t)8 * D)), __builtin_nontemporal_load ...
;     __device__ __forceinline__ void post(const Unit& u, int r, int cit, const float* v0, const float* v1, const Pre& p) const {
;         const size_t off = (size_t)(u.arow0 + r) * D + u.pn * 256 + cit; float g0[8], g1[8], m0[8], m1[8]; unpack8bf(p.g0, g0); unpack8bf(p.g1, g1); unpack8bf(p.m0, m0); unpack8bf(p.m1, m1);
; #pragma unroll
.LBB0_1158:
	s_nop 1
	v_add_u32_e32 v82, v197, v191
	v_ashrrev_i32_e32 v83, 31, v82
	v_lshlrev_b64 v[82:83], 11, v[82:83]
	v_lshl_add_u64 v[82:83], v[82:83], 0, v[182:183]
	v_lshlrev_b64 v[82:83], 1, v[82:83]
	v_lshl_add_u64 v[84:85], s[50:51], 0, v[82:83]
	v_add_co_u32_e32 v86, vcc, 0x8000, v84
	v_lshl_add_u64 v[82:83], s[20:21], 0, v[82:83]
	s_nop 0
	v_addc_co_u32_e32 v87, vcc, 0, v85, vcc
	global_load_dwordx4 v[94:97], v[84:85], off nt
	global_load_dwordx4 v[90:93], v[86:87], off nt
	v_add_co_u32_e32 v84, vcc, 0x8000, v82
	s_nop 1
	v_addc_co_u32_e32 v85, vcc, 0, v83, vcc
	global_load_dwordx4 v[86:89], v[82:83], off nt
	s_nop 0
	global_load_dwordx4 v[82:85], v[84:85], off nt
	s_and_b64 vcc, exec, s[8:9]
	s_cbranch_vccnz .LBB0_1160
	s_waitcnt vmcnt(18)
	v_cndmask_b32_e64 v146, v70, v78, s[0:1]
	v_mov_b32_e32 v147, 0
	s_nop 0
	v_lshlrev_b32_e32 v152, 16, v240
	s_nop 0
	v_lshlrev_b32_e32 v160, 16, v232
	v_mov_b32_dpp v147, v146 row_ror:8 row_mask:0xf bank_mask:0xf
	v_cndmask_b32_e64 v146, v71, v79, s[0:1]
	v_cndmask_b32_e64 v78, v78, v147, s[0:1]
	v_cndmask_b32_e64 v70, v147, v70, s[0:1]
	v_mov_b32_e32 v147, 0
	v_and_b32_e32 v240, 0xffff0000, v240
	v_and_b32_e32 v232, 0xffff0000, v232
	v_mov_b32_dpp v147, v146 row_ror:8 row_mask:0xf bank_mask:0xf
	v_cndmask_b32_e64 v146, v72, v80, s[0:1]
	v_cndmask_b32_e64 v79, v79, v147, s[0:1]
	v_cndmask_b32_e64 v71, v147, v71, s[0:1]
	v_mov_b32_e32 v147, 0
	v_lshlrev_b32_e32 v148, 16, v244
	v_and_b32_e32 v244, 0xffff0000, v244
	v_mov_b32_dpp v147, v146 row_ror:8 row_mask:0xf bank_mask:0xf
	v_cndmask_b32_e64 v146, v73, v81, s[0:1]
	v_cndmask_b32_e64 v80, v80, v147, s[0:1]
	v_cndmask_b32_e64 v72, v147, v72, s[0:1]
	v_mov_b32_e32 v147, 0
	v_lshlrev_b32_e32 v149, 16, v245
	v_and_b32_e32 v245, 0xffff0000, v245
	v_mov_b32_dpp v147, v146 row_ror:8 row_mask:0xf bank_mask:0xf
	v_cndmask_b32_e64 v146, v66, v74, s[0:1]
	v_cndmask_b32_e64 v81, v81, v147, s[0:1]
	v_cndmask_b32_e64 v73, v147, v73, s[0:1]
	v_mov_b32_e32 v147, 0
	v_lshlrev_b32_e32 v154, 16, v234
	v_and_b32_e32 v234, 0xffff0000, v234
	v_mov_b32_dpp v147, v146 row_ror:8 row_mask:0xf bank_mask:0xf
	v_cndmask_b32_e64 v146, v67, v75, s[0:1]
	v_cndmask_b32_e64 v74, v74, v147, s[0:1]
	v_cndmask_b32_e64 v66, v147, v66, s[0:1]
	v_mov_b32_e32 v147, 0
	v_fmac_f32_e32 v160, v66, v152
	v_add_u32_e32 v66, s71, v196
	v_mov_b32_dpp v147, v146 row_ror:8 row_mask:0xf bank_mask:0xf
	v_cndmask_b32_e64 v146, v68, v76, s[0:1]
	v_cndmask_b32_e64 v75, v75, v147, s[0:1]
	v_cndmask_b32_e64 v67, v147, v67, s[0:1]
	v_mov_b32_e32 v147, 0
	v_fmac_f32_e32 v232, v67, v240
	v_ashrrev_i32_e32 v67, 31, v66
	v_mov_b32_dpp v147, v146 row_ror:8 row_mask:0xf bank_mask:0xf
	v_cndmask_b32_e64 v146, v69, v77, s[0:1]
	v_cndmask_b32_e64 v76, v76, v147, s[0:1]
	v_cndmask_b32_e64 v68, v147, v68, s[0:1]
	v_mov_b32_e32 v147, 0
	v_lshlrev_b32_e32 v155, 16, v235
	v_and_b32_e32 v235, 0xffff0000, v235
	v_mov_b32_dpp v147, v146 row_ror:8 row_mask:0xf bank_mask:0xf
	v_cndmask_b32_e64 v77, v77, v147, s[0:1]
	v_cndmask_b32_e64 v69, v147, v69, s[0:1]
	v_lshlrev_b32_e32 v146, 16, v242
	v_and_b32_e32 v242, 0xffff0000, v242
	v_lshlrev_b32_e32 v147, 16, v243
	v_and_b32_e32 v243, 0xffff0000, v243
	v_lshlrev_b32_e32 v156, 16, v236
	v_and_b32_e32 v236, 0xffff0000, v236
	v_lshlrev_b32_e32 v157, 16, v237
	v_and_b32_e32 v237, 0xffff0000, v237
	v_lshlrev_b64 v[66:67], 12, v[66:67]
	v_lshlrev_b32_e32 v150, 16, v238
	v_and_b32_e32 v238, 0xffff0000, v238
	v_lshlrev_b32_e32 v153, 16, v241
	v_and_b32_e32 v241, 0xffff0000, v241
	v_lshlrev_b32_e32 v158, 16, v230
	v_and_b32_e32 v230, 0xffff0000, v230
	v_lshlrev_b32_e32 v161, 16, v233
	v_and_b32_e32 v233, 0xffff0000, v233
	v_fmac_f32_e32 v154, v78, v146
	v_fmac_f32_e32 v234, v79, v242
	v_fmac_f32_e32 v155, v80, v147
	v_fmac_f32_e32 v235, v81, v243
	v_fmac_f32_e32 v156, v74, v148
	v_fmac_f32_e32 v236, v75, v244
	v_fmac_f32_e32 v157, v76, v149
	v_fmac_f32_e32 v237, v77, v245
	v_lshl_add_u64 v[66:67], s[36:37], 0, v[66:67]
	v_lshlrev_b32_e32 v151, 16, v239
	v_and_b32_e32 v239, 0xffff0000, v239
	v_lshlrev_b32_e32 v159, 16, v231
	v_and_b32_e32 v231, 0xffff0000, v231
	v_fmac_f32_e32 v158, v70, v150
	v_fmac_f32_e32 v230, v71, v238
	v_fmac_f32_e32 v161, v68, v153
	v_fmac_f32_e32 v233, v69, v241
	v_lshl_add_u64 v[70:71], v[182:183], 1, v[66:67]
	v_cvt_pk_bf16_f32 v66, v154, v234
	v_cvt_pk_bf16_f32 v67, v155, v235
	v_cvt_pk_bf16_f32 v68, v156, v236
	v_cvt_pk_bf16_f32 v69, v157, v237
	v_fmac_f32_e32 v159, v72, v151
	v_fmac_f32_e32 v231, v73, v239
	global_store_dwordx4 v[70:71], v[66:69], off
	v_add_co_u32_e32 v70, vcc, 0x8000, v70
	s_nop 0
	v_cvt_pk_bf16_f32 v66, v158, v230
	v_cvt_pk_bf16_f32 v67, v159, v231
	v_cvt_pk_bf16_f32 v68, v160, v232
	v_cvt_pk_bf16_f32 v69, v161, v233
	v_addc_co_u32_e32 v71, vcc, 0, v71, vcc
	global_store_dwordx4 v[70:71], v[66:69], off
; template <class Epi, class Sched, bool GATHER, bool ALIGN_EPI = true, bool SP2 = true, bool REMAP64 = false>
; __device__ __forceinline__ void gemm_phase(LAS unsigned char* lds, const bf16* Ag, const bf16* Btg, const int K, const Sched& S, const Epi& E) {
;     ...
;             constexpr bool RP = REMAP64 && Epi::ROWPAIR;
;             const bool hi = RP && (fr >= 8); const int rsh = hi ? -8 : 0, citx = hi ? cit + 32 : cit;
;             typename Epi::Pre pq[2];
;             { const int r0_ = wr * 64 + fr; pq[0] = E.pre(cur, (r0_ < cur.nrows ? r0_ : cur.nrows - 1) + rsh, citx); }
; #pragma unroll
;             for (int gq = 0; gq < 8; ++gq) { const int ai = gq >> 2, m = gq & 3, r = ai * HALF + wr * 64 + m * 16 + fr;
;                 if (gq + 1 < 8) { const int rn = ((gq + 1) >> 2) * HALF + wr * 64 + ((gq + 1) & 3) * 16 + fr; pq[(gq + 1) & 1] = E.pre(cur, (rn < cur.nrows ? rn : cur.nrows - 1) + rsh, citx); }
;                 __builtin_amdgcn_sched_barrier(0);
;                 if (r < cur.nrows) { float v0[8], v1[8];
; #pragma unroll
;                     for (int i = 0; i < 4; ++i) { v0[i] = acc[ai][0][m][0][i]; v0[4 + i] = acc[ai][0][m][1][i]; v1[i] = acc[ai][1][m][0][i]; v1[4 + i] = acc[ai][1][m][1][i]; }
;                     if constexpr (RP) {
; #pragma unroll
;                         for (int i = 0; i < 8; ++i) { const float snd = hi ? v0[i] : v1[i];
;                             const float rcv = __builtin_bit_cast(float, __builtin_amdgcn_update_dpp(0, __builtin_bit_cast(int, snd), 0x128, 0xf, 0xf, false));
;                             if (hi) v0[i] = rcv; else v1[i] = rcv; } }
;                     E.post(cur, r + rsh, citx, v0, v1, pq[gq & 1]); }
;                 __builtin_amdgcn_sched_barrier(0); }
;     __device__ __forceinline__ Pre pre(const Unit& u, int r, int cit) const { const size_t off = (size_t)(u.arow0 + r) * D + u.pn * 256 + cit; return Pre{__builtin_nontemporal_load((const v4u*)(gd + off)), __builtin_nontemporal_load((const v4u*)(gd + off + (size_t)8 * D)), __builtin_nontemporal_load ...
;     __device__ __forceinline__ void post(const Unit& u, int r, int cit, const float* v0, const float* v1, const Pre& p) const {
;         const size_t off = (size_t)(u.arow0 + r) * D + u.pn * 256 + cit; float g0[8], g1[8], m0[8], m1[8]; unpack8bf(p.g0, g0); unpack8bf(p.g1, g1); unpack8bf(p.m0, m0); unpack8bf(p.m1, m1);
; #pragma unroll
.LBB0_1160:
	s_nop 1
	v_add_u32_e32 v66, v197, v192
	v_ashrrev_i32_e32 v67, 31, v66
	v_lshlrev_b64 v[66:67], 11, v[66:67]
	v_lshl_add_u64 v[66:67], v[66:67], 0, v[182:183]
	v_lshlrev_b64 v[66:67], 1, v[66:67]
	v_lshl_add_u64 v[68:69], s[50:51], 0, v[66:67]
	v_add_co_u32_e32 v70, vcc, 0x8000, v68
	v_lshl_add_u64 v[66:67], s[20:21], 0, v[66:67]
	s_nop 0
	v_addc_co_u32_e32 v71, vcc, 0, v69, vcc
	global_load_dwordx4 v[78:81], v[68:69], off nt
	global_load_dwordx4 v[74:77], v[70:71], off nt
	v_add_co_u32_e32 v68, vcc, 0x8000, v66
	s_nop 1
	v_addc_co_u32_e32 v69, vcc, 0, v67, vcc
	global_load_dwordx4 v[70:73], v[66:67], off nt
	s_nop 0
	global_load_dwordx4 v[66:69], v[68:69], off nt
	s_nop 0
	v_cndmask_b32_e64 v146, 0, 1, s[18:19]
	v_cmp_ne_u32_e64 s[8:9], 1, v146
	s_andn2_b64 vcc, exec, s[18:19]
	s_cbranch_vccnz .LBB0_1162
	s_waitcnt vmcnt(18)
	v_cndmask_b32_e64 v130, v54, v62, s[0:1]
	v_mov_b32_e32 v131, 0
	s_nop 0
	v_lshlrev_b32_e32 v136, 16, v124
	s_nop 0
	v_lshlrev_b32_e32 v144, 16, v116
	v_mov_b32_dpp v131, v130 row_ror:8 row_mask:0xf bank_mask:0xf
	v_cndmask_b32_e64 v130, v55, v63, s[0:1]
	v_cndmask_b32_e64 v62, v62, v131, s[0:1]
	v_cndmask_b32_e64 v54, v131, v54, s[0:1]
	v_mov_b32_e32 v131, 0
	v_and_b32_e32 v124, 0xffff0000, v124
	v_and_b32_e32 v116, 0xffff0000, v116
	v_mov_b32_dpp v131, v130 row_ror:8 row_mask:0xf bank_mask:0xf
	v_cndmask_b32_e64 v130, v56, v64, s[0:1]
	v_cndmask_b32_e64 v63, v63, v131, s[0:1]
	v_cndmask_b32_e64 v55, v131, v55, s[0:1]
	v_mov_b32_e32 v131, 0
	v_lshlrev_b32_e32 v132, 16, v128
	v_and_b32_e32 v128, 0xffff0000, v128
	v_mov_b32_dpp v131, v130 row_ror:8 row_mask:0xf bank_mask:0xf
	v_cndmask_b32_e64 v130, v57, v65, s[0:1]
	v_cndmask_b32_e64 v64, v64, v131, s[0:1]
	v_cndmask_b32_e64 v56, v131, v56, s[0:1]
	v_mov_b32_e32 v131, 0
	v_lshlrev_b32_e32 v133, 16, v129
	v_and_b32_e32 v129, 0xffff0000, v129
	v_mov_b32_dpp v131, v130 row_ror:8 row_mask:0xf bank_mask:0xf
	v_cndmask_b32_e64 v130, v50, v58, s[0:1]
	v_cndmask_b32_e64 v65, v65, v131, s[0:1]
	v_cndmask_b32_e64 v57, v131, v57, s[0:1]
	v_mov_b32_e32 v131, 0
	v_lshlrev_b32_e32 v138, 16, v118
	v_and_b32_e32 v118, 0xffff0000, v118
	v_mov_b32_dpp v131, v130 row_ror:8 row_mask:0xf bank_mask:0xf
	v_cndmask_b32_e64 v130, v51, v59, s[0:1]
	v_cndmask_b32_e64 v58, v58, v131, s[0:1]
	v_cndmask_b32_e64 v50, v131, v50, s[0:1]
	v_mov_b32_e32 v131, 0
	v_fmac_f32_e32 v144, v50, v136
	v_add_u32_e32 v50, s70, v196
	v_mov_b32_dpp v131, v130 row_ror:8 row_mask:0xf bank_mask:0xf
	v_cndmask_b32_e64 v130, v52, v60, s[0:1]
	v_cndmask_b32_e64 v59, v59, v131, s[0:1]
	v_cndmask_b32_e64 v51, v131, v51, s[0:1]
	v_mov_b32_e32 v131, 0
	v_fmac_f32_e32 v116, v51, v124
	v_ashrrev_i32_e32 v51, 31, v50
	v_mov_b32_dpp v131, v130 row_ror:8 row_mask:0xf bank_mask:0xf
	v_cndmask_b32_e64 v130, v53, v61, s[0:1]
	v_cndmask_b32_e64 v60, v60, v131, s[0:1]
	v_cndmask_b32_e64 v52, v131, v52, s[0:1]
	v_mov_b32_e32 v131, 0
	v_lshlrev_b32_e32 v139, 16, v119
	v_and_b32_e32 v119, 0xffff0000, v119
	v_mov_b32_dpp v131, v130 row_ror:8 row_mask:0xf bank_mask:0xf
	v_cndmask_b32_e64 v61, v61, v131, s[0:1]
	v_cndmask_b32_e64 v53, v131, v53, s[0:1]
	v_lshlrev_b32_e32 v130, 16, v126
	v_and_b32_e32 v126, 0xffff0000, v126
	v_lshlrev_b32_e32 v131, 16, v127
	v_and_b32_e32 v127, 0xffff0000, v127
	v_lshlrev_b32_e32 v140, 16, v120
	v_and_b32_e32 v120, 0xffff0000, v120
	v_lshlrev_b32_e32 v141, 16, v121
	v_and_b32_e32 v121, 0xffff0000, v121
	v_lshlrev_b64 v[50:51], 12, v[50:51]
	v_lshlrev_b32_e32 v134, 16, v122
	v_and_b32_e32 v122, 0xffff0000, v122
	v_lshlrev_b32_e32 v137, 16, v125
	v_and_b32_e32 v125, 0xffff0000, v125
	v_lshlrev_b32_e32 v142, 16, v114
	v_and_b32_e32 v114, 0xffff0000, v114
	v_lshlrev_b32_e32 v145, 16, v117
	v_and_b32_e32 v117, 0xffff0000, v117
	v_fmac_f32_e32 v138, v62, v130
	v_fmac_f32_e32 v118, v63, v126
	v_fmac_f32_e32 v139, v64, v131
	v_fmac_f32_e32 v119, v65, v127
	v_fmac_f32_e32 v140, v58, v132
	v_fmac_f32_e32 v120, v59, v128
	v_fmac_f32_e32 v141, v60, v133
	v_fmac_f32_e32 v121, v61, v129
	v_lshl_add_u64 v[50:51], s[36:37], 0, v[50:51]
	v_lshlrev_b32_e32 v135, 16, v123
	v_and_b32_e32 v123, 0xffff0000, v123
	v_lshlrev_b32_e32 v143, 16, v115
	v_and_b32_e32 v115, 0xffff0000, v115
	v_fmac_f32_e32 v142, v54, v134
	v_fmac_f32_e32 v114, v55, v122
	v_fmac_f32_e32 v145, v52, v137
	v_fmac_f32_e32 v117, v53, v125
	v_lshl_add_u64 v[54:55], v[182:183], 1, v[50:51]
	v_cvt_pk_bf16_f32 v50, v138, v118
	v_cvt_pk_bf16_f32 v51, v139, v119
	v_cvt_pk_bf16_f32 v52, v140, v120
	v_cvt_pk_bf16_f32 v53, v141, v121
	v_fmac_f32_e32 v143, v56, v135
	v_fmac_f32_e32 v115, v57, v123
	global_store_dwordx4 v[54:55], v[50:53], off
	v_add_co_u32_e32 v54, vcc, 0x8000, v54
	s_nop 0
	v_cvt_pk_bf16_f32 v50, v142, v114
	v_cvt_pk_bf16_f32 v51, v143, v115
	v_cvt_pk_bf16_f32 v52, v144, v116
	v_cvt_pk_bf16_f32 v53, v145, v117
	v_addc_co_u32_e32 v55, vcc, 0, v55, vcc
	global_store_dwordx4 v[54:55], v[50:53], off
; template <class Epi, class Sched, bool GATHER, bool ALIGN_EPI = true, bool SP2 = true, bool REMAP64 = false>
; __device__ __forceinline__ void gemm_phase(LAS unsigned char* lds, const bf16* Ag, const bf16* Btg, const int K, const Sched& S, const Epi& E) {
;     ...
;             constexpr bool RP = REMAP64 && Epi::ROWPAIR;
;             const bool hi = RP && (fr >= 8); const int rsh = hi ? -8 : 0, citx = hi ? cit + 32 : cit;
;             typename Epi::Pre pq[2];
;             { const int r0_ = wr * 64 + fr; pq[0] = E.pre(cur, (r0_ < cur.nrows ? r0_ : cur.nrows - 1) + rsh, citx); }
; #pragma unroll
;             for (int gq = 0; gq < 8; ++gq) { const int ai = gq >> 2, m = gq & 3, r = ai * HALF + wr * 64 + m * 16 + fr;
;                 if (gq + 1 < 8) { const int rn = ((gq + 1) >> 2) * HALF + wr * 64 + ((gq + 1) & 3) * 16 + fr; pq[(gq + 1) & 1] = E.pre(cur, (rn < cur.nrows ? rn : cur.nrows - 1) + rsh, citx); }
;                 __builtin_amdgcn_sched_barrier(0);
;                 if (r < cur.nrows) { float v0[8], v1[8];
; #pragma unroll
;                     for (int i = 0; i < 4; ++i) { v0[i] = acc[ai][0][m][0][i]; v0[4 + i] = acc[ai][0][m][1][i]; v1[i] = acc[ai][1][m][0][i]; v1[4 + i] = acc[ai][1][m][1][i]; }
;                     if constexpr (RP) {
; #pragma unroll
;                         for (int i = 0; i < 8; ++i) { const float snd = hi ? v0[i] : v1[i];
;                             const float rcv = __builtin_bit_cast(float, __builtin_amdgcn_update_dpp(0, __builtin_bit_cast(int, snd), 0x128, 0xf, 0xf, false));
;                             if (hi) v0[i] = rcv; else v1[i] = rcv; } }
;                     E.post(cur, r + rsh, citx, v0, v1, pq[gq & 1]); }
;                 __builtin_amdgcn_sched_barrier(0); }
;     __device__ __forceinline__ Pre pre(const Unit& u, int r, int cit) const { const size_t off = (size_t)(u.arow0 + r) * D + u.pn * 256 + cit; return Pre{__builtin_nontemporal_load((const v4u*)(gd + off)), __builtin_nontemporal_load((const v4u*)(gd + off + (size_t)8 * D)), __builtin_nontemporal_load ...
;     __device__ __forceinline__ void post(const Unit& u, int r, int cit, const float* v0, const float* v1, const Pre& p) const {
;         const size_t off = (size_t)(u.arow0 + r) * D + u.pn * 256 + cit; float g0[8], g1[8], m0[8], m1[8]; unpack8bf(p.g0, g0); unpack8bf(p.g1, g1); unpack8bf(p.m0, m0); unpack8bf(p.m1, m1);
; #pragma unroll
.LBB0_1162:
	s_and_b64 vcc, exec, s[8:9]
	s_cbranch_vccnz .LBB0_1164
	s_waitcnt vmcnt(14)
	s_nop 0
	v_cndmask_b32_e64 v146, v38, v46, s[0:1]
	v_mov_b32_e32 v147, 0
	s_nop 0
	v_lshlrev_b32_e32 v152, 16, v108
	s_nop 0
	v_lshlrev_b32_e32 v160, 16, v100
	v_mov_b32_dpp v147, v146 row_ror:8 row_mask:0xf bank_mask:0xf
	v_cndmask_b32_e64 v146, v39, v47, s[0:1]
	v_cndmask_b32_e64 v46, v46, v147, s[0:1]
	v_cndmask_b32_e64 v38, v147, v38, s[0:1]
	v_mov_b32_e32 v147, 0
	v_and_b32_e32 v108, 0xffff0000, v108
	v_and_b32_e32 v100, 0xffff0000, v100
	v_mov_b32_dpp v147, v146 row_ror:8 row_mask:0xf bank_mask:0xf
	v_cndmask_b32_e64 v146, v40, v48, s[0:1]
	v_cndmask_b32_e64 v47, v47, v147, s[0:1]
	v_cndmask_b32_e64 v39, v147, v39, s[0:1]
	v_mov_b32_e32 v147, 0
	v_lshlrev_b32_e32 v148, 16, v112
	v_and_b32_e32 v112, 0xffff0000, v112
	v_mov_b32_dpp v147, v146 row_ror:8 row_mask:0xf bank_mask:0xf
	v_cndmask_b32_e64 v146, v41, v49, s[0:1]
	v_cndmask_b32_e64 v48, v48, v147, s[0:1]
	v_cndmask_b32_e64 v40, v147, v40, s[0:1]
	v_mov_b32_e32 v147, 0
	v_lshlrev_b32_e32 v149, 16, v113
	v_and_b32_e32 v113, 0xffff0000, v113
	v_mov_b32_dpp v147, v146 row_ror:8 row_mask:0xf bank_mask:0xf
	v_cndmask_b32_e64 v146, v34, v42, s[0:1]
	v_cndmask_b32_e64 v49, v49, v147, s[0:1]
	v_cndmask_b32_e64 v41, v147, v41, s[0:1]
	v_mov_b32_e32 v147, 0
	v_lshlrev_b32_e32 v154, 16, v102
	v_and_b32_e32 v102, 0xffff0000, v102
	v_mov_b32_dpp v147, v146 row_ror:8 row_mask:0xf bank_mask:0xf
	v_cndmask_b32_e64 v146, v35, v43, s[0:1]
	v_cndmask_b32_e64 v42, v42, v147, s[0:1]
	v_cndmask_b32_e64 v34, v147, v34, s[0:1]
	v_mov_b32_e32 v147, 0
	v_fmac_f32_e32 v160, v34, v152
	v_add_u32_e32 v34, s72, v196
	v_mov_b32_dpp v147, v146 row_ror:8 row_mask:0xf bank_mask:0xf
	v_cndmask_b32_e64 v146, v36, v44, s[0:1]
	v_cndmask_b32_e64 v43, v43, v147, s[0:1]
	v_cndmask_b32_e64 v35, v147, v35, s[0:1]
	v_mov_b32_e32 v147, 0
	v_fmac_f32_e32 v100, v35, v108
	v_ashrrev_i32_e32 v35, 31, v34
	v_mov_b32_dpp v147, v146 row_ror:8 row_mask:0xf bank_mask:0xf
	v_cndmask_b32_e64 v146, v37, v45, s[0:1]
	v_cndmask_b32_e64 v44, v44, v147, s[0:1]
	v_cndmask_b32_e64 v36, v147, v36, s[0:1]
	v_mov_b32_e32 v147, 0
	v_lshlrev_b32_e32 v155, 16, v103
	v_and_b32_e32 v103, 0xffff0000, v103
	v_mov_b32_dpp v147, v146 row_ror:8 row_mask:0xf bank_mask:0xf
	v_cndmask_b32_e64 v45, v45, v147, s[0:1]
	v_cndmask_b32_e64 v37, v147, v37, s[0:1]
	v_lshlrev_b32_e32 v146, 16, v110
	v_and_b32_e32 v110, 0xffff0000, v110
	v_lshlrev_b32_e32 v147, 16, v111
	v_and_b32_e32 v111, 0xffff0000, v111
	v_lshlrev_b32_e32 v156, 16, v104
	v_and_b32_e32 v104, 0xffff0000, v104
	v_lshlrev_b32_e32 v157, 16, v105
	v_and_b32_e32 v105, 0xffff0000, v105
	v_lshlrev_b64 v[34:35], 12, v[34:35]
	v_lshlrev_b32_e32 v150, 16, v106
	v_and_b32_e32 v106, 0xffff0000, v106
	v_lshlrev_b32_e32 v153, 16, v109
	v_and_b32_e32 v109, 0xffff0000, v109
	v_lshlrev_b32_e32 v158, 16, v98
	v_and_b32_e32 v98, 0xffff0000, v98
	v_lshlrev_b32_e32 v161, 16, v101
	v_and_b32_e32 v101, 0xffff0000, v101
	v_fmac_f32_e32 v154, v46, v146
	v_fmac_f32_e32 v102, v47, v110
	v_fmac_f32_e32 v155, v48, v147
	v_fmac_f32_e32 v103, v49, v111
	v_fmac_f32_e32 v156, v42, v148
	v_fmac_f32_e32 v104, v43, v112
	v_fmac_f32_e32 v157, v44, v149
	v_fmac_f32_e32 v105, v45, v113
	v_lshl_add_u64 v[34:35], s[36:37], 0, v[34:35]
	v_lshlrev_b32_e32 v151, 16, v107
	v_and_b32_e32 v107, 0xffff0000, v107
	v_lshlrev_b32_e32 v159, 16, v99
	v_and_b32_e32 v99, 0xffff0000, v99
	v_fmac_f32_e32 v158, v38, v150
	v_fmac_f32_e32 v98, v39, v106
	v_fmac_f32_e32 v161, v36, v153
	v_fmac_f32_e32 v101, v37, v109
	v_lshl_add_u64 v[38:39], v[182:183], 1, v[34:35]
	v_cvt_pk_bf16_f32 v34, v154, v102
	v_cvt_pk_bf16_f32 v35, v155, v103
	v_cvt_pk_bf16_f32 v36, v156, v104
	v_cvt_pk_bf16_f32 v37, v157, v105
	v_fmac_f32_e32 v159, v40, v151
	v_fmac_f32_e32 v99, v41, v107
	global_store_dwordx4 v[38:39], v[34:37], off
	v_add_co_u32_e32 v38, vcc, 0x8000, v38
	s_nop 0
	v_cvt_pk_bf16_f32 v34, v158, v98
	v_cvt_pk_bf16_f32 v35, v159, v99
	v_cvt_pk_bf16_f32 v36, v160, v100
	v_cvt_pk_bf16_f32 v37, v161, v101
	v_addc_co_u32_e32 v39, vcc, 0, v39, vcc
	global_store_dwordx4 v[38:39], v[34:37], off
.LBB0_1164:
	s_and_b64 vcc, exec, s[8:9]
	s_cbranch_vccnz .LBB0_1166
	s_waitcnt vmcnt(10)
	s_nop 0
	v_cndmask_b32_e64 v130, v22, v30, s[0:1]
	v_mov_b32_e32 v131, 0
	s_nop 0
	v_lshlrev_b32_e32 v136, 16, v92
	s_nop 0
	v_lshlrev_b32_e32 v144, 16, v84
	v_mov_b32_dpp v131, v130 row_ror:8 row_mask:0xf bank_mask:0xf
	v_cndmask_b32_e64 v130, v23, v31, s[0:1]
	v_cndmask_b32_e64 v30, v30, v131, s[0:1]
	v_cndmask_b32_e64 v22, v131, v22, s[0:1]
	v_mov_b32_e32 v131, 0
	v_and_b32_e32 v92, 0xffff0000, v92
	v_and_b32_e32 v84, 0xffff0000, v84
	v_mov_b32_dpp v131, v130 row_ror:8 row_mask:0xf bank_mask:0xf
	v_cndmask_b32_e64 v130, v24, v32, s[0:1]
	v_cndmask_b32_e64 v31, v31, v131, s[0:1]
	v_cndmask_b32_e64 v23, v131, v23, s[0:1]
	v_mov_b32_e32 v131, 0
	v_lshlrev_b32_e32 v132, 16, v96
	v_and_b32_e32 v96, 0xffff0000, v96
	v_mov_b32_dpp v131, v130 row_ror:8 row_mask:0xf bank_mask:0xf
	v_cndmask_b32_e64 v130, v25, v33, s[0:1]
	v_cndmask_b32_e64 v32, v32, v131, s[0:1]
	v_cndmask_b32_e64 v24, v131, v24, s[0:1]
	v_mov_b32_e32 v131, 0
	v_lshlrev_b32_e32 v133, 16, v97
	v_and_b32_e32 v97, 0xffff0000, v97
	v_mov_b32_dpp v131, v130 row_ror:8 row_mask:0xf bank_mask:0xf
	v_cndmask_b32_e64 v130, v18, v26, s[0:1]
	v_cndmask_b32_e64 v33, v33, v131, s[0:1]
	v_cndmask_b32_e64 v25, v131, v25, s[0:1]
	v_mov_b32_e32 v131, 0
	v_lshlrev_b32_e32 v138, 16, v86
	v_and_b32_e32 v86, 0xffff0000, v86
	v_mov_b32_dpp v131, v130 row_ror:8 row_mask:0xf bank_mask:0xf
	v_cndmask_b32_e64 v130, v19, v27, s[0:1]
	v_cndmask_b32_e64 v26, v26, v131, s[0:1]
; template <class Epi, class Sched, bool GATHER, bool ALIGN_EPI = true, bool SP2 = true, bool REMAP64 = false>
; __device__ __forceinline__ void gemm_phase(LAS unsigned char* lds, const bf16* Ag, const bf16* Btg, const int K, const Sched& S, const Epi& E) {
;     ...
;             constexpr bool RP = REMAP64 && Epi::ROWPAIR;
;             const bool hi = RP && (fr >= 8); const int rsh = hi ? -8 : 0, citx = hi ? cit + 32 : cit;
;             typename Epi::Pre pq[2];
;             { const int r0_ = wr * 64 + fr; pq[0] = E.pre(cur, (r0_ < cur.nrows ? r0_ : cur.nrows - 1) + rsh, citx); }
; #pragma unroll
;             for (int gq = 0; gq < 8; ++gq) { const int ai = gq >> 2, m = gq & 3, r = ai * HALF + wr * 64 + m * 16 + fr;
;                 if (gq + 1 < 8) { const int rn = ((gq + 1) >> 2) * HALF + wr * 64 + ((gq + 1) & 3) * 16 + fr; pq[(gq + 1) & 1] = E.pre(cur, (rn < cur.nrows ? rn : cur.nrows - 1) + rsh, citx); }
;                 __builtin_amdgcn_sched_barrier(0);
;                 if (r < cur.nrows) { float v0[8], v1[8];
; #pragma unroll
;                     for (int i = 0; i < 4; ++i) { v0[i] = acc[ai][0][m][0][i]; v0[4 + i] = acc[ai][0][m][1][i]; v1[i] = acc[ai][1][m][0][i]; v1[4 + i] = acc[ai][1][m][1][i]; }
;                     if constexpr (RP) {
; #pragma unroll
;                         for (int i = 0; i < 8; ++i) { const float snd = hi ? v0[i] : v1[i];
;                             const float rcv = __builtin_bit_cast(float, __builtin_amdgcn_update_dpp(0, __builtin_bit_cast(int, snd), 0x128, 0xf, 0xf, false));
;                             if (hi) v0[i] = rcv; else v1[i] = rcv; } }
;                     E.post(cur, r + rsh, citx, v0, v1, pq[gq & 1]); }
;                 __builtin_amdgcn_sched_barrier(0); }
;     __device__ __forceinline__ Pre pre(const Unit& u, int r, int cit) const { const size_t off = (size_t)(u.arow0 + r) * D + u.pn * 256 + cit; return Pre{__builtin_nontemporal_load((const v4u*)(gd + off)), __builtin_nontemporal_load((const v4u*)(gd + off + (size_t)8 * D)), __builtin_nontemporal_load ...
;     __device__ __forceinline__ void post(const Unit& u, int r, int cit, const float* v0, const float* v1, const Pre& p) const {
;         const size_t off = (size_t)(u.arow0 + r) * D + u.pn * 256 + cit; float g0[8], g1[8], m0[8], m1[8]; unpack8bf(p.g0, g0); unpack8bf(p.g1, g1); unpack8bf(p.m0, m0); unpack8bf(p.m1, m1);
; #pragma unroll
	v_cndmask_b32_e64 v18, v131, v18, s[0:1]
	v_mov_b32_e32 v131, 0
	v_fmac_f32_e32 v144, v18, v136
	v_add_u32_e32 v18, s73, v196
	v_mov_b32_dpp v131, v130 row_ror:8 row_mask:0xf bank_mask:0xf
	v_cndmask_b32_e64 v130, v20, v28, s[0:1]
	v_cndmask_b32_e64 v27, v27, v131, s[0:1]
	v_cndmask_b32_e64 v19, v131, v19, s[0:1]
	v_mov_b32_e32 v131, 0
	v_fmac_f32_e32 v84, v19, v92
	v_ashrrev_i32_e32 v19, 31, v18
	v_mov_b32_dpp v131, v130 row_ror:8 row_mask:0xf bank_mask:0xf
	v_cndmask_b32_e64 v130, v21, v29, s[0:1]
	v_cndmask_b32_e64 v28, v28, v131, s[0:1]
	v_cndmask_b32_e64 v20, v131, v20, s[0:1]
	v_mov_b32_e32 v131, 0
	v_lshlrev_b32_e32 v139, 16, v87
	v_and_b32_e32 v87, 0xffff0000, v87
	v_mov_b32_dpp v131, v130 row_ror:8 row_mask:0xf bank_mask:0xf
	v_cndmask_b32_e64 v29, v29, v131, s[0:1]
	v_cndmask_b32_e64 v21, v131, v21, s[0:1]
	v_lshlrev_b32_e32 v130, 16, v94
	v_and_b32_e32 v94, 0xffff0000, v94
	v_lshlrev_b32_e32 v131, 16, v95
	v_and_b32_e32 v95, 0xffff0000, v95
	v_lshlrev_b32_e32 v140, 16, v88
	v_and_b32_e32 v88, 0xffff0000, v88
	v_lshlrev_b32_e32 v141, 16, v89
	v_and_b32_e32 v89, 0xffff0000, v89
	v_lshlrev_b64 v[18:19], 12, v[18:19]
	v_lshlrev_b32_e32 v134, 16, v90
	v_and_b32_e32 v90, 0xffff0000, v90
	v_lshlrev_b32_e32 v137, 16, v93
	v_and_b32_e32 v93, 0xffff0000, v93
	v_lshlrev_b32_e32 v142, 16, v82
	v_and_b32_e32 v82, 0xffff0000, v82
	v_lshlrev_b32_e32 v145, 16, v85
	v_and_b32_e32 v85, 0xffff0000, v85
	v_fmac_f32_e32 v138, v30, v130
	v_fmac_f32_e32 v86, v31, v94
	v_fmac_f32_e32 v139, v32, v131
	v_fmac_f32_e32 v87, v33, v95
	v_fmac_f32_e32 v140, v26, v132
	v_fmac_f32_e32 v88, v27, v96
	v_fmac_f32_e32 v141, v28, v133
	v_fmac_f32_e32 v89, v29, v97
	v_lshl_add_u64 v[18:19], s[36:37], 0, v[18:19]
	v_lshlrev_b32_e32 v135, 16, v91
	v_and_b32_e32 v91, 0xffff0000, v91
	v_lshlrev_b32_e32 v143, 16, v83
	v_and_b32_e32 v83, 0xffff0000, v83
	v_fmac_f32_e32 v142, v22, v134
	v_fmac_f32_e32 v82, v23, v90
	v_fmac_f32_e32 v145, v20, v137
	v_fmac_f32_e32 v85, v21, v93
	v_lshl_add_u64 v[22:23], v[182:183], 1, v[18:19]
	v_cvt_pk_bf16_f32 v18, v138, v86
	v_cvt_pk_bf16_f32 v19, v139, v87
	v_cvt_pk_bf16_f32 v20, v140, v88
	v_cvt_pk_bf16_f32 v21, v141, v89
	v_fmac_f32_e32 v143, v24, v135
	v_fmac_f32_e32 v83, v25, v91
	global_store_dwordx4 v[22:23], v[18:21], off
	v_add_co_u32_e32 v22, vcc, 0x8000, v22
	s_nop 0
	v_cvt_pk_bf16_f32 v18, v142, v82
	v_cvt_pk_bf16_f32 v19, v143, v83
	v_cvt_pk_bf16_f32 v20, v144, v84
	v_cvt_pk_bf16_f32 v21, v145, v85
	v_addc_co_u32_e32 v23, vcc, 0, v23, vcc
	global_store_dwordx4 v[22:23], v[18:21], off
.LBB0_1166:
	s_and_b64 vcc, exec, s[8:9]
	s_cbranch_vccnz .LBB0_1168
	s_waitcnt vmcnt(6)
	v_cndmask_b32_e64 v18, v6, v14, s[0:1]
	v_mov_b32_e32 v19, 0
	s_nop 0
	v_lshlrev_b32_e32 v22, 16, v80
	v_and_b32_e32 v23, 0xffff0000, v80
	v_mov_b32_dpp v19, v18 row_ror:8 row_mask:0xf bank_mask:0xf
	v_cndmask_b32_e64 v18, v7, v15, s[0:1]
	v_cndmask_b32_e64 v14, v14, v19, s[0:1]
	v_cndmask_b32_e64 v6, v19, v6, s[0:1]
	v_mov_b32_e32 v19, 0
	s_nop 0
	v_lshlrev_b32_e32 v30, 16, v76
	s_nop 0
	v_lshlrev_b32_e32 v80, 16, v68
	v_mov_b32_dpp v19, v18 row_ror:8 row_mask:0xf bank_mask:0xf
	v_cndmask_b32_e64 v18, v8, v16, s[0:1]
	v_cndmask_b32_e64 v15, v15, v19, s[0:1]
	v_cndmask_b32_e64 v7, v19, v7, s[0:1]
	v_mov_b32_e32 v19, 0
	v_and_b32_e32 v31, 0xffff0000, v76
	v_and_b32_e32 v68, 0xffff0000, v68
	v_mov_b32_dpp v19, v18 row_ror:8 row_mask:0xf bank_mask:0xf
	v_cndmask_b32_e64 v18, v9, v17, s[0:1]
	v_cndmask_b32_e64 v16, v16, v19, s[0:1]
	v_cndmask_b32_e64 v8, v19, v8, s[0:1]
	v_mov_b32_e32 v19, 0
	v_lshlrev_b32_e32 v20, 16, v79
	v_and_b32_e32 v21, 0xffff0000, v79
	v_mov_b32_dpp v19, v18 row_ror:8 row_mask:0xf bank_mask:0xf
	v_cndmask_b32_e64 v18, v2, v10, s[0:1]
	v_cndmask_b32_e64 v17, v17, v19, s[0:1]
	v_cndmask_b32_e64 v9, v19, v9, s[0:1]
	v_mov_b32_e32 v19, 0
	v_lshlrev_b32_e32 v24, 16, v81
	v_and_b32_e32 v25, 0xffff0000, v81
	v_mov_b32_dpp v19, v18 row_ror:8 row_mask:0xf bank_mask:0xf
	v_cndmask_b32_e64 v18, v3, v11, s[0:1]
	v_cndmask_b32_e64 v10, v10, v19, s[0:1]
	v_cndmask_b32_e64 v2, v19, v2, s[0:1]
	v_mov_b32_e32 v19, 0
	v_fmac_f32_e32 v80, v2, v30
	v_add_u32_e32 v2, s74, v196
	v_mov_b32_dpp v19, v18 row_ror:8 row_mask:0xf bank_mask:0xf
	v_cndmask_b32_e64 v18, v4, v12, s[0:1]
	v_cndmask_b32_e64 v11, v11, v19, s[0:1]
	v_cndmask_b32_e64 v3, v19, v3, s[0:1]
	v_mov_b32_e32 v19, 0
	v_fmac_f32_e32 v68, v3, v31
	v_ashrrev_i32_e32 v3, 31, v2
	v_mov_b32_dpp v19, v18 row_ror:8 row_mask:0xf bank_mask:0xf
	v_cndmask_b32_e64 v18, v5, v13, s[0:1]
	v_cndmask_b32_e64 v12, v12, v19, s[0:1]
	v_cndmask_b32_e64 v4, v19, v4, s[0:1]
	v_mov_b32_e32 v19, 0
	v_lshlrev_b32_e32 v26, 16, v74
	v_and_b32_e32 v27, 0xffff0000, v74
	v_mov_b32_dpp v19, v18 row_ror:8 row_mask:0xf bank_mask:0xf
	v_cndmask_b32_e64 v13, v13, v19, s[0:1]
	v_cndmask_b32_e64 v5, v19, v5, s[0:1]
	v_lshlrev_b32_e32 v18, 16, v78
	v_and_b32_e32 v19, 0xffff0000, v78
	v_lshlrev_b32_e32 v28, 16, v75
	v_and_b32_e32 v29, 0xffff0000, v75
	v_lshlrev_b32_e32 v32, 16, v77
	v_and_b32_e32 v33, 0xffff0000, v77
	v_lshlrev_b32_e32 v74, 16, v70
	v_and_b32_e32 v70, 0xffff0000, v70
	v_lshlrev_b32_e32 v75, 16, v71
	v_and_b32_e32 v71, 0xffff0000, v71
	v_lshlrev_b32_e32 v76, 16, v72
	v_and_b32_e32 v72, 0xffff0000, v72
	v_lshlrev_b32_e32 v77, 16, v73
	v_and_b32_e32 v73, 0xffff0000, v73
	v_lshlrev_b64 v[2:3], 12, v[2:3]
	v_lshlrev_b32_e32 v78, 16, v66
	v_and_b32_e32 v66, 0xffff0000, v66
	v_lshlrev_b32_e32 v81, 16, v69
	v_and_b32_e32 v69, 0xffff0000, v69
	v_fmac_f32_e32 v74, v14, v18
	v_fmac_f32_e32 v70, v15, v19
	v_fmac_f32_e32 v75, v16, v20
	v_fmac_f32_e32 v71, v17, v21
	v_fmac_f32_e32 v76, v10, v22
	v_fmac_f32_e32 v72, v11, v23
	v_fmac_f32_e32 v77, v12, v24
	v_fmac_f32_e32 v73, v13, v25
	v_lshl_add_u64 v[2:3], s[36:37], 0, v[2:3]
	v_lshlrev_b32_e32 v79, 16, v67
	v_and_b32_e32 v67, 0xffff0000, v67
	v_fmac_f32_e32 v78, v6, v26
	v_fmac_f32_e32 v66, v7, v27
	v_fmac_f32_e32 v81, v4, v32
	v_fmac_f32_e32 v69, v5, v33
	v_lshl_add_u64 v[6:7], v[182:183], 1, v[2:3]
	v_cvt_pk_bf16_f32 v2, v74, v70
	v_cvt_pk_bf16_f32 v3, v75, v71
	v_cvt_pk_bf16_f32 v4, v76, v72
	v_cvt_pk_bf16_f32 v5, v77, v73
	v_fmac_f32_e32 v79, v8, v28
	v_fmac_f32_e32 v67, v9, v29
	global_store_dwordx4 v[6:7], v[2:5], off
	v_add_co_u32_e32 v6, vcc, 0x8000, v6
	s_nop 0
	v_cvt_pk_bf16_f32 v2, v78, v66
	v_cvt_pk_bf16_f32 v3, v79, v67
	v_cvt_pk_bf16_f32 v4, v80, v68
	v_cvt_pk_bf16_f32 v5, v81, v69
	v_addc_co_u32_e32 v7, vcc, 0, v7, vcc
	global_store_dwordx4 v[6:7], v[2:5], off

; template <class Epi, class Sched, bool GATHER, bool ALIGN_EPI = true, bool SP2 = true, bool REMAP64 = false>
; __device__ __forceinline__ void gemm_phase(LAS unsigned char* lds, const bf16* Ag, const bf16* Btg, const int K, const Sched& S, const Epi& E) {
;     ...
;             constexpr bool RP = REMAP64 && Epi::ROWPAIR;
;             const bool hi = RP && (fr >= 8); const int rsh = hi ? -8 : 0, citx = hi ? cit + 32 : cit;
;             typename Epi::Pre pq[2];
;             { const int r0_ = wr * 64 + fr; pq[0] = E.pre(cur, (r0_ < cur.nrows ? r0_ : cur.nrows - 1) + rsh, citx); }
; #pragma unroll
;             for (int gq = 0; gq < 8; ++gq) { const int ai = gq >> 2, m = gq & 3, r = ai * HALF + wr * 64 + m * 16 + fr;
;                 if (gq + 1 < 8) { const int rn = ((gq + 1) >> 2) * HALF + wr * 64 + ((gq + 1) & 3) * 16 + fr; pq[(gq + 1) & 1] = E.pre(cur, (rn < cur.nrows ? rn : cur.nrows - 1) + rsh, citx); }
;                 __builtin_amdgcn_sched_barrier(0);
;                 if (r < cur.nrows) { float v0[8], v1[8];
; #pragma unroll
;                     for (int i = 0; i < 4; ++i) { v0[i] = acc[ai][0][m][0][i]; v0[4 + i] = acc[ai][0][m][1][i]; v1[i] = acc[ai][1][m][0][i]; v1[4 + i] = acc[ai][1][m][1][i]; }
;                     if constexpr (RP) {
; #pragma unroll
;                         for (int i = 0; i < 8; ++i) { const float snd = hi ? v0[i] : v1[i];
;                             const float rcv = __builtin_bit_cast(float, __builtin_amdgcn_update_dpp(0, __builtin_bit_cast(int, snd), 0x128, 0xf, 0xf, false));
;                             if (hi) v0[i] = rcv; else v1[i] = rcv; } }
;                     E.post(cur, r + rsh, citx, v0, v1, pq[gq & 1]); }
;                 __builtin_amdgcn_sched_barrier(0); }
;     __device__ __forceinline__ Pre pre(const Unit& u, int r, int cit) const { const size_t off = (size_t)(u.arow0 + r) * D + u.pn * 256 + cit; return Pre{__builtin_nontemporal_load((const f32x4*)(x + off)), __builtin_nontemporal_load((const f32x4*)(x + off + 4)), __builtin_nontemporal_load((const f3 ...
;     __device__ __forceinline__ void post(const Unit& u, int r, int cit, const float* v0, const float* v1, const Pre& p) const {
;         const size_t off = (size_t)(u.arow0 + r) * D + u.pn * 256 + cit; float a[8], b[8];
; #pragma unroll
.LBB0_1251:
	s_nop 1
	v_add_u32_e32 v114, v204, v196
	v_ashrrev_i32_e32 v115, 31, v114
	v_lshlrev_b64 v[114:115], 13, v[114:115]
	v_lshl_add_u64 v[122:123], v[188:189], 0, v[114:115]
	global_load_dwordx4 v[114:117], v[122:123], off offset:16 nt
	global_load_dwordx4 v[118:121], v[122:123], off nt
	v_lshl_add_u64 v[126:127], v[122:123], 0, s[22:23]
	v_add_co_u32_e32 v122, vcc, 0x10000, v122
	s_nop 1
	v_addc_co_u32_e32 v123, vcc, 0, v123, vcc
	global_load_dwordx4 v[122:125], v[122:123], off nt
	s_nop 0
	global_load_dwordx4 v[126:129], v[126:127], off offset:16 nt
	s_nop 0
	v_cndmask_b32_e64 v146, 0, 1, s[18:19]
	v_cmp_ne_u32_e64 s[8:9], 1, v146
	s_andn2_b64 vcc, exec, s[18:19]
	s_cbranch_vccnz .LBB0_1253
	s_waitcnt vmcnt(14)
	v_cndmask_b32_e64 v146, v102, v110, s[0:1]
	v_mov_b32_e32 v147, v173
	s_nop 1
	v_mov_b32_dpp v147, v146 row_ror:8 row_mask:0xf bank_mask:0xf
	v_cndmask_b32_e64 v146, v103, v111, s[0:1]
	v_cndmask_b32_e64 v110, v110, v147, s[0:1]
	v_cndmask_b32_e64 v102, v147, v102, s[0:1]
	v_mov_b32_e32 v147, v173
	v_add_f32_e32 v110, v134, v110
	s_nop 0
	v_mov_b32_dpp v147, v146 row_ror:8 row_mask:0xf bank_mask:0xf
	v_cndmask_b32_e64 v146, v104, v112, s[0:1]
	v_cndmask_b32_e64 v111, v111, v147, s[0:1]
	v_cndmask_b32_e64 v103, v147, v103, s[0:1]
	v_mov_b32_e32 v147, v173
	v_add_f32_e32 v111, v135, v111
	s_nop 0
	v_mov_b32_dpp v147, v146 row_ror:8 row_mask:0xf bank_mask:0xf
	v_cndmask_b32_e64 v146, v105, v113, s[0:1]
	v_cndmask_b32_e64 v112, v112, v147, s[0:1]
	v_cndmask_b32_e64 v104, v147, v104, s[0:1]
	v_mov_b32_e32 v147, v173
	v_add_f32_e32 v112, v136, v112
	v_add_f32_e32 v104, v140, v104
	v_mov_b32_dpp v147, v146 row_ror:8 row_mask:0xf bank_mask:0xf
	v_cndmask_b32_e64 v146, v98, v106, s[0:1]
	v_cndmask_b32_e64 v113, v113, v147, s[0:1]
	v_cndmask_b32_e64 v105, v147, v105, s[0:1]
	v_mov_b32_e32 v147, v173
	v_add_f32_e32 v105, v141, v105
	s_nop 0
	v_mov_b32_dpp v147, v146 row_ror:8 row_mask:0xf bank_mask:0xf
	v_cndmask_b32_e64 v146, v99, v107, s[0:1]
	v_cndmask_b32_e64 v106, v106, v147, s[0:1]
	v_cndmask_b32_e64 v98, v147, v98, s[0:1]
	v_mov_b32_e32 v147, v173
	v_add_f32_e32 v134, v142, v98
	v_add_u32_e32 v98, s65, v203
	v_mov_b32_dpp v147, v146 row_ror:8 row_mask:0xf bank_mask:0xf
	v_cndmask_b32_e64 v146, v100, v108, s[0:1]
	v_cndmask_b32_e64 v107, v107, v147, s[0:1]
	v_cndmask_b32_e64 v99, v147, v99, s[0:1]
	v_mov_b32_e32 v147, v173
	v_add_f32_e32 v135, v143, v99
	v_ashrrev_i32_e32 v99, 31, v98
	v_mov_b32_dpp v147, v146 row_ror:8 row_mask:0xf bank_mask:0xf
	v_cndmask_b32_e64 v146, v101, v109, s[0:1]
	v_cndmask_b32_e64 v108, v108, v147, s[0:1]
	v_cndmask_b32_e64 v100, v147, v100, s[0:1]
	v_mov_b32_e32 v147, v173
	v_add_f32_e32 v106, v130, v106
	v_add_f32_e32 v107, v131, v107
	v_mov_b32_dpp v147, v146 row_ror:8 row_mask:0xf bank_mask:0xf
	v_cndmask_b32_e64 v109, v109, v147, s[0:1]
	v_cndmask_b32_e64 v101, v147, v101, s[0:1]
	v_add_f32_e32 v108, v132, v108
	v_add_f32_e32 v132, v144, v100
	v_add_f32_e32 v100, v137, v113
	v_add_f32_e32 v109, v133, v109
	v_lshlrev_b64 v[98:99], 12, v[98:99]
	v_add_f32_e32 v130, v138, v102
	v_add_f32_e32 v131, v139, v103
	v_add_f32_e32 v113, v145, v101
	v_lshl_add_u64 v[102:103], v[186:187], 0, v[98:99]
	v_cvt_pk_bf16_f32 v98, v110, v111
	v_cvt_pk_bf16_f32 v99, v112, v100
	v_cvt_pk_bf16_f32 v100, v106, v107
	v_cvt_pk_bf16_f32 v101, v108, v109
	global_store_dwordx4 v[102:103], v[98:101], off
	v_add_co_u32_e32 v102, vcc, 0x8000, v102
	s_nop 0
	v_cvt_pk_bf16_f32 v98, v130, v131
	v_cvt_pk_bf16_f32 v99, v104, v105
	v_cvt_pk_bf16_f32 v100, v134, v135
	v_cvt_pk_bf16_f32 v101, v132, v113
	v_addc_co_u32_e32 v103, vcc, 0, v103, vcc
	global_store_dwordx4 v[102:103], v[98:101], off

; template <class Epi, class Sched, bool GATHER, bool ALIGN_EPI = true, bool SP2 = true, bool REMAP64 = false>
; __device__ __forceinline__ void gemm_phase(LAS unsigned char* lds, const bf16* Ag, const bf16* Btg, const int K, const Sched& S, const Epi& E) {
;     ...
;             constexpr bool RP = REMAP64 && Epi::ROWPAIR;
;             const bool hi = RP && (fr >= 8); const int rsh = hi ? -8 : 0, citx = hi ? cit + 32 : cit;
;             typename Epi::Pre pq[2];
;             { const int r0_ = wr * 64 + fr; pq[0] = E.pre(cur, (r0_ < cur.nrows ? r0_ : cur.nrows - 1) + rsh, citx); }
; #pragma unroll
;             for (int gq = 0; gq < 8; ++gq) { const int ai = gq >> 2, m = gq & 3, r = ai * HALF + wr * 64 + m * 16 + fr;
;                 if (gq + 1 < 8) { const int rn = ((gq + 1) >> 2) * HALF + wr * 64 + ((gq + 1) & 3) * 16 + fr; pq[(gq + 1) & 1] = E.pre(cur, (rn < cur.nrows ? rn : cur.nrows - 1) + rsh, citx); }
;                 __builtin_amdgcn_sched_barrier(0);
;                 if (r < cur.nrows) { float v0[8], v1[8];
; #pragma unroll
;                     for (int i = 0; i < 4; ++i) { v0[i] = acc[ai][0][m][0][i]; v0[4 + i] = acc[ai][0][m][1][i]; v1[i] = acc[ai][1][m][0][i]; v1[4 + i] = acc[ai][1][m][1][i]; }
;                     if constexpr (RP) {
; #pragma unroll
;                         for (int i = 0; i < 8; ++i) { const float snd = hi ? v0[i] : v1[i];
;                             const float rcv = __builtin_bit_cast(float, __builtin_amdgcn_update_dpp(0, __builtin_bit_cast(int, snd), 0x128, 0xf, 0xf, false));
;                             if (hi) v0[i] = rcv; else v1[i] = rcv; } }
;                     E.post(cur, r + rsh, citx, v0, v1, pq[gq & 1]); }
;                 __builtin_amdgcn_sched_barrier(0); }
;     __device__ __forceinline__ Pre pre(const Unit& u, int r, int cit) const { const size_t off = (size_t)(u.arow0 + r) * D + u.pn * 256 + cit; return Pre{__builtin_nontemporal_load((const f32x4*)(x + off)), __builtin_nontemporal_load((const f32x4*)(x + off + 4)), __builtin_nontemporal_load((const f3 ...
;     __device__ __forceinline__ void post(const Unit& u, int r, int cit, const float* v0, const float* v1, const Pre& p) const {
;         const size_t off = (size_t)(u.arow0 + r) * D + u.pn * 256 + cit; float a[8], b[8];
; #pragma unroll
.LBB0_1255:
	s_nop 1
	v_add_u32_e32 v82, v204, v198
	v_ashrrev_i32_e32 v83, 31, v82
	v_lshlrev_b64 v[82:83], 13, v[82:83]
	v_lshl_add_u64 v[90:91], v[188:189], 0, v[82:83]
	global_load_dwordx4 v[82:85], v[90:91], off offset:16 nt
	global_load_dwordx4 v[86:89], v[90:91], off nt
	v_lshl_add_u64 v[94:95], v[90:91], 0, s[22:23]
	v_add_co_u32_e32 v90, vcc, 0x10000, v90
	s_nop 1
	v_addc_co_u32_e32 v91, vcc, 0, v91, vcc
	global_load_dwordx4 v[90:93], v[90:91], off nt
	s_nop 0
	global_load_dwordx4 v[94:97], v[94:95], off offset:16 nt
	s_and_b64 vcc, exec, s[8:9]
	s_cbranch_vccnz .LBB0_1257
	s_waitcnt vmcnt(18)
	v_cndmask_b32_e64 v146, v70, v78, s[0:1]
	v_mov_b32_e32 v147, v173
	s_nop 1
	v_mov_b32_dpp v147, v146 row_ror:8 row_mask:0xf bank_mask:0xf
	v_cndmask_b32_e64 v146, v71, v79, s[0:1]
	v_cndmask_b32_e64 v78, v78, v147, s[0:1]
	v_cndmask_b32_e64 v70, v147, v70, s[0:1]
	v_mov_b32_e32 v147, v173
	s_nop 0
	v_add_f32_e32 v78, v230, v78
	v_mov_b32_dpp v147, v146 row_ror:8 row_mask:0xf bank_mask:0xf
	v_cndmask_b32_e64 v146, v72, v80, s[0:1]
	v_cndmask_b32_e64 v79, v79, v147, s[0:1]
	v_cndmask_b32_e64 v71, v147, v71, s[0:1]
	v_mov_b32_e32 v147, v173
	v_add_f32_e32 v79, v231, v79
	s_nop 0
	v_mov_b32_dpp v147, v146 row_ror:8 row_mask:0xf bank_mask:0xf
	v_cndmask_b32_e64 v146, v73, v81, s[0:1]
	v_cndmask_b32_e64 v80, v80, v147, s[0:1]
	v_cndmask_b32_e64 v72, v147, v72, s[0:1]
	v_mov_b32_e32 v147, v173
	v_add_f32_e32 v80, v232, v80
	s_nop 0
	v_add_f32_e32 v72, v236, v72
	v_mov_b32_dpp v147, v146 row_ror:8 row_mask:0xf bank_mask:0xf
	v_cndmask_b32_e64 v146, v66, v74, s[0:1]
	v_cndmask_b32_e64 v81, v81, v147, s[0:1]
	v_cndmask_b32_e64 v73, v147, v73, s[0:1]
	v_mov_b32_e32 v147, v173
	v_add_f32_e32 v73, v237, v73
	s_nop 0
	v_mov_b32_dpp v147, v146 row_ror:8 row_mask:0xf bank_mask:0xf
	v_cndmask_b32_e64 v146, v67, v75, s[0:1]
	v_cndmask_b32_e64 v74, v74, v147, s[0:1]
	v_cndmask_b32_e64 v66, v147, v66, s[0:1]
	v_mov_b32_e32 v147, v173
	s_nop 0
	v_add_f32_e32 v230, v238, v66
	v_add_u32_e32 v66, s72, v203
	v_mov_b32_dpp v147, v146 row_ror:8 row_mask:0xf bank_mask:0xf
	v_cndmask_b32_e64 v146, v68, v76, s[0:1]
	v_cndmask_b32_e64 v75, v75, v147, s[0:1]
	v_cndmask_b32_e64 v67, v147, v67, s[0:1]
	v_mov_b32_e32 v147, v173
	v_add_f32_e32 v231, v239, v67
	v_ashrrev_i32_e32 v67, 31, v66
	v_mov_b32_dpp v147, v146 row_ror:8 row_mask:0xf bank_mask:0xf
	v_cndmask_b32_e64 v146, v69, v77, s[0:1]
	v_cndmask_b32_e64 v76, v76, v147, s[0:1]
	v_cndmask_b32_e64 v68, v147, v68, s[0:1]
	v_mov_b32_e32 v147, v173
	v_add_f32_e32 v74, v226, v74
	v_add_f32_e32 v75, v227, v75
	v_mov_b32_dpp v147, v146 row_ror:8 row_mask:0xf bank_mask:0xf
	v_cndmask_b32_e64 v77, v77, v147, s[0:1]
	v_cndmask_b32_e64 v69, v147, v69, s[0:1]
	v_add_f32_e32 v76, v228, v76
	v_add_f32_e32 v228, v240, v68
	v_add_f32_e32 v68, v233, v81
	v_add_f32_e32 v77, v229, v77
	v_lshlrev_b64 v[66:67], 12, v[66:67]
	v_add_f32_e32 v226, v234, v70
	v_add_f32_e32 v227, v235, v71
	v_add_f32_e32 v81, v241, v69
	v_lshl_add_u64 v[70:71], v[186:187], 0, v[66:67]
	v_cvt_pk_bf16_f32 v66, v78, v79
	v_cvt_pk_bf16_f32 v67, v80, v68
	v_cvt_pk_bf16_f32 v68, v74, v75
	v_cvt_pk_bf16_f32 v69, v76, v77
	global_store_dwordx4 v[70:71], v[66:69], off
	v_add_co_u32_e32 v70, vcc, 0x8000, v70
	s_nop 0
	v_cvt_pk_bf16_f32 v66, v226, v227
	v_cvt_pk_bf16_f32 v67, v72, v73
	v_cvt_pk_bf16_f32 v68, v230, v231
	v_cvt_pk_bf16_f32 v69, v228, v81
	v_addc_co_u32_e32 v71, vcc, 0, v71, vcc
	global_store_dwordx4 v[70:71], v[66:69], off
.LBB0_1257:
	s_nop 1
	v_add_u32_e32 v66, v204, v199
	v_ashrrev_i32_e32 v67, 31, v66
	v_lshlrev_b64 v[66:67], 13, v[66:67]
	v_lshl_add_u64 v[74:75], v[188:189], 0, v[66:67]
	global_load_dwordx4 v[66:69], v[74:75], off offset:16 nt
	global_load_dwordx4 v[70:73], v[74:75], off nt
	v_lshl_add_u64 v[78:79], v[74:75], 0, s[22:23]
	v_add_co_u32_e32 v74, vcc, 0x10000, v74
	s_nop 1
	v_addc_co_u32_e32 v75, vcc, 0, v75, vcc
	global_load_dwordx4 v[74:77], v[74:75], off nt
	s_nop 0
	global_load_dwordx4 v[78:81], v[78:79], off offset:16 nt
	s_nop 0
	v_cndmask_b32_e64 v146, 0, 1, s[20:21]
	v_cmp_ne_u32_e64 s[8:9], 1, v146
	s_andn2_b64 vcc, exec, s[20:21]
	s_cbranch_vccnz .LBB0_1259
	s_waitcnt vmcnt(18)
	v_cndmask_b32_e64 v130, v54, v62, s[0:1]
	v_mov_b32_e32 v131, v173
	s_nop 1
	v_mov_b32_dpp v131, v130 row_ror:8 row_mask:0xf bank_mask:0xf
	v_cndmask_b32_e64 v130, v55, v63, s[0:1]
	v_cndmask_b32_e64 v62, v62, v131, s[0:1]
	v_cndmask_b32_e64 v54, v131, v54, s[0:1]
	v_mov_b32_e32 v131, v173
	s_nop 0
	v_add_f32_e32 v62, v118, v62
	v_mov_b32_dpp v131, v130 row_ror:8 row_mask:0xf bank_mask:0xf
	v_cndmask_b32_e64 v130, v56, v64, s[0:1]
	v_cndmask_b32_e64 v63, v63, v131, s[0:1]
	v_cndmask_b32_e64 v55, v131, v55, s[0:1]
	v_mov_b32_e32 v131, v173
	v_add_f32_e32 v63, v119, v63
	s_nop 0
	v_mov_b32_dpp v131, v130 row_ror:8 row_mask:0xf bank_mask:0xf
	v_cndmask_b32_e64 v130, v57, v65, s[0:1]
	v_cndmask_b32_e64 v64, v64, v131, s[0:1]
	v_cndmask_b32_e64 v56, v131, v56, s[0:1]
	v_mov_b32_e32 v131, v173
	v_add_f32_e32 v64, v120, v64
	s_nop 0
	v_add_f32_e32 v56, v124, v56
	v_mov_b32_dpp v131, v130 row_ror:8 row_mask:0xf bank_mask:0xf
	v_cndmask_b32_e64 v130, v50, v58, s[0:1]
	v_cndmask_b32_e64 v65, v65, v131, s[0:1]
	v_cndmask_b32_e64 v57, v131, v57, s[0:1]
	v_mov_b32_e32 v131, v173
	v_add_f32_e32 v57, v125, v57
	s_nop 0
	v_mov_b32_dpp v131, v130 row_ror:8 row_mask:0xf bank_mask:0xf
	v_cndmask_b32_e64 v130, v51, v59, s[0:1]
	v_cndmask_b32_e64 v58, v58, v131, s[0:1]
	v_cndmask_b32_e64 v50, v131, v50, s[0:1]
	v_mov_b32_e32 v131, v173
	s_nop 0
	v_add_f32_e32 v118, v126, v50
	v_add_u32_e32 v50, s71, v203
	v_mov_b32_dpp v131, v130 row_ror:8 row_mask:0xf bank_mask:0xf
	v_cndmask_b32_e64 v130, v52, v60, s[0:1]
	v_cndmask_b32_e64 v59, v59, v131, s[0:1]
	v_cndmask_b32_e64 v51, v131, v51, s[0:1]
	v_mov_b32_e32 v131, v173
	v_add_f32_e32 v119, v127, v51
	v_ashrrev_i32_e32 v51, 31, v50
	v_mov_b32_dpp v131, v130 row_ror:8 row_mask:0xf bank_mask:0xf
	v_cndmask_b32_e64 v130, v53, v61, s[0:1]
	v_cndmask_b32_e64 v60, v60, v131, s[0:1]
	v_cndmask_b32_e64 v52, v131, v52, s[0:1]
	v_mov_b32_e32 v131, v173
	v_add_f32_e32 v58, v114, v58
	v_add_f32_e32 v59, v115, v59
	v_mov_b32_dpp v131, v130 row_ror:8 row_mask:0xf bank_mask:0xf
	v_cndmask_b32_e64 v61, v61, v131, s[0:1]
	v_cndmask_b32_e64 v53, v131, v53, s[0:1]
	v_add_f32_e32 v60, v116, v60
	v_add_f32_e32 v116, v128, v52
	v_add_f32_e32 v52, v121, v65
	v_add_f32_e32 v61, v117, v61
	v_lshlrev_b64 v[50:51], 12, v[50:51]
	v_add_f32_e32 v114, v122, v54
	v_add_f32_e32 v115, v123, v55
	v_add_f32_e32 v65, v129, v53
	v_lshl_add_u64 v[54:55], v[186:187], 0, v[50:51]
	v_cvt_pk_bf16_f32 v50, v62, v63
	v_cvt_pk_bf16_f32 v51, v64, v52
	v_cvt_pk_bf16_f32 v52, v58, v59
	v_cvt_pk_bf16_f32 v53, v60, v61
	global_store_dwordx4 v[54:55], v[50:53], off
	v_add_co_u32_e32 v54, vcc, 0x8000, v54
	s_nop 0
	v_cvt_pk_bf16_f32 v50, v114, v115
	v_cvt_pk_bf16_f32 v51, v56, v57
	v_cvt_pk_bf16_f32 v52, v118, v119
	v_cvt_pk_bf16_f32 v53, v116, v65
	v_addc_co_u32_e32 v55, vcc, 0, v55, vcc
	global_store_dwordx4 v[54:55], v[50:53], off
; template <class Epi, class Sched, bool GATHER, bool ALIGN_EPI = true, bool SP2 = true, bool REMAP64 = false>
; __device__ __forceinline__ void gemm_phase(LAS unsigned char* lds, const bf16* Ag, const bf16* Btg, const int K, const Sched& S, const Epi& E) {
;     ...
;             constexpr bool RP = REMAP64 && Epi::ROWPAIR;
;             const bool hi = RP && (fr >= 8); const int rsh = hi ? -8 : 0, citx = hi ? cit + 32 : cit;
;             typename Epi::Pre pq[2];
;             { const int r0_ = wr * 64 + fr; pq[0] = E.pre(cur, (r0_ < cur.nrows ? r0_ : cur.nrows - 1) + rsh, citx); }
; #pragma unroll
;             for (int gq = 0; gq < 8; ++gq) { const int ai = gq >> 2, m = gq & 3, r = ai * HALF + wr * 64 + m * 16 + fr;
;                 if (gq + 1 < 8) { const int rn = ((gq + 1) >> 2) * HALF + wr * 64 + ((gq + 1) & 3) * 16 + fr; pq[(gq + 1) & 1] = E.pre(cur, (rn < cur.nrows ? rn : cur.nrows - 1) + rsh, citx); }
;                 __builtin_amdgcn_sched_barrier(0);
;                 if (r < cur.nrows) { float v0[8], v1[8];
; #pragma unroll
;                     for (int i = 0; i < 4; ++i) { v0[i] = acc[ai][0][m][0][i]; v0[4 + i] = acc[ai][0][m][1][i]; v1[i] = acc[ai][1][m][0][i]; v1[4 + i] = acc[ai][1][m][1][i]; }
;                     if constexpr (RP) {
; #pragma unroll
;                         for (int i = 0; i < 8; ++i) { const float snd = hi ? v0[i] : v1[i];
;                             const float rcv = __builtin_bit_cast(float, __builtin_amdgcn_update_dpp(0, __builtin_bit_cast(int, snd), 0x128, 0xf, 0xf, false));
;                             if (hi) v0[i] = rcv; else v1[i] = rcv; } }
;                     E.post(cur, r + rsh, citx, v0, v1, pq[gq & 1]); }
;                 __builtin_amdgcn_sched_barrier(0); }
;     __device__ __forceinline__ Pre pre(const Unit& u, int r, int cit) const { const size_t off = (size_t)(u.arow0 + r) * D + u.pn * 256 + cit; return Pre{__builtin_nontemporal_load((const f32x4*)(x + off)), __builtin_nontemporal_load((const f32x4*)(x + off + 4)), __builtin_nontemporal_load((const f3 ...
;     __device__ __forceinline__ void post(const Unit& u, int r, int cit, const float* v0, const float* v1, const Pre& p) const {
;         const size_t off = (size_t)(u.arow0 + r) * D + u.pn * 256 + cit; float a[8], b[8];
; #pragma unroll
.LBB0_1259:
	s_and_b64 vcc, exec, s[8:9]
	s_cbranch_vccnz .LBB0_1261
	s_waitcnt vmcnt(14)
	s_nop 0
	v_cndmask_b32_e64 v146, v38, v46, s[0:1]
	v_mov_b32_e32 v147, v173
	s_nop 1
	v_mov_b32_dpp v147, v146 row_ror:8 row_mask:0xf bank_mask:0xf
	v_cndmask_b32_e64 v146, v39, v47, s[0:1]
	v_cndmask_b32_e64 v46, v46, v147, s[0:1]
	v_cndmask_b32_e64 v38, v147, v38, s[0:1]
	v_mov_b32_e32 v147, v173
	s_nop 0
	v_add_f32_e32 v46, v102, v46
	v_mov_b32_dpp v147, v146 row_ror:8 row_mask:0xf bank_mask:0xf
	v_cndmask_b32_e64 v146, v40, v48, s[0:1]
	v_cndmask_b32_e64 v47, v47, v147, s[0:1]
	v_cndmask_b32_e64 v39, v147, v39, s[0:1]
	v_mov_b32_e32 v147, v173
	v_add_f32_e32 v47, v103, v47
	s_nop 0
	v_mov_b32_dpp v147, v146 row_ror:8 row_mask:0xf bank_mask:0xf
	v_cndmask_b32_e64 v146, v41, v49, s[0:1]
	v_cndmask_b32_e64 v48, v48, v147, s[0:1]
	v_cndmask_b32_e64 v40, v147, v40, s[0:1]
	v_mov_b32_e32 v147, v173
	v_add_f32_e32 v48, v104, v48
	s_nop 0
	v_add_f32_e32 v40, v108, v40
	v_mov_b32_dpp v147, v146 row_ror:8 row_mask:0xf bank_mask:0xf
	v_cndmask_b32_e64 v146, v34, v42, s[0:1]
	v_cndmask_b32_e64 v49, v49, v147, s[0:1]
	v_cndmask_b32_e64 v41, v147, v41, s[0:1]
	v_mov_b32_e32 v147, v173
	v_add_f32_e32 v41, v109, v41
	s_nop 0
	v_mov_b32_dpp v147, v146 row_ror:8 row_mask:0xf bank_mask:0xf
	v_cndmask_b32_e64 v146, v35, v43, s[0:1]
	v_cndmask_b32_e64 v42, v42, v147, s[0:1]
	v_cndmask_b32_e64 v34, v147, v34, s[0:1]
	v_mov_b32_e32 v147, v173
	s_nop 0
	v_add_f32_e32 v102, v110, v34
	v_add_u32_e32 v34, s73, v203
	v_mov_b32_dpp v147, v146 row_ror:8 row_mask:0xf bank_mask:0xf
	v_cndmask_b32_e64 v146, v36, v44, s[0:1]
	v_cndmask_b32_e64 v43, v43, v147, s[0:1]
	v_cndmask_b32_e64 v35, v147, v35, s[0:1]
	v_mov_b32_e32 v147, v173
	v_add_f32_e32 v103, v111, v35
	v_ashrrev_i32_e32 v35, 31, v34
	v_mov_b32_dpp v147, v146 row_ror:8 row_mask:0xf bank_mask:0xf
	v_cndmask_b32_e64 v146, v37, v45, s[0:1]
	v_cndmask_b32_e64 v44, v44, v147, s[0:1]
	v_cndmask_b32_e64 v36, v147, v36, s[0:1]
	v_mov_b32_e32 v147, v173
	v_add_f32_e32 v42, v98, v42
	v_add_f32_e32 v43, v99, v43
	v_mov_b32_dpp v147, v146 row_ror:8 row_mask:0xf bank_mask:0xf
	v_cndmask_b32_e64 v45, v45, v147, s[0:1]
	v_cndmask_b32_e64 v37, v147, v37, s[0:1]
	v_add_f32_e32 v44, v100, v44
	v_add_f32_e32 v100, v112, v36
	v_add_f32_e32 v36, v105, v49
	v_add_f32_e32 v45, v101, v45
	v_lshlrev_b64 v[34:35], 12, v[34:35]
	v_add_f32_e32 v98, v106, v38
	v_add_f32_e32 v99, v107, v39
	v_add_f32_e32 v49, v113, v37
	v_lshl_add_u64 v[38:39], v[186:187], 0, v[34:35]
	v_cvt_pk_bf16_f32 v34, v46, v47
	v_cvt_pk_bf16_f32 v35, v48, v36
	v_cvt_pk_bf16_f32 v36, v42, v43
	v_cvt_pk_bf16_f32 v37, v44, v45
	global_store_dwordx4 v[38:39], v[34:37], off
	v_add_co_u32_e32 v38, vcc, 0x8000, v38
	s_nop 0
	v_cvt_pk_bf16_f32 v34, v98, v99
	v_cvt_pk_bf16_f32 v35, v40, v41
	v_cvt_pk_bf16_f32 v36, v102, v103
	v_cvt_pk_bf16_f32 v37, v100, v49
	v_addc_co_u32_e32 v39, vcc, 0, v39, vcc
	global_store_dwordx4 v[38:39], v[34:37], off
.LBB0_1261:
	s_and_b64 vcc, exec, s[8:9]
	s_cbranch_vccnz .LBB0_1263
	s_waitcnt vmcnt(10)
	s_nop 0
	v_cndmask_b32_e64 v130, v22, v30, s[0:1]
	v_mov_b32_e32 v131, v173
	s_nop 1
	v_mov_b32_dpp v131, v130 row_ror:8 row_mask:0xf bank_mask:0xf
	v_cndmask_b32_e64 v130, v23, v31, s[0:1]
	v_cndmask_b32_e64 v30, v30, v131, s[0:1]
	v_cndmask_b32_e64 v22, v131, v22, s[0:1]
	v_mov_b32_e32 v131, v173
	s_nop 0
	v_add_f32_e32 v30, v86, v30
	v_mov_b32_dpp v131, v130 row_ror:8 row_mask:0xf bank_mask:0xf
	v_cndmask_b32_e64 v130, v24, v32, s[0:1]
	v_cndmask_b32_e64 v31, v31, v131, s[0:1]
	v_cndmask_b32_e64 v23, v131, v23, s[0:1]
	v_mov_b32_e32 v131, v173
	v_add_f32_e32 v31, v87, v31
	s_nop 0
	v_mov_b32_dpp v131, v130 row_ror:8 row_mask:0xf bank_mask:0xf
	v_cndmask_b32_e64 v130, v25, v33, s[0:1]
	v_cndmask_b32_e64 v32, v32, v131, s[0:1]
	v_cndmask_b32_e64 v24, v131, v24, s[0:1]
	v_mov_b32_e32 v131, v173
	v_add_f32_e32 v32, v88, v32
	s_nop 0
	v_add_f32_e32 v24, v92, v24
	v_mov_b32_dpp v131, v130 row_ror:8 row_mask:0xf bank_mask:0xf
	v_cndmask_b32_e64 v130, v18, v26, s[0:1]
	v_cndmask_b32_e64 v33, v33, v131, s[0:1]
	v_cndmask_b32_e64 v25, v131, v25, s[0:1]
	v_mov_b32_e32 v131, v173
	v_add_f32_e32 v25, v93, v25
	s_nop 0
	v_mov_b32_dpp v131, v130 row_ror:8 row_mask:0xf bank_mask:0xf
	v_cndmask_b32_e64 v130, v19, v27, s[0:1]
	v_cndmask_b32_e64 v26, v26, v131, s[0:1]
	v_cndmask_b32_e64 v18, v131, v18, s[0:1]
	v_mov_b32_e32 v131, v173
	s_nop 0
	v_add_f32_e32 v86, v94, v18
	v_add_u32_e32 v18, s74, v203
	v_mov_b32_dpp v131, v130 row_ror:8 row_mask:0xf bank_mask:0xf
	v_cndmask_b32_e64 v130, v20, v28, s[0:1]
	v_cndmask_b32_e64 v27, v27, v131, s[0:1]
	v_cndmask_b32_e64 v19, v131, v19, s[0:1]
	v_mov_b32_e32 v131, v173
	v_add_f32_e32 v87, v95, v19
	v_ashrrev_i32_e32 v19, 31, v18
	v_mov_b32_dpp v131, v130 row_ror:8 row_mask:0xf bank_mask:0xf
	v_cndmask_b32_e64 v130, v21, v29, s[0:1]
	v_cndmask_b32_e64 v28, v28, v131, s[0:1]
	v_cndmask_b32_e64 v20, v131, v20, s[0:1]
	v_mov_b32_e32 v131, v173
	v_add_f32_e32 v26, v82, v26
	v_add_f32_e32 v27, v83, v27
	v_mov_b32_dpp v131, v130 row_ror:8 row_mask:0xf bank_mask:0xf
	v_cndmask_b32_e64 v29, v29, v131, s[0:1]
	v_cndmask_b32_e64 v21, v131, v21, s[0:1]
	v_add_f32_e32 v28, v84, v28
	v_add_f32_e32 v84, v96, v20
	v_add_f32_e32 v20, v89, v33
	v_add_f32_e32 v29, v85, v29
	v_lshlrev_b64 v[18:19], 12, v[18:19]
	v_add_f32_e32 v82, v90, v22
	v_add_f32_e32 v83, v91, v23
	v_add_f32_e32 v33, v97, v21
	v_lshl_add_u64 v[22:23], v[186:187], 0, v[18:19]
	v_cvt_pk_bf16_f32 v18, v30, v31
	v_cvt_pk_bf16_f32 v19, v32, v20
	v_cvt_pk_bf16_f32 v20, v26, v27
	v_cvt_pk_bf16_f32 v21, v28, v29
	global_store_dwordx4 v[22:23], v[18:21], off
	v_add_co_u32_e32 v22, vcc, 0x8000, v22
	s_nop 0
	v_cvt_pk_bf16_f32 v18, v82, v83
	v_cvt_pk_bf16_f32 v19, v24, v25
	v_cvt_pk_bf16_f32 v20, v86, v87
	v_cvt_pk_bf16_f32 v21, v84, v33
	v_addc_co_u32_e32 v23, vcc, 0, v23, vcc
	global_store_dwordx4 v[22:23], v[18:21], off

; template <class Epi, class Sched, bool GATHER, bool ALIGN_EPI = true, bool SP2 = true, bool REMAP64 = false>
; __device__ __forceinline__ void gemm_phase(LAS unsigned char* lds, const bf16* Ag, const bf16* Btg, const int K, const Sched& S, const Epi& E) {
;     ...
;             constexpr bool RP = REMAP64 && Epi::ROWPAIR;
;             const bool hi = RP && (fr >= 8); const int rsh = hi ? -8 : 0, citx = hi ? cit + 32 : cit;
;             typename Epi::Pre pq[2];
;             { const int r0_ = wr * 64 + fr; pq[0] = E.pre(cur, (r0_ < cur.nrows ? r0_ : cur.nrows - 1) + rsh, citx); }
; #pragma unroll
;             for (int gq = 0; gq < 8; ++gq) { const int ai = gq >> 2, m = gq & 3, r = ai * HALF + wr * 64 + m * 16 + fr;
;                 if (gq + 1 < 8) { const int rn = ((gq + 1) >> 2) * HALF + wr * 64 + ((gq + 1) & 3) * 16 + fr; pq[(gq + 1) & 1] = E.pre(cur, (rn < cur.nrows ? rn : cur.nrows - 1) + rsh, citx); }
;                 __builtin_amdgcn_sched_barrier(0);
;                 if (r < cur.nrows) { float v0[8], v1[8];
; #pragma unroll
;                     for (int i = 0; i < 4; ++i) { v0[i] = acc[ai][0][m][0][i]; v0[4 + i] = acc[ai][0][m][1][i]; v1[i] = acc[ai][1][m][0][i]; v1[4 + i] = acc[ai][1][m][1][i]; }
;                     if constexpr (RP) {
; #pragma unroll
;                         for (int i = 0; i < 8; ++i) { const float snd = hi ? v0[i] : v1[i];
;                             const float rcv = __builtin_bit_cast(float, __builtin_amdgcn_update_dpp(0, __builtin_bit_cast(int, snd), 0x128, 0xf, 0xf, false));
;                             if (hi) v0[i] = rcv; else v1[i] = rcv; } }
;                     E.post(cur, r + rsh, citx, v0, v1, pq[gq & 1]); }
;                 __builtin_amdgcn_sched_barrier(0); }
;     __device__ __forceinline__ Pre pre(const Unit& u, int r, int cit) const { const size_t off = (size_t)(u.arow0 + r) * D + u.pn * 256 + cit;
;         return Pre{__builtin_nontemporal_load((const v4u*)(pp + off)), __builtin_nontemporal_load((const v4u*)(pp + off + (size_t)8 * D)), *(const v4u*)(h + off), *(const v4u*)(h + off + (size_t)8 * D)}; }
;     __device__ __forceinline__ void post(const Unit& u, int r, int cit, const float* v0, const float* v1, const Pre& p) const {
.LBB0_1736:
	v_add_u32_e32 v128, s8, v189
	v_ashrrev_i32_e32 v129, 31, v128
	s_lshl_b32 s42, s40, 8
	v_lshlrev_b64 v[128:129], 11, v[128:129]
	s_ashr_i32 s43, s42, 31
	v_lshl_add_u64 v[128:129], v[128:129], 0, s[42:43]
	v_or_b32_e32 v128, v128, v172
	v_lshlrev_b64 v[128:129], 1, v[128:129]
	v_lshl_add_u64 v[130:131], s[36:37], 0, v[128:129]
	v_add_co_u32_e32 v132, vcc, s57, v130
	v_lshl_add_u64 v[128:129], s[4:5], 0, v[128:129]
	s_nop 0
	v_addc_co_u32_e32 v133, vcc, 0, v131, vcc
	global_load_dwordx4 v[156:159], v[130:131], off nt
	global_load_dwordx4 v[144:147], v[132:133], off nt
	v_add_co_u32_e32 v130, vcc, s57, v128
	v_add_u32_e32 v201, s8, v188
	s_nop 0
	v_addc_co_u32_e32 v131, vcc, 0, v129, vcc
	global_load_dwordx4 v[152:155], v[128:129], off
	global_load_dwordx4 v[148:151], v[130:131], off
	v_add_u32_e32 v128, v201, v190
	v_ashrrev_i32_e32 v129, 31, v128
	v_mov_b32_e32 v187, s43
	v_or_b32_e32 v186, s42, v172
	v_lshlrev_b64 v[128:129], 11, v[128:129]
	v_lshl_add_u64 v[128:129], v[128:129], 0, v[186:187]
	v_lshlrev_b64 v[132:133], 1, v[128:129]
	v_lshl_add_u64 v[128:129], s[36:37], 0, v[132:133]
	v_add_co_u32_e32 v130, vcc, 0x8000, v128
	v_lshl_add_u64 v[132:133], s[4:5], 0, v[132:133]
	s_nop 0
	v_addc_co_u32_e32 v131, vcc, 0, v129, vcc
	v_add_co_u32_e32 v134, vcc, 0x8000, v132
	global_load_dwordx4 v[140:143], v[128:129], off nt
	s_nop 0
	global_load_dwordx4 v[128:131], v[130:131], off nt
	v_addc_co_u32_e32 v135, vcc, 0, v133, vcc
	global_load_dwordx4 v[136:139], v[132:133], off
	s_nop 0
	global_load_dwordx4 v[132:135], v[134:135], off
	v_lshl_add_u64 v[184:185], s[42:43], 1, v[174:175]
	v_add_u32_e32 v200, v201, v161
	s_nop 1
	v_add_u32_e32 v214, v201, v191
	v_ashrrev_i32_e32 v215, 31, v214
	v_lshlrev_b64 v[214:215], 11, v[214:215]
	v_lshl_add_u64 v[214:215], v[214:215], 0, v[186:187]
	v_lshlrev_b64 v[218:219], 1, v[214:215]
	v_lshl_add_u64 v[214:215], s[36:37], 0, v[218:219]
	v_add_co_u32_e32 v216, vcc, 0x8000, v214
	v_lshl_add_u64 v[218:219], s[4:5], 0, v[218:219]
	s_nop 0
	v_addc_co_u32_e32 v217, vcc, 0, v215, vcc
	v_add_co_u32_e32 v220, vcc, 0x8000, v218
	global_load_dwordx4 v[226:229], v[214:215], off nt
	s_nop 0
	global_load_dwordx4 v[214:217], v[216:217], off nt
	v_addc_co_u32_e32 v221, vcc, 0, v219, vcc
	global_load_dwordx4 v[222:225], v[218:219], off
	s_nop 0
	global_load_dwordx4 v[218:221], v[220:221], off
	s_nop 1
	v_add_u32_e32 v230, v201, v192
	v_ashrrev_i32_e32 v231, 31, v230
	v_lshlrev_b64 v[230:231], 11, v[230:231]
	v_lshl_add_u64 v[230:231], v[230:231], 0, v[186:187]
	v_lshlrev_b64 v[234:235], 1, v[230:231]
	v_lshl_add_u64 v[230:231], s[36:37], 0, v[234:235]
	v_add_co_u32_e32 v232, vcc, 0x8000, v230
	v_lshl_add_u64 v[234:235], s[4:5], 0, v[234:235]
	s_nop 0
	v_addc_co_u32_e32 v233, vcc, 0, v231, vcc
	v_add_co_u32_e32 v236, vcc, 0x8000, v234
	global_load_dwordx4 v[242:245], v[230:231], off nt
	s_nop 0
	global_load_dwordx4 v[230:233], v[232:233], off nt
	v_addc_co_u32_e32 v237, vcc, 0, v235, vcc
	global_load_dwordx4 v[238:241], v[234:235], off
	s_nop 0
	global_load_dwordx4 v[234:237], v[236:237], off
	s_and_b64 vcc, exec, s[20:21]
	s_cbranch_vccz .LBB0_1738
	s_waitcnt vmcnt(12)
	v_cndmask_b32_e64 v202, v116, v124, s[0:1]
	v_mov_b32_e32 v203, 0
	s_nop 1
	v_mov_b32_dpp v203, v202 row_ror:8 row_mask:0xf bank_mask:0xf
	v_cndmask_b32_e64 v202, v117, v125, s[0:1]
	v_cndmask_b32_e64 v124, v124, v203, s[0:1]
	v_cndmask_b32_e64 v116, v203, v116, s[0:1]
	v_mov_b32_e32 v203, 0
	s_nop 1
	v_mov_b32_dpp v203, v202 row_ror:8 row_mask:0xf bank_mask:0xf
	v_cndmask_b32_e64 v202, v118, v126, s[0:1]
	v_cndmask_b32_e64 v125, v125, v203, s[0:1]
	v_cndmask_b32_e64 v203, v203, v117, s[0:1]
	v_mov_b32_e32 v117, 0
	s_nop 1
	v_mov_b32_dpp v117, v202 row_ror:8 row_mask:0xf bank_mask:0xf
	v_cndmask_b32_e64 v202, v119, v127, s[0:1]
	v_cndmask_b32_e64 v126, v126, v117, s[0:1]
	v_cndmask_b32_e64 v204, v117, v118, s[0:1]
	v_mov_b32_e32 v117, 0
	v_cndmask_b32_e64 v118, v112, v120, s[0:1]
	s_nop 0
	v_mov_b32_dpp v117, v202 row_ror:8 row_mask:0xf bank_mask:0xf
	v_cndmask_b32_e64 v127, v127, v117, s[0:1]
	v_cndmask_b32_e64 v202, v117, v119, s[0:1]
	v_mov_b32_e32 v117, 0
	s_nop 0
	v_and_b32_e32 v119, 0xffff0000, v152
	v_mov_b32_dpp v117, v118 row_ror:8 row_mask:0xf bank_mask:0xf
	v_cndmask_b32_e64 v118, v113, v121, s[0:1]
	v_cndmask_b32_e64 v206, v117, v112, s[0:1]
	v_mov_b32_e32 v112, 0
	v_cndmask_b32_e64 v205, v120, v117, s[0:1]
	v_cndmask_b32_e64 v117, v114, v122, s[0:1]
	v_mov_b32_dpp v112, v118 row_ror:8 row_mask:0xf bank_mask:0xf
	v_cndmask_b32_e64 v207, v121, v112, s[0:1]
	v_cndmask_b32_e64 v208, v112, v113, s[0:1]
	v_mov_b32_e32 v112, 0
	v_cndmask_b32_e64 v113, v115, v123, s[0:1]
	v_lshlrev_b32_e32 v118, 16, v152
	v_mov_b32_dpp v112, v117 row_ror:8 row_mask:0xf bank_mask:0xf
	v_cndmask_b32_e64 v210, v112, v114, s[0:1]
	v_mul_f32_e32 v114, 0xbfb8aa3b, v124
	v_exp_f32_e32 v114, v114
	v_cndmask_b32_e64 v209, v122, v112, s[0:1]
	v_mov_b32_e32 v112, 0
	v_and_b32_e32 v117, 0xffff0000, v156
	v_and_b32_e32 v121, 0xffff0000, v157
	v_mov_b32_dpp v112, v113 row_ror:8 row_mask:0xf bank_mask:0xf
	v_mul_f32_e32 v113, 0xbfb8aa3b, v116
	v_cndmask_b32_e64 v211, v123, v112, s[0:1]
	v_cndmask_b32_e64 v212, v112, v115, s[0:1]
	v_add_f32_e32 v112, 1.0, v114
	v_exp_f32_e32 v113, v113
	v_mul_f32_e32 v114, 0xbfb8aa3b, v125
	v_exp_f32_e32 v115, v114
	v_rcp_f32_e32 v112, v112
	v_add_f32_e32 v113, 1.0, v113
	v_rcp_f32_e32 v114, v113
	v_add_f32_e32 v113, 1.0, v115
	v_mul_f32_e32 v115, 0xbfb8aa3b, v203
	v_exp_f32_e32 v115, v115
	v_rcp_f32_e32 v113, v113
	v_lshlrev_b32_e32 v116, 16, v156
	v_lshlrev_b32_e32 v122, 16, v153
	v_add_f32_e32 v115, 1.0, v115
	v_rcp_f32_e32 v115, v115
; template <class Epi, class Sched, bool GATHER, bool ALIGN_EPI = true, bool SP2 = true, bool REMAP64 = false>
; __device__ __forceinline__ void gemm_phase(LAS unsigned char* lds, const bf16* Ag, const bf16* Btg, const int K, const Sched& S, const Epi& E) {
;     ...
;             constexpr bool RP = REMAP64 && Epi::ROWPAIR;
;             const bool hi = RP && (fr >= 8); const int rsh = hi ? -8 : 0, citx = hi ? cit + 32 : cit;
;             typename Epi::Pre pq[2];
;             { const int r0_ = wr * 64 + fr; pq[0] = E.pre(cur, (r0_ < cur.nrows ? r0_ : cur.nrows - 1) + rsh, citx); }
; #pragma unroll
;             for (int gq = 0; gq < 8; ++gq) { const int ai = gq >> 2, m = gq & 3, r = ai * HALF + wr * 64 + m * 16 + fr;
;                 if (gq + 1 < 8) { const int rn = ((gq + 1) >> 2) * HALF + wr * 64 + ((gq + 1) & 3) * 16 + fr; pq[(gq + 1) & 1] = E.pre(cur, (rn < cur.nrows ? rn : cur.nrows - 1) + rsh, citx); }
;                 __builtin_amdgcn_sched_barrier(0);
;                 if (r < cur.nrows) { float v0[8], v1[8];
; #pragma unroll
;                     for (int i = 0; i < 4; ++i) { v0[i] = acc[ai][0][m][0][i]; v0[4 + i] = acc[ai][0][m][1][i]; v1[i] = acc[ai][1][m][0][i]; v1[4 + i] = acc[ai][1][m][1][i]; }
;                     if constexpr (RP) {
; #pragma unroll
;                         for (int i = 0; i < 8; ++i) { const float snd = hi ? v0[i] : v1[i];
;                             const float rcv = __builtin_bit_cast(float, __builtin_amdgcn_update_dpp(0, __builtin_bit_cast(int, snd), 0x128, 0xf, 0xf, false));
;                             if (hi) v0[i] = rcv; else v1[i] = rcv; } }
;                     E.post(cur, r + rsh, citx, v0, v1, pq[gq & 1]); }
;                 __builtin_amdgcn_sched_barrier(0); }
;     __device__ __forceinline__ Pre pre(const Unit& u, int r, int cit) const { const size_t off = (size_t)(u.arow0 + r) * D + u.pn * 256 + cit;
;         return Pre{__builtin_nontemporal_load((const v4u*)(pp + off)), __builtin_nontemporal_load((const v4u*)(pp + off + (size_t)8 * D)), *(const v4u*)(h + off), *(const v4u*)(h + off + (size_t)8 * D)}; }
;     __device__ __forceinline__ void post(const Unit& u, int r, int cit, const float* v0, const float* v1, const Pre& p) const {
	v_pk_fma_f32 v[112:113], v[112:113], v[116:117], v[118:119]
	v_mul_f32_e32 v118, 0xbfb8aa3b, v126
	v_lshlrev_b32_e32 v116, 16, v144
	v_and_b32_e32 v117, 0xffff0000, v144
	v_exp_f32_e32 v120, v118
	v_lshlrev_b32_e32 v118, 16, v148
	v_and_b32_e32 v119, 0xffff0000, v148
	v_pk_fma_f32 v[116:117], v[114:115], v[116:117], v[118:119]
	v_mul_f32_e32 v115, 0xbfb8aa3b, v204
	v_exp_f32_e32 v115, v115
	v_mul_f32_e32 v118, 0xbfb8aa3b, v127
	v_exp_f32_e32 v119, v118
	v_add_f32_e32 v114, 1.0, v120
	v_add_f32_e32 v115, 1.0, v115
	v_rcp_f32_e32 v118, v115
	v_add_f32_e32 v115, 1.0, v119
	v_mul_f32_e32 v119, 0xbfb8aa3b, v202
	v_exp_f32_e32 v119, v119
	v_rcp_f32_e32 v114, v114
	v_rcp_f32_e32 v115, v115
	v_lshlrev_b32_e32 v120, 16, v157
	v_add_f32_e32 v119, 1.0, v119
	v_rcp_f32_e32 v119, v119
	v_and_b32_e32 v123, 0xffff0000, v153
	v_pk_fma_f32 v[114:115], v[114:115], v[120:121], v[122:123]
	v_mul_f32_e32 v122, 0xbfb8aa3b, v205
	v_lshlrev_b32_e32 v120, 16, v145
	v_and_b32_e32 v121, 0xffff0000, v145
	v_exp_f32_e32 v124, v122
	v_lshlrev_b32_e32 v122, 16, v149
	v_and_b32_e32 v123, 0xffff0000, v149
	v_pk_fma_f32 v[118:119], v[118:119], v[120:121], v[122:123]
	v_mul_f32_e32 v121, 0xbfb8aa3b, v206
	v_exp_f32_e32 v121, v121
	v_mul_f32_e32 v122, 0xbfb8aa3b, v207
	v_exp_f32_e32 v123, v122
	v_add_f32_e32 v120, 1.0, v124
	v_add_f32_e32 v121, 1.0, v121
	v_rcp_f32_e32 v122, v121
	v_add_f32_e32 v121, 1.0, v123
	v_mul_f32_e32 v123, 0xbfb8aa3b, v208
	v_exp_f32_e32 v123, v123
	v_rcp_f32_e32 v120, v120
	v_rcp_f32_e32 v121, v121
	v_lshlrev_b32_e32 v124, 16, v158
	v_add_f32_e32 v123, 1.0, v123
	v_rcp_f32_e32 v123, v123
	v_and_b32_e32 v125, 0xffff0000, v158
	v_lshlrev_b32_e32 v126, 16, v154
	v_and_b32_e32 v127, 0xffff0000, v154
	v_pk_fma_f32 v[120:121], v[120:121], v[124:125], v[126:127]
	v_mul_f32_e32 v126, 0xbfb8aa3b, v209
	v_lshlrev_b32_e32 v124, 16, v146
	v_and_b32_e32 v125, 0xffff0000, v146
	v_exp_f32_e32 v144, v126
	v_lshlrev_b32_e32 v126, 16, v150
	v_and_b32_e32 v127, 0xffff0000, v150
	v_pk_fma_f32 v[122:123], v[122:123], v[124:125], v[126:127]
	v_mul_f32_e32 v125, 0xbfb8aa3b, v210
	v_exp_f32_e32 v125, v125
	v_mul_f32_e32 v126, 0xbfb8aa3b, v211
	v_exp_f32_e32 v127, v126
	v_add_f32_e32 v124, 1.0, v144
	v_add_f32_e32 v125, 1.0, v125
	v_rcp_f32_e32 v126, v125
	v_add_f32_e32 v125, 1.0, v127
	v_mul_f32_e32 v127, 0xbfb8aa3b, v212
	v_exp_f32_e32 v127, v127
	v_rcp_f32_e32 v124, v124
	v_rcp_f32_e32 v125, v125
	v_lshlrev_b32_e32 v144, 16, v159
	v_add_f32_e32 v127, 1.0, v127
	v_rcp_f32_e32 v127, v127
	v_and_b32_e32 v145, 0xffff0000, v159
	v_lshlrev_b32_e32 v148, 16, v155
	v_and_b32_e32 v149, 0xffff0000, v155
	v_pk_fma_f32 v[124:125], v[124:125], v[144:145], v[148:149]
	v_lshlrev_b32_e32 v144, 16, v147
	v_and_b32_e32 v145, 0xffff0000, v147
	v_lshlrev_b32_e32 v146, 16, v151
	v_and_b32_e32 v147, 0xffff0000, v151
	v_pk_fma_f32 v[126:127], v[126:127], v[144:145], v[146:147]
	v_add_u32_e32 v144, s54, v200
	v_ashrrev_i32_e32 v145, 31, v144
	v_lshlrev_b64 v[144:145], 12, v[144:145]
	v_lshl_add_u64 v[144:145], v[184:185], 0, v[144:145]
	v_cvt_pk_bf16_f32 v112, v112, v113
	v_cvt_pk_bf16_f32 v113, v114, v115
	v_cvt_pk_bf16_f32 v114, v120, v121
	v_cvt_pk_bf16_f32 v115, v124, v125
	global_store_dwordx4 v[144:145], v[112:115], off
	s_nop 1
	v_cvt_pk_bf16_f32 v112, v116, v117
	v_add_co_u32_e32 v116, vcc, 0x8000, v144
	v_cvt_pk_bf16_f32 v113, v118, v119
	v_cvt_pk_bf16_f32 v114, v122, v123
	v_cvt_pk_bf16_f32 v115, v126, v127
	v_addc_co_u32_e32 v117, vcc, 0, v145, vcc
	global_store_dwordx4 v[116:117], v[112:115], off
.LBB0_1738:
	s_nop 1
	v_add_u32_e32 v112, v201, v193
	v_ashrrev_i32_e32 v113, 31, v112
	v_lshlrev_b64 v[112:113], 11, v[112:113]
	v_lshl_add_u64 v[112:113], v[112:113], 0, v[186:187]
	v_lshlrev_b64 v[116:117], 1, v[112:113]
	v_lshl_add_u64 v[112:113], s[36:37], 0, v[116:117]
	v_add_co_u32_e32 v114, vcc, 0x8000, v112
	v_lshl_add_u64 v[116:117], s[4:5], 0, v[116:117]
	s_nop 0
	v_addc_co_u32_e32 v115, vcc, 0, v113, vcc
	v_add_co_u32_e32 v118, vcc, 0x8000, v116
	global_load_dwordx4 v[124:127], v[112:113], off nt
	s_nop 0
	global_load_dwordx4 v[112:115], v[114:115], off nt
	v_addc_co_u32_e32 v119, vcc, 0, v117, vcc
	global_load_dwordx4 v[120:123], v[116:117], off
	s_nop 0
	global_load_dwordx4 v[116:119], v[118:119], off
	s_nop 0
	v_cndmask_b32_e64 v144, 0, 1, s[20:21]
	v_cmp_ne_u32_e64 s[8:9], 1, v144
	s_andn2_b64 vcc, exec, s[20:21]
	s_cbranch_vccnz .LBB0_1740
; template <class Epi, class Sched, bool GATHER, bool ALIGN_EPI = true, bool SP2 = true, bool REMAP64 = false>
; __device__ __forceinline__ void gemm_phase(LAS unsigned char* lds, const bf16* Ag, const bf16* Btg, const int K, const Sched& S, const Epi& E) {
;     ...
;             constexpr bool RP = REMAP64 && Epi::ROWPAIR;
;             const bool hi = RP && (fr >= 8); const int rsh = hi ? -8 : 0, citx = hi ? cit + 32 : cit;
;             typename Epi::Pre pq[2];
;             { const int r0_ = wr * 64 + fr; pq[0] = E.pre(cur, (r0_ < cur.nrows ? r0_ : cur.nrows - 1) + rsh, citx); }
; #pragma unroll
;             for (int gq = 0; gq < 8; ++gq) { const int ai = gq >> 2, m = gq & 3, r = ai * HALF + wr * 64 + m * 16 + fr;
;                 if (gq + 1 < 8) { const int rn = ((gq + 1) >> 2) * HALF + wr * 64 + ((gq + 1) & 3) * 16 + fr; pq[(gq + 1) & 1] = E.pre(cur, (rn < cur.nrows ? rn : cur.nrows - 1) + rsh, citx); }
;                 __builtin_amdgcn_sched_barrier(0);
;                 if (r < cur.nrows) { float v0[8], v1[8];
; #pragma unroll
;                     for (int i = 0; i < 4; ++i) { v0[i] = acc[ai][0][m][0][i]; v0[4 + i] = acc[ai][0][m][1][i]; v1[i] = acc[ai][1][m][0][i]; v1[4 + i] = acc[ai][1][m][1][i]; }
;                     if constexpr (RP) {
; #pragma unroll
;                         for (int i = 0; i < 8; ++i) { const float snd = hi ? v0[i] : v1[i];
;                             const float rcv = __builtin_bit_cast(float, __builtin_amdgcn_update_dpp(0, __builtin_bit_cast(int, snd), 0x128, 0xf, 0xf, false));
;                             if (hi) v0[i] = rcv; else v1[i] = rcv; } }
;                     E.post(cur, r + rsh, citx, v0, v1, pq[gq & 1]); }
;                 __builtin_amdgcn_sched_barrier(0); }
;     __device__ __forceinline__ Pre pre(const Unit& u, int r, int cit) const { const size_t off = (size_t)(u.arow0 + r) * D + u.pn * 256 + cit;
;         return Pre{__builtin_nontemporal_load((const v4u*)(pp + off)), __builtin_nontemporal_load((const v4u*)(pp + off + (size_t)8 * D)), *(const v4u*)(h + off), *(const v4u*)(h + off + (size_t)8 * D)}; }
;     __device__ __forceinline__ void post(const Unit& u, int r, int cit, const float* v0, const float* v1, const Pre& p) const {
	s_waitcnt vmcnt(14)
	v_cndmask_b32_e64 v144, v100, v108, s[0:1]
	v_mov_b32_e32 v145, 0
	s_nop 1
	v_mov_b32_dpp v145, v144 row_ror:8 row_mask:0xf bank_mask:0xf
	v_cndmask_b32_e64 v144, v101, v109, s[0:1]
	v_cndmask_b32_e64 v108, v108, v145, s[0:1]
	v_cndmask_b32_e64 v100, v145, v100, s[0:1]
	v_mov_b32_e32 v145, 0
	s_nop 1
	v_mov_b32_dpp v145, v144 row_ror:8 row_mask:0xf bank_mask:0xf
	v_cndmask_b32_e64 v144, v102, v110, s[0:1]
	v_cndmask_b32_e64 v109, v109, v145, s[0:1]
	v_cndmask_b32_e64 v145, v145, v101, s[0:1]
	v_mov_b32_e32 v101, 0
	s_nop 1
	v_mov_b32_dpp v101, v144 row_ror:8 row_mask:0xf bank_mask:0xf
	v_cndmask_b32_e64 v144, v103, v111, s[0:1]
	v_cndmask_b32_e64 v110, v110, v101, s[0:1]
	v_cndmask_b32_e64 v146, v101, v102, s[0:1]
	v_mov_b32_e32 v101, 0
	v_cndmask_b32_e64 v102, v96, v104, s[0:1]
	s_nop 0
	v_mov_b32_dpp v101, v144 row_ror:8 row_mask:0xf bank_mask:0xf
	v_cndmask_b32_e64 v111, v111, v101, s[0:1]
	v_cndmask_b32_e64 v144, v101, v103, s[0:1]
	v_mov_b32_e32 v101, 0
	v_and_b32_e32 v103, 0xffff0000, v136
	s_nop 0
	v_mov_b32_dpp v101, v102 row_ror:8 row_mask:0xf bank_mask:0xf
	v_cndmask_b32_e64 v102, v97, v105, s[0:1]
	v_cndmask_b32_e64 v148, v101, v96, s[0:1]
	v_mov_b32_e32 v96, 0
	v_cndmask_b32_e64 v147, v104, v101, s[0:1]
	v_cndmask_b32_e64 v101, v98, v106, s[0:1]
	v_mov_b32_dpp v96, v102 row_ror:8 row_mask:0xf bank_mask:0xf
	v_cndmask_b32_e64 v149, v105, v96, s[0:1]
	v_cndmask_b32_e64 v150, v96, v97, s[0:1]
	v_mov_b32_e32 v96, 0
	v_cndmask_b32_e64 v97, v99, v107, s[0:1]
	v_lshlrev_b32_e32 v102, 16, v136
	v_mov_b32_dpp v96, v101 row_ror:8 row_mask:0xf bank_mask:0xf
	v_cndmask_b32_e64 v152, v96, v98, s[0:1]
	v_mul_f32_e32 v98, 0xbfb8aa3b, v108
	v_exp_f32_e32 v98, v98
	v_cndmask_b32_e64 v151, v106, v96, s[0:1]
	v_mov_b32_e32 v96, 0
	v_and_b32_e32 v101, 0xffff0000, v140
	v_and_b32_e32 v105, 0xffff0000, v141
	v_mov_b32_dpp v96, v97 row_ror:8 row_mask:0xf bank_mask:0xf
	v_mul_f32_e32 v97, 0xbfb8aa3b, v100
	v_cndmask_b32_e64 v153, v107, v96, s[0:1]
	v_cndmask_b32_e64 v154, v96, v99, s[0:1]
	v_add_f32_e32 v96, 1.0, v98
	v_exp_f32_e32 v97, v97
	v_mul_f32_e32 v98, 0xbfb8aa3b, v109
	v_exp_f32_e32 v99, v98
	v_rcp_f32_e32 v96, v96
	v_add_f32_e32 v97, 1.0, v97
	v_rcp_f32_e32 v98, v97
	v_add_f32_e32 v97, 1.0, v99
	v_mul_f32_e32 v99, 0xbfb8aa3b, v145
	v_exp_f32_e32 v99, v99
	v_rcp_f32_e32 v97, v97
	v_lshlrev_b32_e32 v100, 16, v140
	v_lshlrev_b32_e32 v106, 16, v137
	v_add_f32_e32 v99, 1.0, v99
	v_rcp_f32_e32 v99, v99
	v_pk_fma_f32 v[96:97], v[96:97], v[100:101], v[102:103]
	v_mul_f32_e32 v102, 0xbfb8aa3b, v110
	v_lshlrev_b32_e32 v100, 16, v128
	v_and_b32_e32 v101, 0xffff0000, v128
	v_exp_f32_e32 v104, v102
	v_lshlrev_b32_e32 v102, 16, v132
	v_and_b32_e32 v103, 0xffff0000, v132
	v_pk_fma_f32 v[100:101], v[98:99], v[100:101], v[102:103]
	v_mul_f32_e32 v99, 0xbfb8aa3b, v146
	v_exp_f32_e32 v99, v99
	v_mul_f32_e32 v102, 0xbfb8aa3b, v111
	v_exp_f32_e32 v103, v102
	v_add_f32_e32 v98, 1.0, v104
	v_add_f32_e32 v99, 1.0, v99
	v_rcp_f32_e32 v102, v99
	v_add_f32_e32 v99, 1.0, v103
	v_mul_f32_e32 v103, 0xbfb8aa3b, v144
	v_exp_f32_e32 v103, v103
	v_rcp_f32_e32 v98, v98
	v_rcp_f32_e32 v99, v99
	v_lshlrev_b32_e32 v104, 16, v141
	v_add_f32_e32 v103, 1.0, v103
	v_rcp_f32_e32 v103, v103
	v_and_b32_e32 v107, 0xffff0000, v137
	v_pk_fma_f32 v[98:99], v[98:99], v[104:105], v[106:107]
	v_mul_f32_e32 v106, 0xbfb8aa3b, v147
	v_lshlrev_b32_e32 v104, 16, v129
	v_and_b32_e32 v105, 0xffff0000, v129
	v_exp_f32_e32 v108, v106
	v_lshlrev_b32_e32 v106, 16, v133
	v_and_b32_e32 v107, 0xffff0000, v133
	v_pk_fma_f32 v[102:103], v[102:103], v[104:105], v[106:107]
	v_mul_f32_e32 v105, 0xbfb8aa3b, v148
	v_exp_f32_e32 v105, v105
	v_mul_f32_e32 v106, 0xbfb8aa3b, v149
	v_exp_f32_e32 v107, v106
	v_add_f32_e32 v104, 1.0, v108
	v_add_f32_e32 v105, 1.0, v105
	v_rcp_f32_e32 v106, v105
	v_add_f32_e32 v105, 1.0, v107
	v_mul_f32_e32 v107, 0xbfb8aa3b, v150
	v_exp_f32_e32 v107, v107
	v_rcp_f32_e32 v104, v104
	v_rcp_f32_e32 v105, v105
	v_lshlrev_b32_e32 v108, 16, v142
	v_add_f32_e32 v107, 1.0, v107
	v_rcp_f32_e32 v107, v107
	v_and_b32_e32 v109, 0xffff0000, v142
	v_lshlrev_b32_e32 v110, 16, v138
	v_and_b32_e32 v111, 0xffff0000, v138
	v_pk_fma_f32 v[104:105], v[104:105], v[108:109], v[110:111]
	v_mul_f32_e32 v110, 0xbfb8aa3b, v151
	v_lshlrev_b32_e32 v108, 16, v130
	v_and_b32_e32 v109, 0xffff0000, v130
	v_exp_f32_e32 v128, v110
	v_lshlrev_b32_e32 v110, 16, v134
	v_and_b32_e32 v111, 0xffff0000, v134
	v_pk_fma_f32 v[106:107], v[106:107], v[108:109], v[110:111]
	v_mul_f32_e32 v109, 0xbfb8aa3b, v152
	v_exp_f32_e32 v109, v109
	v_mul_f32_e32 v110, 0xbfb8aa3b, v153
	v_exp_f32_e32 v111, v110
	v_add_f32_e32 v108, 1.0, v128
	v_add_f32_e32 v109, 1.0, v109
	v_rcp_f32_e32 v110, v109
	v_add_f32_e32 v109, 1.0, v111
	v_mul_f32_e32 v111, 0xbfb8aa3b, v154
	v_exp_f32_e32 v111, v111
	v_rcp_f32_e32 v108, v108
	v_rcp_f32_e32 v109, v109
	v_lshlrev_b32_e32 v128, 16, v143
	v_add_f32_e32 v111, 1.0, v111
	v_rcp_f32_e32 v111, v111
	v_and_b32_e32 v129, 0xffff0000, v143
	v_lshlrev_b32_e32 v132, 16, v139
	v_and_b32_e32 v133, 0xffff0000, v139
	v_pk_fma_f32 v[108:109], v[108:109], v[128:129], v[132:133]
	v_lshlrev_b32_e32 v128, 16, v131
	v_and_b32_e32 v129, 0xffff0000, v131
	v_lshlrev_b32_e32 v130, 16, v135
	v_and_b32_e32 v131, 0xffff0000, v135
	v_pk_fma_f32 v[110:111], v[110:111], v[128:129], v[130:131]
	v_add_u32_e32 v128, s58, v200
	v_ashrrev_i32_e32 v129, 31, v128
	v_lshlrev_b64 v[128:129], 12, v[128:129]
	v_lshl_add_u64 v[128:129], v[184:185], 0, v[128:129]
	v_cvt_pk_bf16_f32 v96, v96, v97
	v_cvt_pk_bf16_f32 v97, v98, v99
	v_cvt_pk_bf16_f32 v98, v104, v105
	v_cvt_pk_bf16_f32 v99, v108, v109
	global_store_dwordx4 v[128:129], v[96:99], off
	s_nop 1
	v_cvt_pk_bf16_f32 v96, v100, v101
	v_add_co_u32_e32 v100, vcc, 0x8000, v128
	v_cvt_pk_bf16_f32 v97, v102, v103
	v_cvt_pk_bf16_f32 v98, v106, v107
	v_cvt_pk_bf16_f32 v99, v110, v111
	v_addc_co_u32_e32 v101, vcc, 0, v129, vcc
	global_store_dwordx4 v[100:101], v[96:99], off
; template <class Epi, class Sched, bool GATHER, bool ALIGN_EPI = true, bool SP2 = true, bool REMAP64 = false>
; __device__ __forceinline__ void gemm_phase(LAS unsigned char* lds, const bf16* Ag, const bf16* Btg, const int K, const Sched& S, const Epi& E) {
;     ...
;             constexpr bool RP = REMAP64 && Epi::ROWPAIR;
;             const bool hi = RP && (fr >= 8); const int rsh = hi ? -8 : 0, citx = hi ? cit + 32 : cit;
;             typename Epi::Pre pq[2];
;             { const int r0_ = wr * 64 + fr; pq[0] = E.pre(cur, (r0_ < cur.nrows ? r0_ : cur.nrows - 1) + rsh, citx); }
; #pragma unroll
;             for (int gq = 0; gq < 8; ++gq) { const int ai = gq >> 2, m = gq & 3, r = ai * HALF + wr * 64 + m * 16 + fr;
;                 if (gq + 1 < 8) { const int rn = ((gq + 1) >> 2) * HALF + wr * 64 + ((gq + 1) & 3) * 16 + fr; pq[(gq + 1) & 1] = E.pre(cur, (rn < cur.nrows ? rn : cur.nrows - 1) + rsh, citx); }
;                 __builtin_amdgcn_sched_barrier(0);
;                 if (r < cur.nrows) { float v0[8], v1[8];
; #pragma unroll
;                     for (int i = 0; i < 4; ++i) { v0[i] = acc[ai][0][m][0][i]; v0[4 + i] = acc[ai][0][m][1][i]; v1[i] = acc[ai][1][m][0][i]; v1[4 + i] = acc[ai][1][m][1][i]; }
;                     if constexpr (RP) {
; #pragma unroll
;                         for (int i = 0; i < 8; ++i) { const float snd = hi ? v0[i] : v1[i];
;                             const float rcv = __builtin_bit_cast(float, __builtin_amdgcn_update_dpp(0, __builtin_bit_cast(int, snd), 0x128, 0xf, 0xf, false));
;                             if (hi) v0[i] = rcv; else v1[i] = rcv; } }
;                     E.post(cur, r + rsh, citx, v0, v1, pq[gq & 1]); }
;                 __builtin_amdgcn_sched_barrier(0); }
;     __device__ __forceinline__ Pre pre(const Unit& u, int r, int cit) const { const size_t off = (size_t)(u.arow0 + r) * D + u.pn * 256 + cit;
;         return Pre{__builtin_nontemporal_load((const v4u*)(pp + off)), __builtin_nontemporal_load((const v4u*)(pp + off + (size_t)8 * D)), *(const v4u*)(h + off), *(const v4u*)(h + off + (size_t)8 * D)}; }
;     __device__ __forceinline__ void post(const Unit& u, int r, int cit, const float* v0, const float* v1, const Pre& p) const {
.LBB0_1740:
	s_nop 1
	v_add_u32_e32 v96, v201, v194
	v_ashrrev_i32_e32 v97, 31, v96
	v_lshlrev_b64 v[96:97], 11, v[96:97]
	v_lshl_add_u64 v[96:97], v[96:97], 0, v[186:187]
	v_lshlrev_b64 v[100:101], 1, v[96:97]
	v_lshl_add_u64 v[96:97], s[36:37], 0, v[100:101]
	v_add_co_u32_e32 v98, vcc, 0x8000, v96
	v_lshl_add_u64 v[100:101], s[4:5], 0, v[100:101]
	s_nop 0
	v_addc_co_u32_e32 v99, vcc, 0, v97, vcc
	v_add_co_u32_e32 v102, vcc, 0x8000, v100
	global_load_dwordx4 v[108:111], v[96:97], off nt
	s_nop 0
	global_load_dwordx4 v[96:99], v[98:99], off nt
	v_addc_co_u32_e32 v103, vcc, 0, v101, vcc
	global_load_dwordx4 v[104:107], v[100:101], off
	s_nop 0
	global_load_dwordx4 v[100:103], v[102:103], off
	s_and_b64 vcc, exec, s[8:9]
	s_cbranch_vccnz .LBB0_1742
	s_waitcnt vmcnt(16)
	v_cndmask_b32_e64 v128, v84, v92, s[0:1]
	v_mov_b32_e32 v129, 0
	s_nop 1
	v_mov_b32_dpp v129, v128 row_ror:8 row_mask:0xf bank_mask:0xf
	v_cndmask_b32_e64 v128, v85, v93, s[0:1]
	v_cndmask_b32_e64 v92, v92, v129, s[0:1]
	v_cndmask_b32_e64 v84, v129, v84, s[0:1]
	v_mov_b32_e32 v129, 0
	s_nop 1
	v_mov_b32_dpp v129, v128 row_ror:8 row_mask:0xf bank_mask:0xf
	v_cndmask_b32_e64 v128, v86, v94, s[0:1]
	v_cndmask_b32_e64 v93, v93, v129, s[0:1]
	v_cndmask_b32_e64 v129, v129, v85, s[0:1]
	v_mov_b32_e32 v85, 0
	s_nop 1
	v_mov_b32_dpp v85, v128 row_ror:8 row_mask:0xf bank_mask:0xf
	v_cndmask_b32_e64 v128, v87, v95, s[0:1]
	v_cndmask_b32_e64 v94, v94, v85, s[0:1]
	v_cndmask_b32_e64 v130, v85, v86, s[0:1]
	v_mov_b32_e32 v85, 0
	v_cndmask_b32_e64 v86, v80, v88, s[0:1]
	s_nop 0
	v_mov_b32_dpp v85, v128 row_ror:8 row_mask:0xf bank_mask:0xf
	v_cndmask_b32_e64 v95, v95, v85, s[0:1]
	v_cndmask_b32_e64 v128, v85, v87, s[0:1]
	v_mov_b32_e32 v85, 0
	v_and_b32_e32 v87, 0xffff0000, v222
	s_nop 0
	v_mov_b32_dpp v85, v86 row_ror:8 row_mask:0xf bank_mask:0xf
	v_cndmask_b32_e64 v86, v81, v89, s[0:1]
	v_cndmask_b32_e64 v132, v85, v80, s[0:1]
	v_mov_b32_e32 v80, 0
	v_cndmask_b32_e64 v131, v88, v85, s[0:1]
	v_cndmask_b32_e64 v85, v82, v90, s[0:1]
	v_mov_b32_dpp v80, v86 row_ror:8 row_mask:0xf bank_mask:0xf
	v_cndmask_b32_e64 v133, v89, v80, s[0:1]
	v_cndmask_b32_e64 v134, v80, v81, s[0:1]
	v_mov_b32_e32 v80, 0
	v_cndmask_b32_e64 v81, v83, v91, s[0:1]
	v_lshlrev_b32_e32 v86, 16, v222
	v_mov_b32_dpp v80, v85 row_ror:8 row_mask:0xf bank_mask:0xf
	v_cndmask_b32_e64 v136, v80, v82, s[0:1]
	v_mul_f32_e32 v82, 0xbfb8aa3b, v92
	v_exp_f32_e32 v82, v82
	v_cndmask_b32_e64 v135, v90, v80, s[0:1]
	v_mov_b32_e32 v80, 0
	v_and_b32_e32 v85, 0xffff0000, v226
	v_and_b32_e32 v89, 0xffff0000, v227
	v_mov_b32_dpp v80, v81 row_ror:8 row_mask:0xf bank_mask:0xf
	v_mul_f32_e32 v81, 0xbfb8aa3b, v84
	v_cndmask_b32_e64 v137, v91, v80, s[0:1]
	v_cndmask_b32_e64 v138, v80, v83, s[0:1]
	v_add_f32_e32 v80, 1.0, v82
	v_exp_f32_e32 v81, v81
	v_mul_f32_e32 v82, 0xbfb8aa3b, v93
	v_exp_f32_e32 v83, v82
	v_rcp_f32_e32 v80, v80
	v_add_f32_e32 v81, 1.0, v81
	v_rcp_f32_e32 v82, v81
	v_add_f32_e32 v81, 1.0, v83
	v_mul_f32_e32 v83, 0xbfb8aa3b, v129
	v_exp_f32_e32 v83, v83
	v_rcp_f32_e32 v81, v81
	v_lshlrev_b32_e32 v84, 16, v226
	v_lshlrev_b32_e32 v90, 16, v223
	v_add_f32_e32 v83, 1.0, v83
	v_rcp_f32_e32 v83, v83
	v_pk_fma_f32 v[80:81], v[80:81], v[84:85], v[86:87]
	v_mul_f32_e32 v86, 0xbfb8aa3b, v94
	v_lshlrev_b32_e32 v84, 16, v214
	v_and_b32_e32 v85, 0xffff0000, v214
	v_exp_f32_e32 v88, v86
	v_lshlrev_b32_e32 v86, 16, v218
	v_and_b32_e32 v87, 0xffff0000, v218
	v_pk_fma_f32 v[84:85], v[82:83], v[84:85], v[86:87]
	v_mul_f32_e32 v83, 0xbfb8aa3b, v130
	v_exp_f32_e32 v83, v83
	v_mul_f32_e32 v86, 0xbfb8aa3b, v95
	v_exp_f32_e32 v87, v86
	v_add_f32_e32 v82, 1.0, v88
	v_add_f32_e32 v83, 1.0, v83
	v_rcp_f32_e32 v86, v83
	v_add_f32_e32 v83, 1.0, v87
	v_mul_f32_e32 v87, 0xbfb8aa3b, v128
	v_exp_f32_e32 v87, v87
	v_rcp_f32_e32 v82, v82
	v_rcp_f32_e32 v83, v83
	v_lshlrev_b32_e32 v88, 16, v227
	v_add_f32_e32 v87, 1.0, v87
	v_rcp_f32_e32 v87, v87
	v_and_b32_e32 v91, 0xffff0000, v223
	v_pk_fma_f32 v[82:83], v[82:83], v[88:89], v[90:91]
	v_mul_f32_e32 v90, 0xbfb8aa3b, v131
	v_lshlrev_b32_e32 v88, 16, v215
	v_and_b32_e32 v89, 0xffff0000, v215
	v_exp_f32_e32 v92, v90
	v_lshlrev_b32_e32 v90, 16, v219
	v_and_b32_e32 v91, 0xffff0000, v219
	v_pk_fma_f32 v[86:87], v[86:87], v[88:89], v[90:91]
	v_mul_f32_e32 v89, 0xbfb8aa3b, v132
	v_exp_f32_e32 v89, v89
	v_mul_f32_e32 v90, 0xbfb8aa3b, v133
	v_exp_f32_e32 v91, v90
	v_add_f32_e32 v88, 1.0, v92
	v_add_f32_e32 v89, 1.0, v89
	v_rcp_f32_e32 v90, v89
	v_add_f32_e32 v89, 1.0, v91
	v_mul_f32_e32 v91, 0xbfb8aa3b, v134
	v_exp_f32_e32 v91, v91
	v_rcp_f32_e32 v88, v88
	v_rcp_f32_e32 v89, v89
	v_lshlrev_b32_e32 v92, 16, v228
	v_add_f32_e32 v91, 1.0, v91
	v_rcp_f32_e32 v91, v91
	v_and_b32_e32 v93, 0xffff0000, v228
	v_lshlrev_b32_e32 v94, 16, v224
	v_and_b32_e32 v95, 0xffff0000, v224
	v_pk_fma_f32 v[88:89], v[88:89], v[92:93], v[94:95]
	v_mul_f32_e32 v94, 0xbfb8aa3b, v135
	v_lshlrev_b32_e32 v92, 16, v216
	v_and_b32_e32 v93, 0xffff0000, v216
	v_exp_f32_e32 v214, v94
	v_lshlrev_b32_e32 v94, 16, v220
	v_and_b32_e32 v95, 0xffff0000, v220
	v_pk_fma_f32 v[90:91], v[90:91], v[92:93], v[94:95]
	v_mul_f32_e32 v93, 0xbfb8aa3b, v136
	v_exp_f32_e32 v93, v93
	v_mul_f32_e32 v94, 0xbfb8aa3b, v137
	v_exp_f32_e32 v95, v94
	v_add_f32_e32 v92, 1.0, v214
	v_add_f32_e32 v93, 1.0, v93
	v_rcp_f32_e32 v94, v93
	v_add_f32_e32 v93, 1.0, v95
	v_mul_f32_e32 v95, 0xbfb8aa3b, v138
	v_exp_f32_e32 v95, v95
	v_rcp_f32_e32 v92, v92
	v_rcp_f32_e32 v93, v93
	v_lshlrev_b32_e32 v214, 16, v229
	v_add_f32_e32 v95, 1.0, v95
	v_rcp_f32_e32 v95, v95
	v_and_b32_e32 v215, 0xffff0000, v229
	v_lshlrev_b32_e32 v218, 16, v225
	v_and_b32_e32 v219, 0xffff0000, v225
	v_pk_fma_f32 v[92:93], v[92:93], v[214:215], v[218:219]
	v_lshlrev_b32_e32 v214, 16, v217
	v_and_b32_e32 v215, 0xffff0000, v217
	v_lshlrev_b32_e32 v216, 16, v221
	v_and_b32_e32 v217, 0xffff0000, v221
	v_pk_fma_f32 v[94:95], v[94:95], v[214:215], v[216:217]
	v_add_u32_e32 v214, s59, v200
	v_ashrrev_i32_e32 v215, 31, v214
	v_lshlrev_b64 v[214:215], 12, v[214:215]
	v_lshl_add_u64 v[214:215], v[184:185], 0, v[214:215]
	v_cvt_pk_bf16_f32 v80, v80, v81
	v_cvt_pk_bf16_f32 v81, v82, v83
	v_cvt_pk_bf16_f32 v82, v88, v89
	v_cvt_pk_bf16_f32 v83, v92, v93
	global_store_dwordx4 v[214:215], v[80:83], off
	s_nop 1
	v_cvt_pk_bf16_f32 v80, v84, v85
	v_add_co_u32_e32 v84, vcc, 0x8000, v214
	v_cvt_pk_bf16_f32 v81, v86, v87
	v_cvt_pk_bf16_f32 v82, v90, v91
	v_cvt_pk_bf16_f32 v83, v94, v95
	v_addc_co_u32_e32 v85, vcc, 0, v215, vcc
	global_store_dwordx4 v[84:85], v[80:83], off
; template <class Epi, class Sched, bool GATHER, bool ALIGN_EPI = true, bool SP2 = true, bool REMAP64 = false>
; __device__ __forceinline__ void gemm_phase(LAS unsigned char* lds, const bf16* Ag, const bf16* Btg, const int K, const Sched& S, const Epi& E) {
;     ...
;             constexpr bool RP = REMAP64 && Epi::ROWPAIR;
;             const bool hi = RP && (fr >= 8); const int rsh = hi ? -8 : 0, citx = hi ? cit + 32 : cit;
;             typename Epi::Pre pq[2];
;             { const int r0_ = wr * 64 + fr; pq[0] = E.pre(cur, (r0_ < cur.nrows ? r0_ : cur.nrows - 1) + rsh, citx); }
; #pragma unroll
;             for (int gq = 0; gq < 8; ++gq) { const int ai = gq >> 2, m = gq & 3, r = ai * HALF + wr * 64 + m * 16 + fr;
;                 if (gq + 1 < 8) { const int rn = ((gq + 1) >> 2) * HALF + wr * 64 + ((gq + 1) & 3) * 16 + fr; pq[(gq + 1) & 1] = E.pre(cur, (rn < cur.nrows ? rn : cur.nrows - 1) + rsh, citx); }
;                 __builtin_amdgcn_sched_barrier(0);
;                 if (r < cur.nrows) { float v0[8], v1[8];
; #pragma unroll
;                     for (int i = 0; i < 4; ++i) { v0[i] = acc[ai][0][m][0][i]; v0[4 + i] = acc[ai][0][m][1][i]; v1[i] = acc[ai][1][m][0][i]; v1[4 + i] = acc[ai][1][m][1][i]; }
;                     if constexpr (RP) {
; #pragma unroll
;                         for (int i = 0; i < 8; ++i) { const float snd = hi ? v0[i] : v1[i];
;                             const float rcv = __builtin_bit_cast(float, __builtin_amdgcn_update_dpp(0, __builtin_bit_cast(int, snd), 0x128, 0xf, 0xf, false));
;                             if (hi) v0[i] = rcv; else v1[i] = rcv; } }
;                     E.post(cur, r + rsh, citx, v0, v1, pq[gq & 1]); }
;                 __builtin_amdgcn_sched_barrier(0); }
;     __device__ __forceinline__ Pre pre(const Unit& u, int r, int cit) const { const size_t off = (size_t)(u.arow0 + r) * D + u.pn * 256 + cit;
;         return Pre{__builtin_nontemporal_load((const v4u*)(pp + off)), __builtin_nontemporal_load((const v4u*)(pp + off + (size_t)8 * D)), *(const v4u*)(h + off), *(const v4u*)(h + off + (size_t)8 * D)}; }
;     __device__ __forceinline__ void post(const Unit& u, int r, int cit, const float* v0, const float* v1, const Pre& p) const {
.LBB0_1742:
	s_nop 1
	v_add_u32_e32 v80, v201, v195
	v_ashrrev_i32_e32 v81, 31, v80
	v_lshlrev_b64 v[80:81], 11, v[80:81]
	v_lshl_add_u64 v[80:81], v[80:81], 0, v[186:187]
	v_lshlrev_b64 v[84:85], 1, v[80:81]
	v_lshl_add_u64 v[80:81], s[36:37], 0, v[84:85]
	v_add_co_u32_e32 v82, vcc, 0x8000, v80
	v_lshl_add_u64 v[84:85], s[4:5], 0, v[84:85]
	s_nop 0
	v_addc_co_u32_e32 v83, vcc, 0, v81, vcc
	v_add_co_u32_e32 v86, vcc, 0x8000, v84
	global_load_dwordx4 v[92:95], v[80:81], off nt
	s_nop 0
	global_load_dwordx4 v[80:83], v[82:83], off nt
	v_addc_co_u32_e32 v87, vcc, 0, v85, vcc
	global_load_dwordx4 v[88:91], v[84:85], off
	s_nop 0
	global_load_dwordx4 v[84:87], v[86:87], off
	s_and_b64 vcc, exec, s[8:9]
	s_cbranch_vccnz .LBB0_1744
	s_waitcnt vmcnt(18)
	v_cndmask_b32_e64 v144, v68, v76, s[0:1]
	v_mov_b32_e32 v145, 0
	s_nop 1
	v_mov_b32_dpp v145, v144 row_ror:8 row_mask:0xf bank_mask:0xf
	v_cndmask_b32_e64 v144, v69, v77, s[0:1]
	v_cndmask_b32_e64 v76, v76, v145, s[0:1]
	v_cndmask_b32_e64 v68, v145, v68, s[0:1]
	v_mov_b32_e32 v145, 0
	s_nop 1
	v_mov_b32_dpp v145, v144 row_ror:8 row_mask:0xf bank_mask:0xf
	v_cndmask_b32_e64 v144, v70, v78, s[0:1]
	v_cndmask_b32_e64 v77, v77, v145, s[0:1]
	v_cndmask_b32_e64 v145, v145, v69, s[0:1]
	v_mov_b32_e32 v69, 0
	s_nop 1
	v_mov_b32_dpp v69, v144 row_ror:8 row_mask:0xf bank_mask:0xf
	v_cndmask_b32_e64 v144, v71, v79, s[0:1]
	v_cndmask_b32_e64 v78, v78, v69, s[0:1]
	v_cndmask_b32_e64 v146, v69, v70, s[0:1]
	v_mov_b32_e32 v69, 0
	v_cndmask_b32_e64 v70, v64, v72, s[0:1]
	s_nop 0
	v_mov_b32_dpp v69, v144 row_ror:8 row_mask:0xf bank_mask:0xf
	v_cndmask_b32_e64 v79, v79, v69, s[0:1]
	v_cndmask_b32_e64 v144, v69, v71, s[0:1]
	v_mov_b32_e32 v69, 0
	s_nop 0
	v_and_b32_e32 v71, 0xffff0000, v238
	v_mov_b32_dpp v69, v70 row_ror:8 row_mask:0xf bank_mask:0xf
	v_cndmask_b32_e64 v70, v65, v73, s[0:1]
	v_cndmask_b32_e64 v148, v69, v64, s[0:1]
	v_mov_b32_e32 v64, 0
	v_cndmask_b32_e64 v147, v72, v69, s[0:1]
	v_cndmask_b32_e64 v69, v66, v74, s[0:1]
	v_mov_b32_dpp v64, v70 row_ror:8 row_mask:0xf bank_mask:0xf
	v_cndmask_b32_e64 v149, v73, v64, s[0:1]
	v_cndmask_b32_e64 v150, v64, v65, s[0:1]
	v_mov_b32_e32 v64, 0
	v_cndmask_b32_e64 v65, v67, v75, s[0:1]
	v_lshlrev_b32_e32 v70, 16, v238
	v_mov_b32_dpp v64, v69 row_ror:8 row_mask:0xf bank_mask:0xf
	v_cndmask_b32_e64 v152, v64, v66, s[0:1]
	v_mul_f32_e32 v66, 0xbfb8aa3b, v76
	v_exp_f32_e32 v66, v66
	v_cndmask_b32_e64 v151, v74, v64, s[0:1]
	v_mov_b32_e32 v64, 0
	v_and_b32_e32 v69, 0xffff0000, v242
	v_and_b32_e32 v73, 0xffff0000, v243
	v_mov_b32_dpp v64, v65 row_ror:8 row_mask:0xf bank_mask:0xf
	v_mul_f32_e32 v65, 0xbfb8aa3b, v68
	v_cndmask_b32_e64 v153, v75, v64, s[0:1]
	v_cndmask_b32_e64 v154, v64, v67, s[0:1]
	v_add_f32_e32 v64, 1.0, v66
	v_exp_f32_e32 v65, v65
	v_mul_f32_e32 v66, 0xbfb8aa3b, v77
	v_exp_f32_e32 v67, v66
	v_rcp_f32_e32 v64, v64
	v_add_f32_e32 v65, 1.0, v65
	v_rcp_f32_e32 v66, v65
	v_add_f32_e32 v65, 1.0, v67
	v_mul_f32_e32 v67, 0xbfb8aa3b, v145
	v_exp_f32_e32 v67, v67
	v_rcp_f32_e32 v65, v65
	v_lshlrev_b32_e32 v68, 16, v242
	v_lshlrev_b32_e32 v74, 16, v239
	v_add_f32_e32 v67, 1.0, v67
	v_rcp_f32_e32 v67, v67
	v_pk_fma_f32 v[64:65], v[64:65], v[68:69], v[70:71]
	v_mul_f32_e32 v70, 0xbfb8aa3b, v78
	v_lshlrev_b32_e32 v68, 16, v230
	v_and_b32_e32 v69, 0xffff0000, v230
	v_exp_f32_e32 v72, v70
	s_nop 0
	v_lshlrev_b32_e32 v70, 16, v234
	v_and_b32_e32 v71, 0xffff0000, v234
	v_pk_fma_f32 v[68:69], v[66:67], v[68:69], v[70:71]
	v_mul_f32_e32 v67, 0xbfb8aa3b, v146
	v_exp_f32_e32 v67, v67
	v_mul_f32_e32 v70, 0xbfb8aa3b, v79
	v_exp_f32_e32 v71, v70
	v_add_f32_e32 v66, 1.0, v72
	v_add_f32_e32 v67, 1.0, v67
	v_rcp_f32_e32 v70, v67
	v_add_f32_e32 v67, 1.0, v71
	v_mul_f32_e32 v71, 0xbfb8aa3b, v144
	v_exp_f32_e32 v71, v71
	v_rcp_f32_e32 v66, v66
	v_rcp_f32_e32 v67, v67
	v_lshlrev_b32_e32 v72, 16, v243
	v_add_f32_e32 v71, 1.0, v71
	v_rcp_f32_e32 v71, v71
	v_and_b32_e32 v75, 0xffff0000, v239
	v_pk_fma_f32 v[66:67], v[66:67], v[72:73], v[74:75]
	v_mul_f32_e32 v74, 0xbfb8aa3b, v147
	v_lshlrev_b32_e32 v72, 16, v231
	v_and_b32_e32 v73, 0xffff0000, v231
	v_exp_f32_e32 v76, v74
	v_lshlrev_b32_e32 v74, 16, v235
	v_and_b32_e32 v75, 0xffff0000, v235
	v_pk_fma_f32 v[70:71], v[70:71], v[72:73], v[74:75]
	v_mul_f32_e32 v73, 0xbfb8aa3b, v148
	v_exp_f32_e32 v73, v73
	v_mul_f32_e32 v74, 0xbfb8aa3b, v149
	v_exp_f32_e32 v75, v74
	v_add_f32_e32 v72, 1.0, v76
	v_add_f32_e32 v73, 1.0, v73
	v_rcp_f32_e32 v74, v73
	v_add_f32_e32 v73, 1.0, v75
	v_mul_f32_e32 v75, 0xbfb8aa3b, v150
	v_exp_f32_e32 v75, v75
	v_rcp_f32_e32 v72, v72
	v_rcp_f32_e32 v73, v73
	v_lshlrev_b32_e32 v76, 16, v244
	v_add_f32_e32 v75, 1.0, v75
	v_rcp_f32_e32 v75, v75
	v_and_b32_e32 v77, 0xffff0000, v244
	v_lshlrev_b32_e32 v78, 16, v240
	v_and_b32_e32 v79, 0xffff0000, v240
	v_pk_fma_f32 v[72:73], v[72:73], v[76:77], v[78:79]
	v_mul_f32_e32 v78, 0xbfb8aa3b, v151
	v_lshlrev_b32_e32 v76, 16, v232
	v_and_b32_e32 v77, 0xffff0000, v232
	v_exp_f32_e32 v230, v78
	v_lshlrev_b32_e32 v78, 16, v236
	v_and_b32_e32 v79, 0xffff0000, v236
	v_pk_fma_f32 v[74:75], v[74:75], v[76:77], v[78:79]
	v_mul_f32_e32 v77, 0xbfb8aa3b, v152
	v_exp_f32_e32 v77, v77
	v_mul_f32_e32 v78, 0xbfb8aa3b, v153
	v_exp_f32_e32 v79, v78
	v_add_f32_e32 v76, 1.0, v230
	v_add_f32_e32 v77, 1.0, v77
	v_rcp_f32_e32 v78, v77
	v_add_f32_e32 v77, 1.0, v79
	v_mul_f32_e32 v79, 0xbfb8aa3b, v154
	v_exp_f32_e32 v79, v79
	v_rcp_f32_e32 v76, v76
	v_rcp_f32_e32 v77, v77
	v_lshlrev_b32_e32 v230, 16, v245
	v_add_f32_e32 v79, 1.0, v79
	v_rcp_f32_e32 v79, v79
	v_and_b32_e32 v231, 0xffff0000, v245
	v_lshlrev_b32_e32 v234, 16, v241
	v_and_b32_e32 v235, 0xffff0000, v241
	v_pk_fma_f32 v[76:77], v[76:77], v[230:231], v[234:235]
	v_lshlrev_b32_e32 v230, 16, v233
	v_and_b32_e32 v231, 0xffff0000, v233
	v_lshlrev_b32_e32 v232, 16, v237
	v_and_b32_e32 v233, 0xffff0000, v237
	v_pk_fma_f32 v[78:79], v[78:79], v[230:231], v[232:233]
	v_add_u32_e32 v230, s61, v200
	v_ashrrev_i32_e32 v231, 31, v230
	v_lshlrev_b64 v[230:231], 12, v[230:231]
	v_lshl_add_u64 v[230:231], v[184:185], 0, v[230:231]
	v_cvt_pk_bf16_f32 v64, v64, v65
	v_cvt_pk_bf16_f32 v65, v66, v67
	v_cvt_pk_bf16_f32 v66, v72, v73
	v_cvt_pk_bf16_f32 v67, v76, v77
	global_store_dwordx4 v[230:231], v[64:67], off
	s_nop 1
	v_cvt_pk_bf16_f32 v64, v68, v69
	v_add_co_u32_e32 v68, vcc, 0x8000, v230
	v_cvt_pk_bf16_f32 v65, v70, v71
	v_cvt_pk_bf16_f32 v66, v74, v75
	v_cvt_pk_bf16_f32 v67, v78, v79
	v_addc_co_u32_e32 v69, vcc, 0, v231, vcc
	global_store_dwordx4 v[68:69], v[64:67], off
; template <class Epi, class Sched, bool GATHER, bool ALIGN_EPI = true, bool SP2 = true, bool REMAP64 = false>
; __device__ __forceinline__ void gemm_phase(LAS unsigned char* lds, const bf16* Ag, const bf16* Btg, const int K, const Sched& S, const Epi& E) {
;     ...
;             constexpr bool RP = REMAP64 && Epi::ROWPAIR;
;             const bool hi = RP && (fr >= 8); const int rsh = hi ? -8 : 0, citx = hi ? cit + 32 : cit;
;             typename Epi::Pre pq[2];
;             { const int r0_ = wr * 64 + fr; pq[0] = E.pre(cur, (r0_ < cur.nrows ? r0_ : cur.nrows - 1) + rsh, citx); }
; #pragma unroll
;             for (int gq = 0; gq < 8; ++gq) { const int ai = gq >> 2, m = gq & 3, r = ai * HALF + wr * 64 + m * 16 + fr;
;                 if (gq + 1 < 8) { const int rn = ((gq + 1) >> 2) * HALF + wr * 64 + ((gq + 1) & 3) * 16 + fr; pq[(gq + 1) & 1] = E.pre(cur, (rn < cur.nrows ? rn : cur.nrows - 1) + rsh, citx); }
;                 __builtin_amdgcn_sched_barrier(0);
;                 if (r < cur.nrows) { float v0[8], v1[8];
; #pragma unroll
;                     for (int i = 0; i < 4; ++i) { v0[i] = acc[ai][0][m][0][i]; v0[4 + i] = acc[ai][0][m][1][i]; v1[i] = acc[ai][1][m][0][i]; v1[4 + i] = acc[ai][1][m][1][i]; }
;                     if constexpr (RP) {
; #pragma unroll
;                         for (int i = 0; i < 8; ++i) { const float snd = hi ? v0[i] : v1[i];
;                             const float rcv = __builtin_bit_cast(float, __builtin_amdgcn_update_dpp(0, __builtin_bit_cast(int, snd), 0x128, 0xf, 0xf, false));
;                             if (hi) v0[i] = rcv; else v1[i] = rcv; } }
;                     E.post(cur, r + rsh, citx, v0, v1, pq[gq & 1]); }
;                 __builtin_amdgcn_sched_barrier(0); }
;     __device__ __forceinline__ Pre pre(const Unit& u, int r, int cit) const { const size_t off = (size_t)(u.arow0 + r) * D + u.pn * 256 + cit;
;         return Pre{__builtin_nontemporal_load((const v4u*)(pp + off)), __builtin_nontemporal_load((const v4u*)(pp + off + (size_t)8 * D)), *(const v4u*)(h + off), *(const v4u*)(h + off + (size_t)8 * D)}; }
;     __device__ __forceinline__ void post(const Unit& u, int r, int cit, const float* v0, const float* v1, const Pre& p) const {
.LBB0_1744:
	s_nop 1
	v_add_u32_e32 v64, v201, v196
	v_ashrrev_i32_e32 v65, 31, v64
	v_lshlrev_b64 v[64:65], 11, v[64:65]
	v_lshl_add_u64 v[64:65], v[64:65], 0, v[186:187]
	v_lshlrev_b64 v[68:69], 1, v[64:65]
	v_lshl_add_u64 v[64:65], s[36:37], 0, v[68:69]
	v_add_co_u32_e32 v66, vcc, 0x8000, v64
	v_lshl_add_u64 v[68:69], s[4:5], 0, v[68:69]
	s_nop 0
	v_addc_co_u32_e32 v67, vcc, 0, v65, vcc
	v_add_co_u32_e32 v70, vcc, 0x8000, v68
	global_load_dwordx4 v[76:79], v[64:65], off nt
	s_nop 0
	global_load_dwordx4 v[64:67], v[66:67], off nt
	v_addc_co_u32_e32 v71, vcc, 0, v69, vcc
	global_load_dwordx4 v[72:75], v[68:69], off
	s_nop 0
	global_load_dwordx4 v[68:71], v[70:71], off
	s_nop 0
	v_cndmask_b32_e64 v144, 0, 1, s[22:23]
	v_cmp_ne_u32_e64 s[8:9], 1, v144
	s_andn2_b64 vcc, exec, s[22:23]
	s_cbranch_vccnz .LBB0_1746
	s_waitcnt vmcnt(18)
	v_cndmask_b32_e64 v128, v52, v60, s[0:1]
	v_mov_b32_e32 v129, 0
	s_nop 1
	v_mov_b32_dpp v129, v128 row_ror:8 row_mask:0xf bank_mask:0xf
	v_cndmask_b32_e64 v128, v53, v61, s[0:1]
	v_cndmask_b32_e64 v60, v60, v129, s[0:1]
	v_cndmask_b32_e64 v52, v129, v52, s[0:1]
	v_mov_b32_e32 v129, 0
	s_nop 1
	v_mov_b32_dpp v129, v128 row_ror:8 row_mask:0xf bank_mask:0xf
	v_cndmask_b32_e64 v128, v54, v62, s[0:1]
	v_cndmask_b32_e64 v61, v61, v129, s[0:1]
	v_cndmask_b32_e64 v129, v129, v53, s[0:1]
	v_mov_b32_e32 v53, 0
	s_nop 1
	v_mov_b32_dpp v53, v128 row_ror:8 row_mask:0xf bank_mask:0xf
	v_cndmask_b32_e64 v128, v55, v63, s[0:1]
	v_cndmask_b32_e64 v62, v62, v53, s[0:1]
	v_cndmask_b32_e64 v130, v53, v54, s[0:1]
	v_mov_b32_e32 v53, 0
	v_cndmask_b32_e64 v54, v48, v56, s[0:1]
	s_nop 0
	v_mov_b32_dpp v53, v128 row_ror:8 row_mask:0xf bank_mask:0xf
	v_cndmask_b32_e64 v63, v63, v53, s[0:1]
	v_cndmask_b32_e64 v128, v53, v55, s[0:1]
	v_mov_b32_e32 v53, 0
	s_nop 0
	v_and_b32_e32 v55, 0xffff0000, v120
	v_mov_b32_dpp v53, v54 row_ror:8 row_mask:0xf bank_mask:0xf
	v_cndmask_b32_e64 v54, v49, v57, s[0:1]
	v_cndmask_b32_e64 v132, v53, v48, s[0:1]
	v_mov_b32_e32 v48, 0
	v_cndmask_b32_e64 v131, v56, v53, s[0:1]
	v_cndmask_b32_e64 v53, v50, v58, s[0:1]
	v_mov_b32_dpp v48, v54 row_ror:8 row_mask:0xf bank_mask:0xf
	v_cndmask_b32_e64 v133, v57, v48, s[0:1]
	v_cndmask_b32_e64 v134, v48, v49, s[0:1]
	v_mov_b32_e32 v48, 0
	v_cndmask_b32_e64 v49, v51, v59, s[0:1]
	v_lshlrev_b32_e32 v54, 16, v120
	v_mov_b32_dpp v48, v53 row_ror:8 row_mask:0xf bank_mask:0xf
	v_cndmask_b32_e64 v136, v48, v50, s[0:1]
	v_mul_f32_e32 v50, 0xbfb8aa3b, v60
	v_exp_f32_e32 v50, v50
	v_cndmask_b32_e64 v135, v58, v48, s[0:1]
	v_mov_b32_e32 v48, 0
	v_and_b32_e32 v53, 0xffff0000, v124
	v_and_b32_e32 v57, 0xffff0000, v125
	v_mov_b32_dpp v48, v49 row_ror:8 row_mask:0xf bank_mask:0xf
	v_mul_f32_e32 v49, 0xbfb8aa3b, v52
	v_cndmask_b32_e64 v137, v59, v48, s[0:1]
	v_cndmask_b32_e64 v138, v48, v51, s[0:1]
	v_add_f32_e32 v48, 1.0, v50
	v_exp_f32_e32 v49, v49
	v_mul_f32_e32 v50, 0xbfb8aa3b, v61
	v_exp_f32_e32 v51, v50
	v_rcp_f32_e32 v48, v48
	v_add_f32_e32 v49, 1.0, v49
	v_rcp_f32_e32 v50, v49
	v_add_f32_e32 v49, 1.0, v51
	v_mul_f32_e32 v51, 0xbfb8aa3b, v129
	v_exp_f32_e32 v51, v51
	v_rcp_f32_e32 v49, v49
	v_lshlrev_b32_e32 v52, 16, v124
	v_lshlrev_b32_e32 v58, 16, v121
	v_add_f32_e32 v51, 1.0, v51
	v_rcp_f32_e32 v51, v51
	v_pk_fma_f32 v[48:49], v[48:49], v[52:53], v[54:55]
	v_mul_f32_e32 v54, 0xbfb8aa3b, v62
	v_lshlrev_b32_e32 v52, 16, v112
	v_and_b32_e32 v53, 0xffff0000, v112
	v_exp_f32_e32 v56, v54
	s_nop 0
	v_lshlrev_b32_e32 v54, 16, v116
	v_and_b32_e32 v55, 0xffff0000, v116
	v_pk_fma_f32 v[52:53], v[50:51], v[52:53], v[54:55]
	v_mul_f32_e32 v51, 0xbfb8aa3b, v130
	v_exp_f32_e32 v51, v51
	v_mul_f32_e32 v54, 0xbfb8aa3b, v63
	v_exp_f32_e32 v55, v54
	v_add_f32_e32 v50, 1.0, v56
	v_add_f32_e32 v51, 1.0, v51
	v_rcp_f32_e32 v54, v51
	v_add_f32_e32 v51, 1.0, v55
	v_mul_f32_e32 v55, 0xbfb8aa3b, v128
	v_exp_f32_e32 v55, v55
	v_rcp_f32_e32 v50, v50
	v_rcp_f32_e32 v51, v51
	v_lshlrev_b32_e32 v56, 16, v125
	v_add_f32_e32 v55, 1.0, v55
	v_rcp_f32_e32 v55, v55
	v_and_b32_e32 v59, 0xffff0000, v121
	v_pk_fma_f32 v[50:51], v[50:51], v[56:57], v[58:59]
	v_mul_f32_e32 v58, 0xbfb8aa3b, v131
	v_lshlrev_b32_e32 v56, 16, v113
	v_and_b32_e32 v57, 0xffff0000, v113
	v_exp_f32_e32 v60, v58
	v_lshlrev_b32_e32 v58, 16, v117
	v_and_b32_e32 v59, 0xffff0000, v117
	v_pk_fma_f32 v[54:55], v[54:55], v[56:57], v[58:59]
	v_mul_f32_e32 v57, 0xbfb8aa3b, v132
	v_exp_f32_e32 v57, v57
	v_mul_f32_e32 v58, 0xbfb8aa3b, v133
	v_exp_f32_e32 v59, v58
	v_add_f32_e32 v56, 1.0, v60
	v_add_f32_e32 v57, 1.0, v57
	v_rcp_f32_e32 v58, v57
	v_add_f32_e32 v57, 1.0, v59
	v_mul_f32_e32 v59, 0xbfb8aa3b, v134
	v_exp_f32_e32 v59, v59
	v_rcp_f32_e32 v56, v56
	v_rcp_f32_e32 v57, v57
	v_lshlrev_b32_e32 v60, 16, v126
	v_add_f32_e32 v59, 1.0, v59
	v_rcp_f32_e32 v59, v59
	v_and_b32_e32 v61, 0xffff0000, v126
	v_lshlrev_b32_e32 v62, 16, v122
	v_and_b32_e32 v63, 0xffff0000, v122
	v_pk_fma_f32 v[56:57], v[56:57], v[60:61], v[62:63]
	v_mul_f32_e32 v62, 0xbfb8aa3b, v135
	v_lshlrev_b32_e32 v60, 16, v114
	v_and_b32_e32 v61, 0xffff0000, v114
	v_exp_f32_e32 v112, v62
	v_lshlrev_b32_e32 v62, 16, v118
	v_and_b32_e32 v63, 0xffff0000, v118
	v_pk_fma_f32 v[58:59], v[58:59], v[60:61], v[62:63]
	v_mul_f32_e32 v61, 0xbfb8aa3b, v136
	v_exp_f32_e32 v61, v61
	v_mul_f32_e32 v62, 0xbfb8aa3b, v137
	v_exp_f32_e32 v63, v62
	v_add_f32_e32 v60, 1.0, v112
	v_add_f32_e32 v61, 1.0, v61
	v_rcp_f32_e32 v62, v61
	v_add_f32_e32 v61, 1.0, v63
	v_mul_f32_e32 v63, 0xbfb8aa3b, v138
	v_exp_f32_e32 v63, v63
	v_rcp_f32_e32 v60, v60
	v_rcp_f32_e32 v61, v61
	v_lshlrev_b32_e32 v112, 16, v127
	v_add_f32_e32 v63, 1.0, v63
	v_rcp_f32_e32 v63, v63
	v_and_b32_e32 v113, 0xffff0000, v127
	v_lshlrev_b32_e32 v116, 16, v123
	v_and_b32_e32 v117, 0xffff0000, v123
	v_pk_fma_f32 v[60:61], v[60:61], v[112:113], v[116:117]
	v_lshlrev_b32_e32 v112, 16, v115
	v_and_b32_e32 v113, 0xffff0000, v115
	v_lshlrev_b32_e32 v114, 16, v119
	v_and_b32_e32 v115, 0xffff0000, v119
	v_pk_fma_f32 v[62:63], v[62:63], v[112:113], v[114:115]
	v_add_u32_e32 v112, s60, v200
	v_ashrrev_i32_e32 v113, 31, v112
	v_lshlrev_b64 v[112:113], 12, v[112:113]
	v_lshl_add_u64 v[112:113], v[184:185], 0, v[112:113]
	v_cvt_pk_bf16_f32 v48, v48, v49
	v_cvt_pk_bf16_f32 v49, v50, v51
	v_cvt_pk_bf16_f32 v50, v56, v57
	v_cvt_pk_bf16_f32 v51, v60, v61
	global_store_dwordx4 v[112:113], v[48:51], off
	s_nop 1
	v_cvt_pk_bf16_f32 v48, v52, v53
	v_add_co_u32_e32 v52, vcc, 0x8000, v112
	v_cvt_pk_bf16_f32 v49, v54, v55
	v_cvt_pk_bf16_f32 v50, v58, v59
	v_cvt_pk_bf16_f32 v51, v62, v63
	v_addc_co_u32_e32 v53, vcc, 0, v113, vcc
	global_store_dwordx4 v[52:53], v[48:51], off
; template <class Epi, class Sched, bool GATHER, bool ALIGN_EPI = true, bool SP2 = true, bool REMAP64 = false>
; __device__ __forceinline__ void gemm_phase(LAS unsigned char* lds, const bf16* Ag, const bf16* Btg, const int K, const Sched& S, const Epi& E) {
;     ...
;             constexpr bool RP = REMAP64 && Epi::ROWPAIR;
;             const bool hi = RP && (fr >= 8); const int rsh = hi ? -8 : 0, citx = hi ? cit + 32 : cit;
;             typename Epi::Pre pq[2];
;             { const int r0_ = wr * 64 + fr; pq[0] = E.pre(cur, (r0_ < cur.nrows ? r0_ : cur.nrows - 1) + rsh, citx); }
; #pragma unroll
;             for (int gq = 0; gq < 8; ++gq) { const int ai = gq >> 2, m = gq & 3, r = ai * HALF + wr * 64 + m * 16 + fr;
;                 if (gq + 1 < 8) { const int rn = ((gq + 1) >> 2) * HALF + wr * 64 + ((gq + 1) & 3) * 16 + fr; pq[(gq + 1) & 1] = E.pre(cur, (rn < cur.nrows ? rn : cur.nrows - 1) + rsh, citx); }
;                 __builtin_amdgcn_sched_barrier(0);
;                 if (r < cur.nrows) { float v0[8], v1[8];
; #pragma unroll
;                     for (int i = 0; i < 4; ++i) { v0[i] = acc[ai][0][m][0][i]; v0[4 + i] = acc[ai][0][m][1][i]; v1[i] = acc[ai][1][m][0][i]; v1[4 + i] = acc[ai][1][m][1][i]; }
;                     if constexpr (RP) {
; #pragma unroll
;                         for (int i = 0; i < 8; ++i) { const float snd = hi ? v0[i] : v1[i];
;                             const float rcv = __builtin_bit_cast(float, __builtin_amdgcn_update_dpp(0, __builtin_bit_cast(int, snd), 0x128, 0xf, 0xf, false));
;                             if (hi) v0[i] = rcv; else v1[i] = rcv; } }
;                     E.post(cur, r + rsh, citx, v0, v1, pq[gq & 1]); }
;                 __builtin_amdgcn_sched_barrier(0); }
;     __device__ __forceinline__ Pre pre(const Unit& u, int r, int cit) const { const size_t off = (size_t)(u.arow0 + r) * D + u.pn * 256 + cit;
;         return Pre{__builtin_nontemporal_load((const v4u*)(pp + off)), __builtin_nontemporal_load((const v4u*)(pp + off + (size_t)8 * D)), *(const v4u*)(h + off), *(const v4u*)(h + off + (size_t)8 * D)}; }
;     __device__ __forceinline__ void post(const Unit& u, int r, int cit, const float* v0, const float* v1, const Pre& p) const {
.LBB0_1746:
	s_and_b64 vcc, exec, s[8:9]
	s_cbranch_vccnz .LBB0_1748
	s_waitcnt vmcnt(14)
	s_nop 0
	v_cndmask_b32_e64 v144, v36, v44, s[0:1]
	v_mov_b32_e32 v145, 0
	s_nop 1
	v_mov_b32_dpp v145, v144 row_ror:8 row_mask:0xf bank_mask:0xf
	v_cndmask_b32_e64 v144, v37, v45, s[0:1]
	v_cndmask_b32_e64 v44, v44, v145, s[0:1]
	v_cndmask_b32_e64 v36, v145, v36, s[0:1]
	v_mov_b32_e32 v145, 0
	s_nop 1
	v_mov_b32_dpp v145, v144 row_ror:8 row_mask:0xf bank_mask:0xf
	v_cndmask_b32_e64 v144, v38, v46, s[0:1]
	v_cndmask_b32_e64 v45, v45, v145, s[0:1]
	v_cndmask_b32_e64 v145, v145, v37, s[0:1]
	v_mov_b32_e32 v37, 0
	s_nop 1
	v_mov_b32_dpp v37, v144 row_ror:8 row_mask:0xf bank_mask:0xf
	v_cndmask_b32_e64 v144, v39, v47, s[0:1]
	v_cndmask_b32_e64 v46, v46, v37, s[0:1]
	v_cndmask_b32_e64 v146, v37, v38, s[0:1]
	v_mov_b32_e32 v37, 0
	v_cndmask_b32_e64 v38, v32, v40, s[0:1]
	s_nop 0
	v_mov_b32_dpp v37, v144 row_ror:8 row_mask:0xf bank_mask:0xf
	v_cndmask_b32_e64 v47, v47, v37, s[0:1]
	v_cndmask_b32_e64 v144, v37, v39, s[0:1]
	v_mov_b32_e32 v37, 0
	s_nop 0
	v_and_b32_e32 v39, 0xffff0000, v104
	v_mov_b32_dpp v37, v38 row_ror:8 row_mask:0xf bank_mask:0xf
	v_cndmask_b32_e64 v38, v33, v41, s[0:1]
	v_cndmask_b32_e64 v148, v37, v32, s[0:1]
	v_mov_b32_e32 v32, 0
	v_cndmask_b32_e64 v147, v40, v37, s[0:1]
	v_cndmask_b32_e64 v37, v34, v42, s[0:1]
	v_mov_b32_dpp v32, v38 row_ror:8 row_mask:0xf bank_mask:0xf
	v_cndmask_b32_e64 v149, v41, v32, s[0:1]
	v_cndmask_b32_e64 v150, v32, v33, s[0:1]
	v_mov_b32_e32 v32, 0
	v_cndmask_b32_e64 v33, v35, v43, s[0:1]
	v_lshlrev_b32_e32 v38, 16, v104
	v_mov_b32_dpp v32, v37 row_ror:8 row_mask:0xf bank_mask:0xf
	v_cndmask_b32_e64 v152, v32, v34, s[0:1]
	v_mul_f32_e32 v34, 0xbfb8aa3b, v44
	v_exp_f32_e32 v34, v34
	v_cndmask_b32_e64 v151, v42, v32, s[0:1]
	v_mov_b32_e32 v32, 0
	v_and_b32_e32 v37, 0xffff0000, v108
	v_and_b32_e32 v41, 0xffff0000, v109
	v_mov_b32_dpp v32, v33 row_ror:8 row_mask:0xf bank_mask:0xf
	v_mul_f32_e32 v33, 0xbfb8aa3b, v36
	v_cndmask_b32_e64 v153, v43, v32, s[0:1]
	v_cndmask_b32_e64 v154, v32, v35, s[0:1]
	v_add_f32_e32 v32, 1.0, v34
	v_exp_f32_e32 v33, v33
	v_mul_f32_e32 v34, 0xbfb8aa3b, v45
	v_exp_f32_e32 v35, v34
	v_rcp_f32_e32 v32, v32
	v_add_f32_e32 v33, 1.0, v33
	v_rcp_f32_e32 v34, v33
	v_add_f32_e32 v33, 1.0, v35
	v_mul_f32_e32 v35, 0xbfb8aa3b, v145
	v_exp_f32_e32 v35, v35
	v_rcp_f32_e32 v33, v33
	v_lshlrev_b32_e32 v36, 16, v108
	v_lshlrev_b32_e32 v42, 16, v105
	v_add_f32_e32 v35, 1.0, v35
	v_rcp_f32_e32 v35, v35
	v_pk_fma_f32 v[32:33], v[32:33], v[36:37], v[38:39]
	v_mul_f32_e32 v38, 0xbfb8aa3b, v46
	v_lshlrev_b32_e32 v36, 16, v96
	v_and_b32_e32 v37, 0xffff0000, v96
	v_exp_f32_e32 v40, v38
	s_nop 0
	v_lshlrev_b32_e32 v38, 16, v100
	v_and_b32_e32 v39, 0xffff0000, v100
	v_pk_fma_f32 v[36:37], v[34:35], v[36:37], v[38:39]
	v_mul_f32_e32 v35, 0xbfb8aa3b, v146
	v_exp_f32_e32 v35, v35
	v_mul_f32_e32 v38, 0xbfb8aa3b, v47
	v_exp_f32_e32 v39, v38
	v_add_f32_e32 v34, 1.0, v40
	v_add_f32_e32 v35, 1.0, v35
	v_rcp_f32_e32 v38, v35
	v_add_f32_e32 v35, 1.0, v39
	v_mul_f32_e32 v39, 0xbfb8aa3b, v144
	v_exp_f32_e32 v39, v39
	v_rcp_f32_e32 v34, v34
	v_rcp_f32_e32 v35, v35
	v_lshlrev_b32_e32 v40, 16, v109
	v_add_f32_e32 v39, 1.0, v39
	v_rcp_f32_e32 v39, v39
	v_and_b32_e32 v43, 0xffff0000, v105
	v_pk_fma_f32 v[34:35], v[34:35], v[40:41], v[42:43]
	v_mul_f32_e32 v42, 0xbfb8aa3b, v147
	v_lshlrev_b32_e32 v40, 16, v97
	v_and_b32_e32 v41, 0xffff0000, v97
	v_exp_f32_e32 v44, v42
	v_lshlrev_b32_e32 v42, 16, v101
	v_and_b32_e32 v43, 0xffff0000, v101
	v_pk_fma_f32 v[38:39], v[38:39], v[40:41], v[42:43]
	v_mul_f32_e32 v41, 0xbfb8aa3b, v148
	v_exp_f32_e32 v41, v41
	v_mul_f32_e32 v42, 0xbfb8aa3b, v149
	v_exp_f32_e32 v43, v42
	v_add_f32_e32 v40, 1.0, v44
	v_add_f32_e32 v41, 1.0, v41
	v_rcp_f32_e32 v42, v41
	v_add_f32_e32 v41, 1.0, v43
	v_mul_f32_e32 v43, 0xbfb8aa3b, v150
	v_exp_f32_e32 v43, v43
	v_rcp_f32_e32 v40, v40
	v_rcp_f32_e32 v41, v41
	v_lshlrev_b32_e32 v44, 16, v110
	v_add_f32_e32 v43, 1.0, v43
	v_rcp_f32_e32 v43, v43
	v_and_b32_e32 v45, 0xffff0000, v110
	v_lshlrev_b32_e32 v46, 16, v106
	v_and_b32_e32 v47, 0xffff0000, v106
	v_pk_fma_f32 v[40:41], v[40:41], v[44:45], v[46:47]
	v_mul_f32_e32 v46, 0xbfb8aa3b, v151
	v_lshlrev_b32_e32 v44, 16, v98
	v_and_b32_e32 v45, 0xffff0000, v98
	v_exp_f32_e32 v96, v46
	v_lshlrev_b32_e32 v46, 16, v102
	v_and_b32_e32 v47, 0xffff0000, v102
	v_pk_fma_f32 v[42:43], v[42:43], v[44:45], v[46:47]
	v_mul_f32_e32 v45, 0xbfb8aa3b, v152
	v_exp_f32_e32 v45, v45
	v_mul_f32_e32 v46, 0xbfb8aa3b, v153
	v_exp_f32_e32 v47, v46
	v_add_f32_e32 v44, 1.0, v96
	v_add_f32_e32 v45, 1.0, v45
	v_rcp_f32_e32 v46, v45
	v_add_f32_e32 v45, 1.0, v47
	v_mul_f32_e32 v47, 0xbfb8aa3b, v154
	v_exp_f32_e32 v47, v47
	v_rcp_f32_e32 v44, v44
	v_rcp_f32_e32 v45, v45
	v_lshlrev_b32_e32 v96, 16, v111
	v_add_f32_e32 v47, 1.0, v47
	v_rcp_f32_e32 v47, v47
	v_and_b32_e32 v97, 0xffff0000, v111
	v_lshlrev_b32_e32 v100, 16, v107
	v_and_b32_e32 v101, 0xffff0000, v107
	v_pk_fma_f32 v[44:45], v[44:45], v[96:97], v[100:101]
	v_lshlrev_b32_e32 v96, 16, v99
	v_and_b32_e32 v97, 0xffff0000, v99
	v_lshlrev_b32_e32 v98, 16, v103
	v_and_b32_e32 v99, 0xffff0000, v103
	v_pk_fma_f32 v[46:47], v[46:47], v[96:97], v[98:99]
	v_add_u32_e32 v96, s62, v200
	v_ashrrev_i32_e32 v97, 31, v96
	v_lshlrev_b64 v[96:97], 12, v[96:97]
	v_lshl_add_u64 v[96:97], v[184:185], 0, v[96:97]
	v_cvt_pk_bf16_f32 v32, v32, v33
	v_cvt_pk_bf16_f32 v33, v34, v35
	v_cvt_pk_bf16_f32 v34, v40, v41
	v_cvt_pk_bf16_f32 v35, v44, v45
	global_store_dwordx4 v[96:97], v[32:35], off
	s_nop 1
	v_cvt_pk_bf16_f32 v32, v36, v37
	v_add_co_u32_e32 v36, vcc, 0x8000, v96
	v_cvt_pk_bf16_f32 v33, v38, v39
	v_cvt_pk_bf16_f32 v34, v42, v43
	v_cvt_pk_bf16_f32 v35, v46, v47
	v_addc_co_u32_e32 v37, vcc, 0, v97, vcc
	global_store_dwordx4 v[36:37], v[32:35], off
; template <class Epi, class Sched, bool GATHER, bool ALIGN_EPI = true, bool SP2 = true, bool REMAP64 = false>
; __device__ __forceinline__ void gemm_phase(LAS unsigned char* lds, const bf16* Ag, const bf16* Btg, const int K, const Sched& S, const Epi& E) {
;     ...
;             constexpr bool RP = REMAP64 && Epi::ROWPAIR;
;             const bool hi = RP && (fr >= 8); const int rsh = hi ? -8 : 0, citx = hi ? cit + 32 : cit;
;             typename Epi::Pre pq[2];
;             { const int r0_ = wr * 64 + fr; pq[0] = E.pre(cur, (r0_ < cur.nrows ? r0_ : cur.nrows - 1) + rsh, citx); }
; #pragma unroll
;             for (int gq = 0; gq < 8; ++gq) { const int ai = gq >> 2, m = gq & 3, r = ai * HALF + wr * 64 + m * 16 + fr;
;                 if (gq + 1 < 8) { const int rn = ((gq + 1) >> 2) * HALF + wr * 64 + ((gq + 1) & 3) * 16 + fr; pq[(gq + 1) & 1] = E.pre(cur, (rn < cur.nrows ? rn : cur.nrows - 1) + rsh, citx); }
;                 __builtin_amdgcn_sched_barrier(0);
;                 if (r < cur.nrows) { float v0[8], v1[8];
; #pragma unroll
;                     for (int i = 0; i < 4; ++i) { v0[i] = acc[ai][0][m][0][i]; v0[4 + i] = acc[ai][0][m][1][i]; v1[i] = acc[ai][1][m][0][i]; v1[4 + i] = acc[ai][1][m][1][i]; }
;                     if constexpr (RP) {
; #pragma unroll
;                         for (int i = 0; i < 8; ++i) { const float snd = hi ? v0[i] : v1[i];
;                             const float rcv = __builtin_bit_cast(float, __builtin_amdgcn_update_dpp(0, __builtin_bit_cast(int, snd), 0x128, 0xf, 0xf, false));
;                             if (hi) v0[i] = rcv; else v1[i] = rcv; } }
;                     E.post(cur, r + rsh, citx, v0, v1, pq[gq & 1]); }
;                 __builtin_amdgcn_sched_barrier(0); }
;     __device__ __forceinline__ Pre pre(const Unit& u, int r, int cit) const { const size_t off = (size_t)(u.arow0 + r) * D + u.pn * 256 + cit;
;         return Pre{__builtin_nontemporal_load((const v4u*)(pp + off)), __builtin_nontemporal_load((const v4u*)(pp + off + (size_t)8 * D)), *(const v4u*)(h + off), *(const v4u*)(h + off + (size_t)8 * D)}; }
;     __device__ __forceinline__ void post(const Unit& u, int r, int cit, const float* v0, const float* v1, const Pre& p) const {
.LBB0_1748:
	s_and_b64 vcc, exec, s[8:9]
	s_cbranch_vccnz .LBB0_1750
	s_waitcnt vmcnt(10)
	s_nop 0
	v_cndmask_b32_e64 v128, v20, v28, s[0:1]
	v_mov_b32_e32 v129, 0
	s_nop 1
	v_mov_b32_dpp v129, v128 row_ror:8 row_mask:0xf bank_mask:0xf
	v_cndmask_b32_e64 v128, v21, v29, s[0:1]
	v_cndmask_b32_e64 v28, v28, v129, s[0:1]
	v_cndmask_b32_e64 v20, v129, v20, s[0:1]
	v_mov_b32_e32 v129, 0
	s_nop 1
	v_mov_b32_dpp v129, v128 row_ror:8 row_mask:0xf bank_mask:0xf
	v_cndmask_b32_e64 v128, v22, v30, s[0:1]
	v_cndmask_b32_e64 v29, v29, v129, s[0:1]
	v_cndmask_b32_e64 v129, v129, v21, s[0:1]
	v_mov_b32_e32 v21, 0
	s_nop 1
	v_mov_b32_dpp v21, v128 row_ror:8 row_mask:0xf bank_mask:0xf
	v_cndmask_b32_e64 v128, v23, v31, s[0:1]
	v_cndmask_b32_e64 v30, v30, v21, s[0:1]
	v_cndmask_b32_e64 v130, v21, v22, s[0:1]
	v_mov_b32_e32 v21, 0
	v_cndmask_b32_e64 v22, v16, v24, s[0:1]
	s_nop 0
	v_mov_b32_dpp v21, v128 row_ror:8 row_mask:0xf bank_mask:0xf
	v_cndmask_b32_e64 v31, v31, v21, s[0:1]
	v_cndmask_b32_e64 v128, v21, v23, s[0:1]
	v_mov_b32_e32 v21, 0
	s_nop 0
	v_and_b32_e32 v23, 0xffff0000, v88
	v_mov_b32_dpp v21, v22 row_ror:8 row_mask:0xf bank_mask:0xf
	v_cndmask_b32_e64 v22, v17, v25, s[0:1]
	v_cndmask_b32_e64 v132, v21, v16, s[0:1]
	v_mov_b32_e32 v16, 0
	v_cndmask_b32_e64 v131, v24, v21, s[0:1]
	v_cndmask_b32_e64 v21, v18, v26, s[0:1]
	v_mov_b32_dpp v16, v22 row_ror:8 row_mask:0xf bank_mask:0xf
	v_cndmask_b32_e64 v133, v25, v16, s[0:1]
	v_cndmask_b32_e64 v134, v16, v17, s[0:1]
	v_mov_b32_e32 v16, 0
	v_cndmask_b32_e64 v17, v19, v27, s[0:1]
	v_lshlrev_b32_e32 v22, 16, v88
	v_mov_b32_dpp v16, v21 row_ror:8 row_mask:0xf bank_mask:0xf
	v_cndmask_b32_e64 v136, v16, v18, s[0:1]
	v_mul_f32_e32 v18, 0xbfb8aa3b, v28
	v_exp_f32_e32 v18, v18
	v_cndmask_b32_e64 v135, v26, v16, s[0:1]
	v_mov_b32_e32 v16, 0
	v_and_b32_e32 v21, 0xffff0000, v92
	v_and_b32_e32 v25, 0xffff0000, v93
	v_mov_b32_dpp v16, v17 row_ror:8 row_mask:0xf bank_mask:0xf
	v_mul_f32_e32 v17, 0xbfb8aa3b, v20
	v_cndmask_b32_e64 v137, v27, v16, s[0:1]
	v_cndmask_b32_e64 v138, v16, v19, s[0:1]
	v_add_f32_e32 v16, 1.0, v18
	v_exp_f32_e32 v17, v17
	v_mul_f32_e32 v18, 0xbfb8aa3b, v29
	v_exp_f32_e32 v19, v18
	v_rcp_f32_e32 v16, v16
	v_add_f32_e32 v17, 1.0, v17
	v_rcp_f32_e32 v18, v17
	v_add_f32_e32 v17, 1.0, v19
	v_mul_f32_e32 v19, 0xbfb8aa3b, v129
	v_exp_f32_e32 v19, v19
	v_rcp_f32_e32 v17, v17
	v_lshlrev_b32_e32 v20, 16, v92
	v_lshlrev_b32_e32 v26, 16, v89
	v_add_f32_e32 v19, 1.0, v19
	v_rcp_f32_e32 v19, v19
	v_pk_fma_f32 v[16:17], v[16:17], v[20:21], v[22:23]
	v_mul_f32_e32 v22, 0xbfb8aa3b, v30
	v_lshlrev_b32_e32 v20, 16, v80
	v_and_b32_e32 v21, 0xffff0000, v80
	v_exp_f32_e32 v24, v22
	s_nop 0
	v_lshlrev_b32_e32 v22, 16, v84
	v_and_b32_e32 v23, 0xffff0000, v84
	v_pk_fma_f32 v[20:21], v[18:19], v[20:21], v[22:23]
	v_mul_f32_e32 v19, 0xbfb8aa3b, v130
	v_exp_f32_e32 v19, v19
	v_mul_f32_e32 v22, 0xbfb8aa3b, v31
	v_exp_f32_e32 v23, v22
	v_add_f32_e32 v18, 1.0, v24
	v_add_f32_e32 v19, 1.0, v19
	v_rcp_f32_e32 v22, v19
	v_add_f32_e32 v19, 1.0, v23
	v_mul_f32_e32 v23, 0xbfb8aa3b, v128
	v_exp_f32_e32 v23, v23
	v_rcp_f32_e32 v18, v18
	v_rcp_f32_e32 v19, v19
	v_lshlrev_b32_e32 v24, 16, v93
	v_add_f32_e32 v23, 1.0, v23
	v_rcp_f32_e32 v23, v23
	v_and_b32_e32 v27, 0xffff0000, v89
	v_pk_fma_f32 v[18:19], v[18:19], v[24:25], v[26:27]
	v_mul_f32_e32 v26, 0xbfb8aa3b, v131
	v_lshlrev_b32_e32 v24, 16, v81
	v_and_b32_e32 v25, 0xffff0000, v81
	v_exp_f32_e32 v28, v26
	v_lshlrev_b32_e32 v26, 16, v85
	v_and_b32_e32 v27, 0xffff0000, v85
	v_pk_fma_f32 v[22:23], v[22:23], v[24:25], v[26:27]
	v_mul_f32_e32 v25, 0xbfb8aa3b, v132
	v_exp_f32_e32 v25, v25
	v_mul_f32_e32 v26, 0xbfb8aa3b, v133
	v_exp_f32_e32 v27, v26
	v_add_f32_e32 v24, 1.0, v28
	v_add_f32_e32 v25, 1.0, v25
	v_rcp_f32_e32 v26, v25
	v_add_f32_e32 v25, 1.0, v27
	v_mul_f32_e32 v27, 0xbfb8aa3b, v134
	v_exp_f32_e32 v27, v27
	v_rcp_f32_e32 v24, v24
	v_rcp_f32_e32 v25, v25
	v_lshlrev_b32_e32 v28, 16, v94
	v_add_f32_e32 v27, 1.0, v27
	v_rcp_f32_e32 v27, v27
	v_and_b32_e32 v29, 0xffff0000, v94
	v_lshlrev_b32_e32 v30, 16, v90
	v_and_b32_e32 v31, 0xffff0000, v90
	v_pk_fma_f32 v[24:25], v[24:25], v[28:29], v[30:31]
	v_mul_f32_e32 v30, 0xbfb8aa3b, v135
	v_lshlrev_b32_e32 v28, 16, v82
	v_and_b32_e32 v29, 0xffff0000, v82
	v_exp_f32_e32 v80, v30
	v_lshlrev_b32_e32 v30, 16, v86
	v_and_b32_e32 v31, 0xffff0000, v86
	v_pk_fma_f32 v[26:27], v[26:27], v[28:29], v[30:31]
	v_mul_f32_e32 v29, 0xbfb8aa3b, v136
	v_exp_f32_e32 v29, v29
	v_mul_f32_e32 v30, 0xbfb8aa3b, v137
	v_exp_f32_e32 v31, v30
	v_add_f32_e32 v28, 1.0, v80
	v_add_f32_e32 v29, 1.0, v29
	v_rcp_f32_e32 v30, v29
	v_add_f32_e32 v29, 1.0, v31
	v_mul_f32_e32 v31, 0xbfb8aa3b, v138
	v_exp_f32_e32 v31, v31
	v_rcp_f32_e32 v28, v28
	v_rcp_f32_e32 v29, v29
	v_lshlrev_b32_e32 v80, 16, v95
	v_add_f32_e32 v31, 1.0, v31
	v_rcp_f32_e32 v31, v31
	v_and_b32_e32 v81, 0xffff0000, v95
	v_lshlrev_b32_e32 v84, 16, v91
	v_and_b32_e32 v85, 0xffff0000, v91
	v_pk_fma_f32 v[28:29], v[28:29], v[80:81], v[84:85]
	v_lshlrev_b32_e32 v80, 16, v83
	v_and_b32_e32 v81, 0xffff0000, v83
	v_lshlrev_b32_e32 v82, 16, v87
	v_and_b32_e32 v83, 0xffff0000, v87
	v_pk_fma_f32 v[30:31], v[30:31], v[80:81], v[82:83]
	v_add_u32_e32 v80, s63, v200
	v_ashrrev_i32_e32 v81, 31, v80
	v_lshlrev_b64 v[80:81], 12, v[80:81]
	v_lshl_add_u64 v[80:81], v[184:185], 0, v[80:81]
	v_cvt_pk_bf16_f32 v16, v16, v17
	v_cvt_pk_bf16_f32 v17, v18, v19
	v_cvt_pk_bf16_f32 v18, v24, v25
	v_cvt_pk_bf16_f32 v19, v28, v29
	global_store_dwordx4 v[80:81], v[16:19], off
	s_nop 1
	v_cvt_pk_bf16_f32 v16, v20, v21
	v_add_co_u32_e32 v20, vcc, 0x8000, v80
	v_cvt_pk_bf16_f32 v17, v22, v23
	v_cvt_pk_bf16_f32 v18, v26, v27
	v_cvt_pk_bf16_f32 v19, v30, v31
	v_addc_co_u32_e32 v21, vcc, 0, v81, vcc
	global_store_dwordx4 v[20:21], v[16:19], off
; template <class Epi, class Sched, bool GATHER, bool ALIGN_EPI = true, bool SP2 = true, bool REMAP64 = false>
; __device__ __forceinline__ void gemm_phase(LAS unsigned char* lds, const bf16* Ag, const bf16* Btg, const int K, const Sched& S, const Epi& E) {
;     ...
;             constexpr bool RP = REMAP64 && Epi::ROWPAIR;
;             const bool hi = RP && (fr >= 8); const int rsh = hi ? -8 : 0, citx = hi ? cit + 32 : cit;
;             typename Epi::Pre pq[2];
;             { const int r0_ = wr * 64 + fr; pq[0] = E.pre(cur, (r0_ < cur.nrows ? r0_ : cur.nrows - 1) + rsh, citx); }
; #pragma unroll
;             for (int gq = 0; gq < 8; ++gq) { const int ai = gq >> 2, m = gq & 3, r = ai * HALF + wr * 64 + m * 16 + fr;
;                 if (gq + 1 < 8) { const int rn = ((gq + 1) >> 2) * HALF + wr * 64 + ((gq + 1) & 3) * 16 + fr; pq[(gq + 1) & 1] = E.pre(cur, (rn < cur.nrows ? rn : cur.nrows - 1) + rsh, citx); }
;                 __builtin_amdgcn_sched_barrier(0);
;                 if (r < cur.nrows) { float v0[8], v1[8];
; #pragma unroll
;                     for (int i = 0; i < 4; ++i) { v0[i] = acc[ai][0][m][0][i]; v0[4 + i] = acc[ai][0][m][1][i]; v1[i] = acc[ai][1][m][0][i]; v1[4 + i] = acc[ai][1][m][1][i]; }
;                     if constexpr (RP) {
; #pragma unroll
;                         for (int i = 0; i < 8; ++i) { const float snd = hi ? v0[i] : v1[i];
;                             const float rcv = __builtin_bit_cast(float, __builtin_amdgcn_update_dpp(0, __builtin_bit_cast(int, snd), 0x128, 0xf, 0xf, false));
;                             if (hi) v0[i] = rcv; else v1[i] = rcv; } }
;                     E.post(cur, r + rsh, citx, v0, v1, pq[gq & 1]); }
;                 __builtin_amdgcn_sched_barrier(0); }
;     __device__ __forceinline__ Pre pre(const Unit& u, int r, int cit) const { const size_t off = (size_t)(u.arow0 + r) * D + u.pn * 256 + cit;
;         return Pre{__builtin_nontemporal_load((const v4u*)(pp + off)), __builtin_nontemporal_load((const v4u*)(pp + off + (size_t)8 * D)), *(const v4u*)(h + off), *(const v4u*)(h + off + (size_t)8 * D)}; }
;     __device__ __forceinline__ void post(const Unit& u, int r, int cit, const float* v0, const float* v1, const Pre& p) const {
.LBB0_1750:
	s_and_b64 vcc, exec, s[8:9]
	s_cbranch_vccnz .LBB0_1752
	s_waitcnt vmcnt(6)
	v_cndmask_b32_e64 v16, v4, v12, s[0:1]
	v_mov_b32_e32 v17, 0
	s_nop 1
	v_mov_b32_dpp v17, v16 row_ror:8 row_mask:0xf bank_mask:0xf
	v_cndmask_b32_e64 v16, v5, v13, s[0:1]
	v_cndmask_b32_e64 v12, v12, v17, s[0:1]
	v_cndmask_b32_e64 v4, v17, v4, s[0:1]
	v_mov_b32_e32 v17, 0
	s_nop 1
	v_mov_b32_dpp v17, v16 row_ror:8 row_mask:0xf bank_mask:0xf
	v_cndmask_b32_e64 v16, v6, v14, s[0:1]
	v_cndmask_b32_e64 v13, v13, v17, s[0:1]
	v_cndmask_b32_e64 v17, v17, v5, s[0:1]
	v_mov_b32_e32 v5, 0
	s_nop 1
	v_mov_b32_dpp v5, v16 row_ror:8 row_mask:0xf bank_mask:0xf
	v_cndmask_b32_e64 v16, v7, v15, s[0:1]
	v_cndmask_b32_e64 v14, v14, v5, s[0:1]
	v_cndmask_b32_e64 v18, v5, v6, s[0:1]
	v_mov_b32_e32 v5, 0
	v_cndmask_b32_e64 v6, v0, v8, s[0:1]
	s_nop 0
	v_mov_b32_dpp v5, v16 row_ror:8 row_mask:0xf bank_mask:0xf
	v_cndmask_b32_e64 v15, v15, v5, s[0:1]
	v_cndmask_b32_e64 v16, v5, v7, s[0:1]
	v_mov_b32_e32 v5, 0
	s_nop 0
	v_and_b32_e32 v7, 0xffff0000, v72
	v_mov_b32_dpp v5, v6 row_ror:8 row_mask:0xf bank_mask:0xf
	v_cndmask_b32_e64 v6, v1, v9, s[0:1]
	v_cndmask_b32_e64 v20, v5, v0, s[0:1]
	v_mov_b32_e32 v0, 0
	v_cndmask_b32_e64 v19, v8, v5, s[0:1]
	v_cndmask_b32_e64 v5, v2, v10, s[0:1]
	v_mov_b32_dpp v0, v6 row_ror:8 row_mask:0xf bank_mask:0xf
	v_cndmask_b32_e64 v21, v9, v0, s[0:1]
	v_cndmask_b32_e64 v22, v0, v1, s[0:1]
	v_mov_b32_e32 v0, 0
	v_cndmask_b32_e64 v1, v3, v11, s[0:1]
	v_lshlrev_b32_e32 v6, 16, v72
	v_mov_b32_dpp v0, v5 row_ror:8 row_mask:0xf bank_mask:0xf
	v_cndmask_b32_e64 v24, v0, v2, s[0:1]
	v_mul_f32_e32 v2, 0xbfb8aa3b, v12
	v_exp_f32_e32 v2, v2
	v_cndmask_b32_e64 v23, v10, v0, s[0:1]
	v_mov_b32_e32 v0, 0
	v_and_b32_e32 v5, 0xffff0000, v76
	v_and_b32_e32 v9, 0xffff0000, v77
	v_mov_b32_dpp v0, v1 row_ror:8 row_mask:0xf bank_mask:0xf
	v_mul_f32_e32 v1, 0xbfb8aa3b, v4
	v_cndmask_b32_e64 v25, v11, v0, s[0:1]
	v_cndmask_b32_e64 v26, v0, v3, s[0:1]
	v_add_f32_e32 v0, 1.0, v2
	v_exp_f32_e32 v1, v1
	v_mul_f32_e32 v2, 0xbfb8aa3b, v13
	v_exp_f32_e32 v3, v2
	v_rcp_f32_e32 v0, v0
	v_add_f32_e32 v1, 1.0, v1
	v_rcp_f32_e32 v2, v1
	v_add_f32_e32 v1, 1.0, v3
	v_mul_f32_e32 v3, 0xbfb8aa3b, v17
	v_exp_f32_e32 v3, v3
	v_rcp_f32_e32 v1, v1
	v_lshlrev_b32_e32 v4, 16, v76
	v_lshlrev_b32_e32 v10, 16, v73
	v_add_f32_e32 v3, 1.0, v3
	v_rcp_f32_e32 v3, v3
	v_pk_fma_f32 v[0:1], v[0:1], v[4:5], v[6:7]
	v_mul_f32_e32 v6, 0xbfb8aa3b, v14
	v_lshlrev_b32_e32 v4, 16, v64
	v_and_b32_e32 v5, 0xffff0000, v64
	v_exp_f32_e32 v8, v6
	s_nop 0
	v_lshlrev_b32_e32 v6, 16, v68
	v_and_b32_e32 v7, 0xffff0000, v68
	v_pk_fma_f32 v[4:5], v[2:3], v[4:5], v[6:7]
	v_mul_f32_e32 v3, 0xbfb8aa3b, v18
	v_exp_f32_e32 v3, v3
	v_mul_f32_e32 v6, 0xbfb8aa3b, v15
	v_exp_f32_e32 v7, v6
	v_add_f32_e32 v2, 1.0, v8
	v_add_f32_e32 v3, 1.0, v3
	v_rcp_f32_e32 v6, v3
	v_add_f32_e32 v3, 1.0, v7
	v_mul_f32_e32 v7, 0xbfb8aa3b, v16
	v_exp_f32_e32 v7, v7
	v_rcp_f32_e32 v2, v2
	v_rcp_f32_e32 v3, v3
	v_lshlrev_b32_e32 v8, 16, v77
	v_add_f32_e32 v7, 1.0, v7
	v_rcp_f32_e32 v7, v7
	v_and_b32_e32 v11, 0xffff0000, v73
	v_pk_fma_f32 v[2:3], v[2:3], v[8:9], v[10:11]
	v_mul_f32_e32 v10, 0xbfb8aa3b, v19
	v_lshlrev_b32_e32 v8, 16, v65
	v_and_b32_e32 v9, 0xffff0000, v65
	v_exp_f32_e32 v12, v10
	v_lshlrev_b32_e32 v10, 16, v69
	v_and_b32_e32 v11, 0xffff0000, v69
	v_pk_fma_f32 v[6:7], v[6:7], v[8:9], v[10:11]
	v_mul_f32_e32 v9, 0xbfb8aa3b, v20
	v_exp_f32_e32 v9, v9
	v_mul_f32_e32 v10, 0xbfb8aa3b, v21
	v_exp_f32_e32 v11, v10
	v_add_f32_e32 v8, 1.0, v12
	v_add_f32_e32 v9, 1.0, v9
	v_rcp_f32_e32 v10, v9
	v_add_f32_e32 v9, 1.0, v11
	v_mul_f32_e32 v11, 0xbfb8aa3b, v22
	v_exp_f32_e32 v11, v11
	v_rcp_f32_e32 v8, v8
	v_rcp_f32_e32 v9, v9
	v_lshlrev_b32_e32 v12, 16, v78
	v_add_f32_e32 v11, 1.0, v11
	v_rcp_f32_e32 v11, v11
	v_and_b32_e32 v13, 0xffff0000, v78
	v_lshlrev_b32_e32 v14, 16, v74
	v_and_b32_e32 v15, 0xffff0000, v74
	v_pk_fma_f32 v[8:9], v[8:9], v[12:13], v[14:15]
	v_mul_f32_e32 v14, 0xbfb8aa3b, v23
	v_lshlrev_b32_e32 v12, 16, v66
	v_and_b32_e32 v13, 0xffff0000, v66
	v_exp_f32_e32 v16, v14
	v_lshlrev_b32_e32 v14, 16, v70
	v_and_b32_e32 v15, 0xffff0000, v70
	v_pk_fma_f32 v[10:11], v[10:11], v[12:13], v[14:15]
	v_mul_f32_e32 v13, 0xbfb8aa3b, v24
	v_exp_f32_e32 v13, v13
	v_mul_f32_e32 v14, 0xbfb8aa3b, v25
	v_exp_f32_e32 v15, v14
	v_add_f32_e32 v12, 1.0, v16
	v_add_f32_e32 v13, 1.0, v13
	v_rcp_f32_e32 v14, v13
	v_add_f32_e32 v13, 1.0, v15
	v_mul_f32_e32 v15, 0xbfb8aa3b, v26
	v_exp_f32_e32 v15, v15
	v_rcp_f32_e32 v12, v12
	v_rcp_f32_e32 v13, v13
	v_lshlrev_b32_e32 v16, 16, v79
	v_add_f32_e32 v15, 1.0, v15
	v_rcp_f32_e32 v15, v15
	v_and_b32_e32 v17, 0xffff0000, v79
	v_lshlrev_b32_e32 v18, 16, v75
	v_and_b32_e32 v19, 0xffff0000, v75
	v_pk_fma_f32 v[12:13], v[12:13], v[16:17], v[18:19]
	v_lshlrev_b32_e32 v16, 16, v67
	v_and_b32_e32 v17, 0xffff0000, v67
	v_lshlrev_b32_e32 v18, 16, v71
	v_and_b32_e32 v19, 0xffff0000, v71
	v_pk_fma_f32 v[14:15], v[14:15], v[16:17], v[18:19]
	v_add_u32_e32 v16, s64, v200
	v_ashrrev_i32_e32 v17, 31, v16
	v_lshlrev_b64 v[16:17], 12, v[16:17]
	v_lshl_add_u64 v[16:17], v[184:185], 0, v[16:17]
	v_cvt_pk_bf16_f32 v0, v0, v1
	v_cvt_pk_bf16_f32 v1, v2, v3
	v_cvt_pk_bf16_f32 v2, v8, v9
	v_cvt_pk_bf16_f32 v3, v12, v13
	global_store_dwordx4 v[16:17], v[0:3], off
	s_nop 1
	v_cvt_pk_bf16_f32 v0, v4, v5
	v_add_co_u32_e32 v4, vcc, 0x8000, v16
	v_cvt_pk_bf16_f32 v1, v6, v7
	v_cvt_pk_bf16_f32 v2, v10, v11
	v_cvt_pk_bf16_f32 v3, v14, v15
	v_addc_co_u32_e32 v5, vcc, 0, v17, vcc
	global_store_dwordx4 v[4:5], v[0:3], off
